# speedup vs baseline: 1.0072x; 1.0061x over previous
_Z4k_k2ILb0EEvPKDF16_S1_PKfS3_S3_S1_S1_PfS3_S3_S1_PDF16_PKiS4_S4_:
	s_load_dwordx2 s[24:25], s[0:1], 0x58
	s_load_dwordx8 s[4:11], s[0:1], 0x38
	s_load_dwordx4 s[20:23], s[0:1], 0x0
	s_load_dwordx8 s[12:19], s[0:1], 0x18
	s_load_dwordx2 s[54:55], s[0:1], 0x10
	s_lshl_b32 s3, s2, 5
	s_and_b32 s3, s3, 0xe0
	s_lshr_b32 s26, s2, 3
	s_or_b32 s3, s3, s26
	s_movk_i32 s26, 0x100
	s_lshl_b32 s28, s3, 5
	v_cmp_gt_u32_e32 vcc, s26, v0
	v_mov_b32_e32 v67, 0
	v_lshlrev_b32_e32 v66, 4, v0
	s_lshl_b32 s0, s3, 1
	s_and_b32 s26, s0, 0xffffffe
	s_mov_b32 s27, 0
	s_waitcnt lgkmcnt(0)
	v_lshl_add_u64 v[2:3], s[16:17], 0, v[66:67]
	s_lshl_b64 s[0:1], s[26:27], 13
	s_or_b32 s26, s26, 1
	v_lshl_add_u64 v[4:5], v[2:3], 0, s[0:1]
	s_lshl_b64 s[0:1], s[26:27], 13
	v_lshl_add_u64 v[2:3], v[2:3], 0, s[0:1]
	global_load_dwordx4 v[68:71], v[4:5], off
	global_load_dwordx4 v[72:75], v[2:3], off
	v_lshl_add_u64 v[2:3], s[12:13], 0, v[66:67]
	s_movk_i32 s29, 0x2000
	v_add_co_u32_e32 v4, vcc, s29, v2
	s_movk_i32 s52, 0x4000
	s_nop 0
	v_addc_co_u32_e32 v5, vcc, 0, v3, vcc
	v_add_co_u32_e32 v18, vcc, s52, v2
	s_movk_i32 s33, 0x6000
	s_nop 0
	v_addc_co_u32_e32 v19, vcc, 0, v3, vcc
	s_lshl_b32 s26, s3, 2
	global_load_dwordx4 v[14:17], v66, s[12:13]
	global_load_dwordx4 v[10:13], v[4:5], off
	global_load_dwordx4 v[6:9], v[18:19], off
	v_add_co_u32_e32 v18, vcc, s33, v2
	s_add_u32 s0, s24, 0x800000
	s_nop 0
	v_addc_co_u32_e32 v19, vcc, 0, v3, vcc
	s_addc_u32 s1, s25, 0
	s_lshl_b64 s[12:13], s[26:27], 13
	v_lshlrev_b32_e32 v20, 2, v0
	global_load_dwordx4 v[2:5], v[18:19], off
	global_load_dword v1, v20, s[14:15]
	v_or_b32_e32 v18, s12, v66
	v_mov_b32_e32 v19, s13
	s_or_b32 s12, s26, 1
	s_mov_b32 s13, s27
	s_lshl_b64 s[12:13], s[12:13], 13
	v_lshl_add_u64 v[76:77], s[22:23], 0, v[18:19]
	v_lshl_add_u64 v[78:79], s[20:21], 0, v[18:19]
	v_lshl_add_u64 v[80:81], s[0:1], 0, v[18:19]
	v_or_b32_e32 v18, s12, v66
	v_mov_b32_e32 v19, s13
	s_or_b32 s12, s26, 2
	s_mov_b32 s13, s27
	s_lshl_b64 s[12:13], s[12:13], 13
	s_or_b32 s26, s26, 3
	v_lshl_add_u64 v[82:83], s[22:23], 0, v[18:19]
	v_lshl_add_u64 v[84:85], s[20:21], 0, v[18:19]
	v_lshl_add_u64 v[86:87], s[0:1], 0, v[18:19]
	v_or_b32_e32 v18, s12, v66
	v_mov_b32_e32 v19, s13
	s_lshl_b64 s[12:13], s[26:27], 13
	v_lshl_add_u64 v[88:89], s[22:23], 0, v[18:19]
	v_lshl_add_u64 v[90:91], s[20:21], 0, v[18:19]
	v_lshl_add_u64 v[92:93], s[0:1], 0, v[18:19]
	v_or_b32_e32 v18, s12, v66
	v_mov_b32_e32 v19, s13
	v_lshl_add_u64 v[94:95], s[22:23], 0, v[18:19]
	v_lshl_add_u64 v[96:97], s[20:21], 0, v[18:19]
	v_lshl_add_u64 v[98:99], s[0:1], 0, v[18:19]
	global_load_dwordx4 v[62:65], v[76:77], off
	global_load_dwordx4 v[54:57], v[78:79], off
	global_load_dwordx4 v[58:61], v[80:81], off
	v_mov_b64_e32 v[212:213], v[82:83]
	v_mov_b64_e32 v[214:215], v[84:85]
	v_mov_b64_e32 v[216:217], v[86:87]
	v_mov_b64_e32 v[218:219], v[88:89]
	v_mov_b64_e32 v[220:221], v[90:91]
	v_mov_b64_e32 v[222:223], v[92:93]
	v_mov_b64_e32 v[224:225], v[94:95]
	v_mov_b64_e32 v[226:227], v[96:97]
	v_mov_b64_e32 v[228:229], v[98:99]
	s_lshl_b32 s30, s28, 7
	s_add_u32 s54, s54, s30
	s_addc_u32 s55, s55, 0
	s_load_dwordx16 s[36:51], s[54:55], 0x0
	s_load_dwordx16 s[72:87], s[54:55], 0x40
	s_load_dwordx16 s[56:71], s[54:55], 0x80
	s_load_dwordx8 s[88:95], s[54:55], 0xc0
	s_load_dwordx4 s[96:99], s[54:55], 0xe0
	s_load_dwordx4 s[20:23], s[54:55], 0xf0
	v_lshrrev_b32_e32 v196, 6, v0
	s_nop 1
	v_readfirstlane_b32 s16, v196
	s_nop 3
	s_lshl_b32 s16, s16, 9
	s_add_u32 s16, s54, s16
	s_addc_u32 s17, s55, 0
	s_load_dword s30, s[16:17], 0x0
	s_load_dword s30, s[16:17], 0x40
	s_load_dword s30, s[16:17], 0x80
	s_load_dword s30, s[16:17], 0xc0
	s_load_dword s30, s[16:17], 0x100
	s_load_dword s30, s[16:17], 0x140
	s_load_dword s30, s[16:17], 0x180
	s_load_dword s30, s[16:17], 0x1c0
	s_waitcnt vmcnt(9)
	v_cvt_f32_f16_e32 v134, v68
	v_cvt_f32_f16_sdwa v135, v68 dst_sel:DWORD dst_unused:UNUSED_PAD src0_sel:WORD_1
	v_cvt_f32_f16_e32 v136, v69
	v_cvt_f32_f16_sdwa v137, v69 dst_sel:DWORD dst_unused:UNUSED_PAD src0_sel:WORD_1
	v_cvt_f32_f16_e32 v138, v70
	v_cvt_f32_f16_sdwa v139, v70 dst_sel:DWORD dst_unused:UNUSED_PAD src0_sel:WORD_1
	v_cvt_f32_f16_e32 v140, v71
	v_cvt_f32_f16_sdwa v141, v71 dst_sel:DWORD dst_unused:UNUSED_PAD src0_sel:WORD_1
	s_waitcnt vmcnt(8)
	v_cvt_f32_f16_e32 v142, v72
	v_cvt_f32_f16_sdwa v143, v72 dst_sel:DWORD dst_unused:UNUSED_PAD src0_sel:WORD_1
	v_cvt_f32_f16_e32 v144, v73
	v_cvt_f32_f16_sdwa v145, v73 dst_sel:DWORD dst_unused:UNUSED_PAD src0_sel:WORD_1
	v_cvt_f32_f16_e32 v146, v74
	v_cvt_f32_f16_sdwa v147, v74 dst_sel:DWORD dst_unused:UNUSED_PAD src0_sel:WORD_1
	v_cvt_f32_f16_e32 v148, v75
	v_cvt_f32_f16_sdwa v149, v75 dst_sel:DWORD dst_unused:UNUSED_PAD src0_sel:WORD_1
	s_waitcnt lgkmcnt(0)
	v_lshlrev_b32_e32 v68, 1, v0
	s_waitcnt vmcnt(2)
	v_cvt_f32_f16_e32 v150, v62
	s_waitcnt vmcnt(1)
	v_pk_mul_f32 v[154:155], v[150:151], v[14:15] op_sel_hi:[0,1]
	v_exp_f32_e32 v154, v154
	v_exp_f32_e32 v155, v155
	v_pk_mul_f32 v[156:157], v[150:151], v[16:17] op_sel_hi:[0,1]
	v_exp_f32_e32 v156, v156
	v_exp_f32_e32 v157, v157
	v_fma_mix_f32 v152, v150, v54, 0 op_sel_hi:[0,1,0]
	v_pk_mul_f32 v[134:135], v[154:155], v[134:135]
	v_pk_fma_f32 v[134:135], v[152:153], s[36:37], v[134:135] op_sel_hi:[0, 1, 1]
	v_pk_fma_f32 v[70:71], s[72:73], v[134:135], 0 op_sel_hi:[1, 1, 0]
	v_pk_mul_f32 v[86:87], v[156:157], v[136:137]
	s_nop 0
	v_pk_fma_f32 v[136:137], v[152:153], s[38:39], v[86:87] op_sel_hi:[0, 1, 1]
	v_pk_mul_f32 v[72:73], v[150:151], v[10:11] op_sel_hi:[0,1]
	v_exp_f32_e32 v72, v72
	v_exp_f32_e32 v73, v73
	v_pk_mul_f32 v[86:87], v[150:151], v[12:13] op_sel_hi:[0,1]
	v_exp_f32_e32 v86, v86
	v_exp_f32_e32 v87, v87
	v_pk_mul_f32 v[72:73], v[72:73], v[138:139]
	v_pk_fma_f32 v[70:71], s[74:75], v[136:137], v[70:71]
	v_pk_fma_f32 v[138:139], v[152:153], s[40:41], v[72:73] op_sel_hi:[0, 1, 1]
	v_pk_mul_f32 v[72:73], v[86:87], v[140:141]
	v_pk_mul_f32 v[74:75], v[150:151], v[8:9] op_sel_hi:[0,1]
	v_pk_fma_f32 v[140:141], v[152:153], s[42:43], v[72:73] op_sel_hi:[0, 1, 1]
	v_pk_mul_f32 v[72:73], v[150:151], v[6:7] op_sel_hi:[0,1]
	v_exp_f32_e32 v72, v72
	v_exp_f32_e32 v73, v73
	v_exp_f32_e32 v74, v74
	v_exp_f32_e32 v75, v75
	v_pk_fma_f32 v[70:71], s[76:77], v[138:139], v[70:71]
	v_pk_mul_f32 v[72:73], v[72:73], v[142:143]
	v_pk_fma_f32 v[70:71], s[78:79], v[140:141], v[70:71]
	v_pk_fma_f32 v[142:143], v[152:153], s[44:45], v[72:73] op_sel_hi:[0, 1, 1]
	v_pk_mul_f32 v[72:73], v[74:75], v[144:145]
	v_pk_mul_f32 v[74:75], v[150:151], v[4:5] op_sel_hi:[0,1]
	v_pk_fma_f32 v[144:145], v[152:153], s[46:47], v[72:73] op_sel_hi:[0, 1, 1]
	v_pk_mul_f32 v[72:73], v[150:151], v[2:3] op_sel_hi:[0,1]
	v_exp_f32_e32 v72, v72
	v_exp_f32_e32 v73, v73
	v_exp_f32_e32 v74, v74
	v_exp_f32_e32 v75, v75
	v_pk_fma_f32 v[70:71], s[80:81], v[142:143], v[70:71]
	v_pk_mul_f32 v[72:73], v[72:73], v[146:147]
	v_pk_fma_f32 v[70:71], s[82:83], v[144:145], v[70:71]
	v_pk_fma_f32 v[146:147], v[152:153], s[48:49], v[72:73] op_sel_hi:[0, 1, 1]
	v_pk_mul_f32 v[72:73], v[74:75], v[148:149]
	v_pk_fma_f32 v[70:71], s[84:85], v[146:147], v[70:71]
	v_pk_fma_f32 v[148:149], v[152:153], s[50:51], v[72:73] op_sel_hi:[0, 1, 1]
	v_pk_fma_f32 v[70:71], s[86:87], v[148:149], v[70:71]
	s_nop 0
	v_add_f32_e32 v69, v70, v71
	v_fma_mix_f32 v69, v1, v54, v69 op_sel_hi:[0,1,0]
	s_waitcnt vmcnt(0)
	v_fma_mixlo_f16 v69, v69, v58, 0 op_sel_hi:[0,1,0]
	ds_write_b16 v68, v69 offset:4096
	global_load_dwordx4 v[50:53], v[212:213], off
	global_load_dwordx4 v[42:45], v[214:215], off
	global_load_dwordx4 v[46:49], v[216:217], off
	global_load_dwordx4 v[38:41], v[218:219], off
	global_load_dwordx4 v[30:33], v[220:221], off
	global_load_dwordx4 v[34:37], v[222:223], off
	global_load_dwordx4 v[26:29], v[224:225], off
	global_load_dwordx4 v[18:21], v[226:227], off
	global_load_dwordx4 v[22:25], v[228:229], off
	s_waitcnt lgkmcnt(0)
	s_load_dwordx16 s[36:51], s[54:55], 0x100
	s_load_dwordx16 s[72:87], s[54:55], 0x140
	v_cvt_f32_f16_sdwa v62, v62 dst_sel:DWORD dst_unused:UNUSED_PAD src0_sel:WORD_1
	v_pk_mul_f32 v[152:153], v[62:63], v[14:15] op_sel_hi:[0,1]
	v_exp_f32_e32 v152, v152
	v_exp_f32_e32 v153, v153
	v_pk_mul_f32 v[154:155], v[62:63], v[16:17] op_sel_hi:[0,1]
	v_exp_f32_e32 v154, v154
	v_exp_f32_e32 v155, v155
	v_fma_mix_f32 v150, v62, v54, 0 op_sel:[0,1,0] op_sel_hi:[0,1,0]
	v_pk_mul_f32 v[134:135], v[152:153], v[134:135]
	v_pk_fma_f32 v[134:135], v[150:151], s[56:57], v[134:135] op_sel_hi:[0, 1, 1]
	v_pk_fma_f32 v[102:103], s[88:89], v[134:135], 0 op_sel_hi:[1, 1, 0]
	v_pk_mul_f32 v[118:119], v[154:155], v[136:137]
	s_nop 0
	v_pk_fma_f32 v[136:137], v[150:151], s[58:59], v[118:119] op_sel_hi:[0, 1, 1]
	v_pk_mul_f32 v[104:105], v[62:63], v[10:11] op_sel_hi:[0,1]
	v_exp_f32_e32 v104, v104
	v_exp_f32_e32 v105, v105
	v_pk_mul_f32 v[118:119], v[62:63], v[12:13] op_sel_hi:[0,1]
	v_exp_f32_e32 v118, v118
	v_exp_f32_e32 v119, v119
	v_pk_mul_f32 v[104:105], v[104:105], v[138:139]
	v_pk_fma_f32 v[102:103], s[90:91], v[136:137], v[102:103]
	v_pk_fma_f32 v[138:139], v[150:151], s[60:61], v[104:105] op_sel_hi:[0, 1, 1]
	v_pk_mul_f32 v[104:105], v[118:119], v[140:141]
	v_pk_mul_f32 v[106:107], v[62:63], v[8:9] op_sel_hi:[0,1]
	v_pk_fma_f32 v[140:141], v[150:151], s[62:63], v[104:105] op_sel_hi:[0, 1, 1]
	v_pk_mul_f32 v[104:105], v[62:63], v[6:7] op_sel_hi:[0,1]
	v_exp_f32_e32 v104, v104
	v_exp_f32_e32 v105, v105
	v_exp_f32_e32 v106, v106
	v_exp_f32_e32 v107, v107
	v_pk_fma_f32 v[102:103], s[92:93], v[138:139], v[102:103]
	v_pk_mul_f32 v[104:105], v[104:105], v[142:143]
	v_pk_fma_f32 v[102:103], s[94:95], v[140:141], v[102:103]
	v_pk_fma_f32 v[142:143], v[150:151], s[64:65], v[104:105] op_sel_hi:[0, 1, 1]
	v_pk_mul_f32 v[104:105], v[106:107], v[144:145]
	v_pk_mul_f32 v[106:107], v[62:63], v[4:5] op_sel_hi:[0,1]
	v_pk_fma_f32 v[144:145], v[150:151], s[66:67], v[104:105] op_sel_hi:[0, 1, 1]
	v_pk_mul_f32 v[104:105], v[62:63], v[2:3] op_sel_hi:[0,1]
	v_exp_f32_e32 v104, v104
	v_exp_f32_e32 v105, v105
	v_exp_f32_e32 v106, v106
	v_exp_f32_e32 v107, v107
	v_pk_fma_f32 v[102:103], s[96:97], v[142:143], v[102:103]
	v_pk_mul_f32 v[104:105], v[104:105], v[146:147]
	v_pk_fma_f32 v[102:103], s[98:99], v[144:145], v[102:103]
	v_pk_fma_f32 v[146:147], v[150:151], s[68:69], v[104:105] op_sel_hi:[0, 1, 1]
	v_pk_mul_f32 v[104:105], v[106:107], v[148:149]
	v_pk_fma_f32 v[102:103], s[20:21], v[146:147], v[102:103]
	v_pk_fma_f32 v[148:149], v[150:151], s[70:71], v[104:105] op_sel_hi:[0, 1, 1]
	v_pk_fma_f32 v[102:103], s[22:23], v[148:149], v[102:103]
	s_waitcnt lgkmcnt(0)
	s_load_dwordx16 s[56:71], s[54:55], 0x180
	s_load_dwordx8 s[88:95], s[54:55], 0x1c0
	s_load_dwordx4 s[96:99], s[54:55], 0x1e0
	s_load_dwordx4 s[20:23], s[54:55], 0x1f0
	s_nop 0
	v_add_f32_e32 v62, v102, v103
	v_fma_mix_f32 v54, v1, v54, v62 op_sel:[0,1,0] op_sel_hi:[0,1,0]
	v_fma_mixlo_f16 v54, v54, v58, 0 op_sel:[0,1,0] op_sel_hi:[0,1,0]
	ds_write_b16 v68, v54 offset:5136
	v_cvt_f32_f16_e32 v54, v63
	v_pk_mul_f32 v[150:151], v[54:55], v[14:15] op_sel_hi:[0,1]
	v_exp_f32_e32 v150, v150
	v_exp_f32_e32 v151, v151
	v_pk_mul_f32 v[152:153], v[54:55], v[16:17] op_sel_hi:[0,1]
	v_exp_f32_e32 v152, v152
	v_exp_f32_e32 v153, v153
	v_fma_mix_f32 v58, v54, v55, 0 op_sel_hi:[0,1,0]
	v_pk_mul_f32 v[134:135], v[150:151], v[134:135]
	v_pk_fma_f32 v[134:135], v[58:59], s[36:37], v[134:135] op_sel_hi:[0, 1, 1]
	v_pk_fma_f32 v[70:71], s[72:73], v[134:135], 0 op_sel_hi:[1, 1, 0]
	v_pk_mul_f32 v[86:87], v[152:153], v[136:137]
	s_nop 0
	v_pk_fma_f32 v[136:137], v[58:59], s[38:39], v[86:87] op_sel_hi:[0, 1, 1]
	v_pk_mul_f32 v[72:73], v[54:55], v[10:11] op_sel_hi:[0,1]
	v_exp_f32_e32 v72, v72
	v_exp_f32_e32 v73, v73
	v_pk_mul_f32 v[86:87], v[54:55], v[12:13] op_sel_hi:[0,1]
	v_exp_f32_e32 v86, v86
	v_exp_f32_e32 v87, v87
	v_pk_mul_f32 v[72:73], v[72:73], v[138:139]
	v_pk_fma_f32 v[70:71], s[74:75], v[136:137], v[70:71]
	v_pk_fma_f32 v[138:139], v[58:59], s[40:41], v[72:73] op_sel_hi:[0, 1, 1]
	v_pk_mul_f32 v[72:73], v[86:87], v[140:141]
	v_pk_mul_f32 v[74:75], v[54:55], v[8:9] op_sel_hi:[0,1]
	v_pk_fma_f32 v[140:141], v[58:59], s[42:43], v[72:73] op_sel_hi:[0, 1, 1]
	v_pk_mul_f32 v[72:73], v[54:55], v[6:7] op_sel_hi:[0,1]
	v_exp_f32_e32 v72, v72
	v_exp_f32_e32 v73, v73
	v_exp_f32_e32 v74, v74
	v_exp_f32_e32 v75, v75
	v_pk_fma_f32 v[70:71], s[76:77], v[138:139], v[70:71]
	v_pk_mul_f32 v[72:73], v[72:73], v[142:143]
	v_pk_fma_f32 v[70:71], s[78:79], v[140:141], v[70:71]
	v_pk_fma_f32 v[142:143], v[58:59], s[44:45], v[72:73] op_sel_hi:[0, 1, 1]
	v_pk_mul_f32 v[72:73], v[74:75], v[144:145]
	v_pk_mul_f32 v[74:75], v[54:55], v[4:5] op_sel_hi:[0,1]
	v_pk_fma_f32 v[144:145], v[58:59], s[46:47], v[72:73] op_sel_hi:[0, 1, 1]
	v_pk_mul_f32 v[72:73], v[54:55], v[2:3] op_sel_hi:[0,1]
	v_exp_f32_e32 v72, v72
	v_exp_f32_e32 v73, v73
	v_exp_f32_e32 v74, v74
	v_exp_f32_e32 v75, v75
	v_pk_fma_f32 v[70:71], s[80:81], v[142:143], v[70:71]
	v_pk_mul_f32 v[72:73], v[72:73], v[146:147]
	v_pk_fma_f32 v[70:71], s[82:83], v[144:145], v[70:71]
	v_pk_fma_f32 v[146:147], v[58:59], s[48:49], v[72:73] op_sel_hi:[0, 1, 1]
	v_pk_mul_f32 v[72:73], v[74:75], v[148:149]
	v_pk_fma_f32 v[70:71], s[84:85], v[146:147], v[70:71]
	v_pk_fma_f32 v[148:149], v[58:59], s[50:51], v[72:73] op_sel_hi:[0, 1, 1]
	v_pk_fma_f32 v[70:71], s[86:87], v[148:149], v[70:71]
	s_waitcnt lgkmcnt(0)
	s_load_dwordx16 s[36:51], s[54:55], 0x200
	s_load_dwordx16 s[72:87], s[54:55], 0x240
	s_nop 0
	v_add_f32_e32 v54, v70, v71
	v_fma_mix_f32 v54, v1, v55, v54 op_sel_hi:[0,1,0]
	v_fma_mixlo_f16 v54, v54, v59, 0 op_sel_hi:[0,1,0]
	ds_write_b16 v68, v54 offset:6176
	v_cvt_f32_f16_sdwa v54, v63 dst_sel:DWORD dst_unused:UNUSED_PAD src0_sel:WORD_1
	v_pk_mul_f32 v[62:63], v[54:55], v[14:15] op_sel_hi:[0,1]
	v_exp_f32_e32 v62, v62
	v_exp_f32_e32 v63, v63
	v_pk_mul_f32 v[150:151], v[54:55], v[16:17] op_sel_hi:[0,1]
	v_exp_f32_e32 v150, v150
	v_exp_f32_e32 v151, v151
	v_fma_mix_f32 v58, v54, v55, 0 op_sel:[0,1,0] op_sel_hi:[0,1,0]
	v_pk_mul_f32 v[62:63], v[62:63], v[134:135]
	v_pk_fma_f32 v[62:63], v[58:59], s[56:57], v[62:63] op_sel_hi:[0, 1, 1]
	v_pk_fma_f32 v[102:103], s[88:89], v[62:63], 0 op_sel_hi:[1, 1, 0]
	v_pk_mul_f32 v[118:119], v[150:151], v[136:137]
	s_nop 0
	v_pk_fma_f32 v[134:135], v[58:59], s[58:59], v[118:119] op_sel_hi:[0, 1, 1]
	v_pk_mul_f32 v[104:105], v[54:55], v[10:11] op_sel_hi:[0,1]
	v_exp_f32_e32 v104, v104
	v_exp_f32_e32 v105, v105
	v_pk_mul_f32 v[118:119], v[54:55], v[12:13] op_sel_hi:[0,1]
	v_exp_f32_e32 v118, v118
	v_exp_f32_e32 v119, v119
	v_pk_mul_f32 v[104:105], v[104:105], v[138:139]
	v_pk_fma_f32 v[102:103], s[90:91], v[134:135], v[102:103]
	v_pk_fma_f32 v[136:137], v[58:59], s[60:61], v[104:105] op_sel_hi:[0, 1, 1]
	v_pk_mul_f32 v[104:105], v[118:119], v[140:141]
	v_pk_mul_f32 v[106:107], v[54:55], v[8:9] op_sel_hi:[0,1]
	v_pk_fma_f32 v[138:139], v[58:59], s[62:63], v[104:105] op_sel_hi:[0, 1, 1]
	v_pk_mul_f32 v[104:105], v[54:55], v[6:7] op_sel_hi:[0,1]
	v_exp_f32_e32 v104, v104
	v_exp_f32_e32 v105, v105
	v_exp_f32_e32 v106, v106
	v_exp_f32_e32 v107, v107
	v_pk_fma_f32 v[102:103], s[92:93], v[136:137], v[102:103]
	v_pk_mul_f32 v[104:105], v[104:105], v[142:143]
	v_pk_fma_f32 v[102:103], s[94:95], v[138:139], v[102:103]
	v_pk_fma_f32 v[140:141], v[58:59], s[64:65], v[104:105] op_sel_hi:[0, 1, 1]
	v_pk_mul_f32 v[104:105], v[106:107], v[144:145]
	v_pk_mul_f32 v[106:107], v[54:55], v[4:5] op_sel_hi:[0,1]
	v_pk_fma_f32 v[142:143], v[58:59], s[66:67], v[104:105] op_sel_hi:[0, 1, 1]
	v_pk_mul_f32 v[104:105], v[54:55], v[2:3] op_sel_hi:[0,1]
	v_exp_f32_e32 v104, v104
	v_exp_f32_e32 v105, v105
	v_exp_f32_e32 v106, v106
	v_exp_f32_e32 v107, v107
	v_pk_fma_f32 v[102:103], s[96:97], v[140:141], v[102:103]
	v_pk_mul_f32 v[104:105], v[104:105], v[146:147]
	v_pk_fma_f32 v[102:103], s[98:99], v[142:143], v[102:103]
	v_pk_fma_f32 v[144:145], v[58:59], s[68:69], v[104:105] op_sel_hi:[0, 1, 1]
	v_pk_mul_f32 v[104:105], v[106:107], v[148:149]
	v_pk_fma_f32 v[102:103], s[20:21], v[144:145], v[102:103]
	v_pk_fma_f32 v[146:147], v[58:59], s[70:71], v[104:105] op_sel_hi:[0, 1, 1]
	v_pk_fma_f32 v[102:103], s[22:23], v[146:147], v[102:103]
	s_waitcnt lgkmcnt(0)
	s_load_dwordx16 s[56:71], s[54:55], 0x280
	s_load_dwordx8 s[88:95], s[54:55], 0x2c0
	s_load_dwordx4 s[96:99], s[54:55], 0x2e0
	s_load_dwordx4 s[20:23], s[54:55], 0x2f0
	s_nop 0
	v_add_f32_e32 v54, v102, v103
	v_fma_mix_f32 v54, v1, v55, v54 op_sel:[0,1,0] op_sel_hi:[0,1,0]
	v_fma_mixlo_f16 v54, v54, v59, 0 op_sel:[0,1,0] op_sel_hi:[0,1,0]
	ds_write_b16 v68, v54 offset:7216
	v_cvt_f32_f16_e32 v54, v64
	v_pk_mul_f32 v[148:149], v[54:55], v[14:15] op_sel_hi:[0,1]
	v_exp_f32_e32 v148, v148
	v_exp_f32_e32 v149, v149
	v_pk_mul_f32 v[150:151], v[54:55], v[16:17] op_sel_hi:[0,1]
	v_exp_f32_e32 v150, v150
	v_exp_f32_e32 v151, v151
	v_fma_mix_f32 v58, v54, v56, 0 op_sel_hi:[0,1,0]
	v_pk_mul_f32 v[62:63], v[148:149], v[62:63]
	v_pk_fma_f32 v[62:63], v[58:59], s[36:37], v[62:63] op_sel_hi:[0, 1, 1]
	v_pk_fma_f32 v[70:71], s[72:73], v[62:63], 0 op_sel_hi:[1, 1, 0]
	v_pk_mul_f32 v[86:87], v[150:151], v[134:135]
	s_nop 0
	v_pk_fma_f32 v[134:135], v[58:59], s[38:39], v[86:87] op_sel_hi:[0, 1, 1]
	v_pk_mul_f32 v[72:73], v[54:55], v[10:11] op_sel_hi:[0,1]
	v_exp_f32_e32 v72, v72
	v_exp_f32_e32 v73, v73
	v_pk_mul_f32 v[86:87], v[54:55], v[12:13] op_sel_hi:[0,1]
	v_exp_f32_e32 v86, v86
	v_exp_f32_e32 v87, v87
	v_pk_mul_f32 v[72:73], v[72:73], v[136:137]
	v_pk_fma_f32 v[70:71], s[74:75], v[134:135], v[70:71]
	v_pk_fma_f32 v[136:137], v[58:59], s[40:41], v[72:73] op_sel_hi:[0, 1, 1]
	v_pk_mul_f32 v[72:73], v[86:87], v[138:139]
	v_pk_mul_f32 v[74:75], v[54:55], v[8:9] op_sel_hi:[0,1]
	v_pk_fma_f32 v[138:139], v[58:59], s[42:43], v[72:73] op_sel_hi:[0, 1, 1]
	v_pk_mul_f32 v[72:73], v[54:55], v[6:7] op_sel_hi:[0,1]
	v_exp_f32_e32 v72, v72
	v_exp_f32_e32 v73, v73
	v_exp_f32_e32 v74, v74
	v_exp_f32_e32 v75, v75
	v_pk_fma_f32 v[70:71], s[76:77], v[136:137], v[70:71]
	v_pk_mul_f32 v[72:73], v[72:73], v[140:141]
	v_pk_fma_f32 v[70:71], s[78:79], v[138:139], v[70:71]
	v_pk_fma_f32 v[140:141], v[58:59], s[44:45], v[72:73] op_sel_hi:[0, 1, 1]
	v_pk_mul_f32 v[72:73], v[74:75], v[142:143]
	v_pk_fma_f32 v[70:71], s[80:81], v[140:141], v[70:71]
	v_pk_fma_f32 v[142:143], v[58:59], s[46:47], v[72:73] op_sel_hi:[0, 1, 1]
	v_pk_mul_f32 v[72:73], v[54:55], v[2:3] op_sel_hi:[0,1]
	v_exp_f32_e32 v72, v72
	v_exp_f32_e32 v73, v73
	v_pk_mul_f32 v[54:55], v[54:55], v[4:5] op_sel_hi:[0,1]
	v_exp_f32_e32 v54, v54
	v_exp_f32_e32 v55, v55
	v_pk_mul_f32 v[72:73], v[72:73], v[144:145]
	v_pk_fma_f32 v[70:71], s[82:83], v[142:143], v[70:71]
	v_pk_fma_f32 v[144:145], v[58:59], s[48:49], v[72:73] op_sel_hi:[0, 1, 1]
	v_pk_mul_f32 v[54:55], v[54:55], v[146:147]
	v_pk_fma_f32 v[70:71], s[84:85], v[144:145], v[70:71]
	v_pk_fma_f32 v[54:55], v[58:59], s[50:51], v[54:55] op_sel_hi:[0, 1, 1]
	v_pk_fma_f32 v[58:59], s[86:87], v[54:55], v[70:71]
	s_waitcnt lgkmcnt(0)
	s_load_dwordx16 s[36:51], s[54:55], 0x300
	s_load_dwordx16 s[72:87], s[54:55], 0x340
	s_nop 0
	v_add_f32_e32 v58, v58, v59
	v_fma_mix_f32 v58, v1, v56, v58 op_sel_hi:[0,1,0]
	v_fma_mixlo_f16 v58, v58, v60, 0 op_sel_hi:[0,1,0]
	ds_write_b16 v68, v58 offset:8256
	v_cvt_f32_f16_sdwa v58, v64 dst_sel:DWORD dst_unused:UNUSED_PAD src0_sel:WORD_1
	v_pk_mul_f32 v[146:147], v[58:59], v[14:15] op_sel_hi:[0,1]
	v_exp_f32_e32 v146, v146
	v_exp_f32_e32 v147, v147
	v_pk_mul_f32 v[148:149], v[58:59], v[16:17] op_sel_hi:[0,1]
	v_exp_f32_e32 v148, v148
	v_exp_f32_e32 v149, v149
	v_fma_mix_f32 v64, v58, v56, 0 op_sel:[0,1,0] op_sel_hi:[0,1,0]
	v_pk_mul_f32 v[62:63], v[146:147], v[62:63]
	v_pk_fma_f32 v[62:63], v[64:65], s[56:57], v[62:63] op_sel_hi:[0, 1, 1]
	v_pk_fma_f32 v[102:103], s[88:89], v[62:63], 0 op_sel_hi:[1, 1, 0]
	v_pk_mul_f32 v[118:119], v[148:149], v[134:135]
	s_nop 0
	v_pk_fma_f32 v[134:135], v[64:65], s[58:59], v[118:119] op_sel_hi:[0, 1, 1]
	v_pk_mul_f32 v[104:105], v[58:59], v[10:11] op_sel_hi:[0,1]
	v_exp_f32_e32 v104, v104
	v_exp_f32_e32 v105, v105
	v_pk_mul_f32 v[118:119], v[58:59], v[12:13] op_sel_hi:[0,1]
	v_exp_f32_e32 v118, v118
	v_exp_f32_e32 v119, v119
	v_pk_mul_f32 v[104:105], v[104:105], v[136:137]
	v_pk_fma_f32 v[102:103], s[90:91], v[134:135], v[102:103]
	v_pk_fma_f32 v[136:137], v[64:65], s[60:61], v[104:105] op_sel_hi:[0, 1, 1]
	v_pk_mul_f32 v[104:105], v[118:119], v[138:139]
	v_pk_mul_f32 v[106:107], v[58:59], v[8:9] op_sel_hi:[0,1]
	v_pk_fma_f32 v[138:139], v[64:65], s[62:63], v[104:105] op_sel_hi:[0, 1, 1]
	v_pk_mul_f32 v[104:105], v[58:59], v[6:7] op_sel_hi:[0,1]
	v_exp_f32_e32 v104, v104
	v_exp_f32_e32 v105, v105
	v_exp_f32_e32 v106, v106
	v_exp_f32_e32 v107, v107
	v_pk_fma_f32 v[102:103], s[92:93], v[136:137], v[102:103]
	v_pk_mul_f32 v[104:105], v[104:105], v[140:141]
	v_pk_fma_f32 v[102:103], s[94:95], v[138:139], v[102:103]
	v_pk_fma_f32 v[140:141], v[64:65], s[64:65], v[104:105] op_sel_hi:[0, 1, 1]
	v_pk_mul_f32 v[104:105], v[106:107], v[142:143]
	v_pk_fma_f32 v[102:103], s[96:97], v[140:141], v[102:103]
	v_pk_fma_f32 v[142:143], v[64:65], s[66:67], v[104:105] op_sel_hi:[0, 1, 1]
	v_pk_mul_f32 v[104:105], v[58:59], v[2:3] op_sel_hi:[0,1]
	v_exp_f32_e32 v104, v104
	v_exp_f32_e32 v105, v105
	v_pk_mul_f32 v[58:59], v[58:59], v[4:5] op_sel_hi:[0,1]
	v_exp_f32_e32 v58, v58
	v_exp_f32_e32 v59, v59
	v_pk_mul_f32 v[104:105], v[104:105], v[144:145]
	v_pk_fma_f32 v[102:103], s[98:99], v[142:143], v[102:103]
	v_pk_fma_f32 v[144:145], v[64:65], s[68:69], v[104:105] op_sel_hi:[0, 1, 1]
	v_pk_mul_f32 v[54:55], v[58:59], v[54:55]
	v_pk_fma_f32 v[102:103], s[20:21], v[144:145], v[102:103]
	v_pk_fma_f32 v[54:55], v[64:65], s[70:71], v[54:55] op_sel_hi:[0, 1, 1]
	v_pk_fma_f32 v[58:59], s[22:23], v[54:55], v[102:103]
	s_waitcnt lgkmcnt(0)
	s_load_dwordx16 s[56:71], s[54:55], 0x380
	s_load_dwordx8 s[88:95], s[54:55], 0x3c0
	s_load_dwordx4 s[96:99], s[54:55], 0x3e0
	s_load_dwordx4 s[20:23], s[54:55], 0x3f0
	s_nop 0
	v_add_f32_e32 v58, v58, v59
	v_fma_mix_f32 v56, v1, v56, v58 op_sel:[0,1,0] op_sel_hi:[0,1,0]
	v_fma_mixlo_f16 v56, v56, v60, 0 op_sel:[0,1,0] op_sel_hi:[0,1,0]
	ds_write_b16 v68, v56 offset:9296
	v_cvt_f32_f16_e32 v56, v65
	v_pk_mul_f32 v[146:147], v[56:57], v[14:15] op_sel_hi:[0,1]
	v_exp_f32_e32 v146, v146
	v_exp_f32_e32 v147, v147
	v_pk_mul_f32 v[148:149], v[56:57], v[16:17] op_sel_hi:[0,1]
	v_exp_f32_e32 v148, v148
	v_exp_f32_e32 v149, v149
	v_fma_mix_f32 v58, v56, v57, 0 op_sel_hi:[0,1,0]
	v_pk_mul_f32 v[62:63], v[146:147], v[62:63]
	v_pk_fma_f32 v[62:63], v[58:59], s[36:37], v[62:63] op_sel_hi:[0, 1, 1]
	v_pk_fma_f32 v[70:71], s[72:73], v[62:63], 0 op_sel_hi:[1, 1, 0]
	v_pk_mul_f32 v[86:87], v[148:149], v[134:135]
	s_nop 0
	v_pk_fma_f32 v[134:135], v[58:59], s[38:39], v[86:87] op_sel_hi:[0, 1, 1]
	v_pk_mul_f32 v[72:73], v[56:57], v[10:11] op_sel_hi:[0,1]
	v_exp_f32_e32 v72, v72
	v_exp_f32_e32 v73, v73
	v_pk_mul_f32 v[86:87], v[56:57], v[12:13] op_sel_hi:[0,1]
	v_exp_f32_e32 v86, v86
	v_exp_f32_e32 v87, v87
	v_pk_mul_f32 v[72:73], v[72:73], v[136:137]
	v_pk_fma_f32 v[70:71], s[74:75], v[134:135], v[70:71]
	v_pk_fma_f32 v[136:137], v[58:59], s[40:41], v[72:73] op_sel_hi:[0, 1, 1]
	v_pk_mul_f32 v[72:73], v[86:87], v[138:139]
	v_pk_mul_f32 v[74:75], v[56:57], v[8:9] op_sel_hi:[0,1]
	v_pk_fma_f32 v[138:139], v[58:59], s[42:43], v[72:73] op_sel_hi:[0, 1, 1]
	v_pk_mul_f32 v[72:73], v[56:57], v[6:7] op_sel_hi:[0,1]
	v_exp_f32_e32 v72, v72
	v_exp_f32_e32 v73, v73
	v_exp_f32_e32 v74, v74
	v_exp_f32_e32 v75, v75
	v_pk_fma_f32 v[70:71], s[76:77], v[136:137], v[70:71]
	v_pk_mul_f32 v[72:73], v[72:73], v[140:141]
	v_pk_fma_f32 v[70:71], s[78:79], v[138:139], v[70:71]
	v_pk_fma_f32 v[140:141], v[58:59], s[44:45], v[72:73] op_sel_hi:[0, 1, 1]
	v_pk_mul_f32 v[72:73], v[74:75], v[142:143]
	v_pk_mul_f32 v[74:75], v[56:57], v[4:5] op_sel_hi:[0,1]
	v_pk_fma_f32 v[142:143], v[58:59], s[46:47], v[72:73] op_sel_hi:[0, 1, 1]
	v_pk_mul_f32 v[72:73], v[56:57], v[2:3] op_sel_hi:[0,1]
	v_exp_f32_e32 v72, v72
	v_exp_f32_e32 v73, v73
	v_exp_f32_e32 v74, v74
	v_exp_f32_e32 v75, v75
	v_pk_fma_f32 v[70:71], s[80:81], v[140:141], v[70:71]
	v_pk_mul_f32 v[72:73], v[72:73], v[144:145]
	v_pk_fma_f32 v[70:71], s[82:83], v[142:143], v[70:71]
	v_pk_fma_f32 v[144:145], v[58:59], s[48:49], v[72:73] op_sel_hi:[0, 1, 1]
	v_pk_mul_f32 v[54:55], v[74:75], v[54:55]
	v_pk_fma_f32 v[70:71], s[84:85], v[144:145], v[70:71]
	v_pk_fma_f32 v[54:55], v[58:59], s[50:51], v[54:55] op_sel_hi:[0, 1, 1]
	v_pk_fma_f32 v[58:59], s[86:87], v[54:55], v[70:71]
	s_waitcnt lgkmcnt(0)
	s_load_dwordx16 s[36:51], s[54:55], 0x400
	s_load_dwordx16 s[72:87], s[54:55], 0x440
	s_nop 0
	v_add_f32_e32 v56, v58, v59
	v_fma_mix_f32 v56, v1, v57, v56 op_sel_hi:[0,1,0]
	v_fma_mixlo_f16 v56, v56, v61, 0 op_sel_hi:[0,1,0]
	ds_write_b16 v68, v56 offset:10336
	v_cvt_f32_f16_sdwa v56, v65 dst_sel:DWORD dst_unused:UNUSED_PAD src0_sel:WORD_1
	v_pk_mul_f32 v[64:65], v[56:57], v[14:15] op_sel_hi:[0,1]
	v_pk_mul_f32 v[146:147], v[56:57], v[16:17] op_sel_hi:[0,1]
	v_exp_f32_e32 v64, v64
	v_exp_f32_e32 v65, v65
	v_exp_f32_e32 v146, v146
	v_exp_f32_e32 v147, v147
	v_fma_mix_f32 v58, v56, v57, 0 op_sel:[0,1,0] op_sel_hi:[0,1,0]
	v_pk_mul_f32 v[62:63], v[64:65], v[62:63]
	v_pk_mul_f32 v[64:65], v[146:147], v[134:135]
	v_pk_fma_f32 v[134:135], v[58:59], s[58:59], v[64:65] op_sel_hi:[0, 1, 1]
	v_pk_mul_f32 v[64:65], v[56:57], v[10:11] op_sel_hi:[0,1]
	v_pk_fma_f32 v[148:149], v[58:59], s[56:57], v[62:63] op_sel_hi:[0, 1, 1]
	v_exp_f32_e32 v64, v64
	v_exp_f32_e32 v65, v65
	v_pk_mul_f32 v[102:103], v[56:57], v[12:13] op_sel_hi:[0,1]
	v_exp_f32_e32 v102, v102
	v_exp_f32_e32 v103, v103
	v_pk_fma_f32 v[62:63], s[88:89], v[148:149], 0 op_sel_hi:[1, 1, 0]
	v_pk_mul_f32 v[64:65], v[64:65], v[136:137]
	v_pk_fma_f32 v[62:63], s[90:91], v[134:135], v[62:63]
	v_pk_fma_f32 v[136:137], v[58:59], s[60:61], v[64:65] op_sel_hi:[0, 1, 1]
	v_pk_mul_f32 v[64:65], v[102:103], v[138:139]
	v_pk_fma_f32 v[62:63], s[92:93], v[136:137], v[62:63]
	v_pk_fma_f32 v[122:123], v[58:59], s[62:63], v[64:65] op_sel_hi:[0, 1, 1]
	v_pk_mul_f32 v[64:65], v[56:57], v[6:7] op_sel_hi:[0,1]
	v_exp_f32_e32 v64, v64
	v_exp_f32_e32 v65, v65
	v_pk_mul_f32 v[102:103], v[56:57], v[8:9] op_sel_hi:[0,1]
	v_exp_f32_e32 v102, v102
	v_exp_f32_e32 v103, v103
	v_pk_mul_f32 v[64:65], v[64:65], v[140:141]
	v_pk_fma_f32 v[62:63], s[94:95], v[122:123], v[62:63]
	v_pk_fma_f32 v[124:125], v[58:59], s[64:65], v[64:65] op_sel_hi:[0, 1, 1]
	v_pk_mul_f32 v[64:65], v[102:103], v[142:143]
	v_pk_fma_f32 v[62:63], s[96:97], v[124:125], v[62:63]
	v_pk_fma_f32 v[126:127], v[58:59], s[66:67], v[64:65] op_sel_hi:[0, 1, 1]
	v_pk_mul_f32 v[64:65], v[56:57], v[2:3] op_sel_hi:[0,1]
	v_exp_f32_e32 v64, v64
	v_exp_f32_e32 v65, v65
	v_pk_mul_f32 v[102:103], v[56:57], v[4:5] op_sel_hi:[0,1]
	v_exp_f32_e32 v102, v102
	v_exp_f32_e32 v103, v103
	v_pk_mul_f32 v[64:65], v[64:65], v[144:145]
	v_pk_fma_f32 v[62:63], s[98:99], v[126:127], v[62:63]
	v_pk_fma_f32 v[128:129], v[58:59], s[68:69], v[64:65] op_sel_hi:[0, 1, 1]
	v_pk_mul_f32 v[54:55], v[102:103], v[54:55]
	v_pk_fma_f32 v[62:63], s[20:21], v[128:129], v[62:63]
	v_pk_fma_f32 v[130:131], v[58:59], s[70:71], v[54:55] op_sel_hi:[0, 1, 1]
	v_pk_fma_f32 v[54:55], s[22:23], v[130:131], v[62:63]
	s_waitcnt lgkmcnt(0)
	s_load_dwordx16 s[56:71], s[54:55], 0x480
	s_load_dwordx8 s[88:95], s[54:55], 0x4c0
	s_load_dwordx4 s[96:99], s[54:55], 0x4e0
	s_load_dwordx4 s[20:23], s[54:55], 0x4f0
	s_nop 0
	v_add_f32_e32 v54, v54, v55
	v_fma_mix_f32 v54, v1, v57, v54 op_sel:[0,1,0] op_sel_hi:[0,1,0]
	v_fma_mixlo_f16 v54, v54, v61, 0 op_sel:[0,1,0] op_sel_hi:[0,1,0]
	ds_write_b16 v68, v54 offset:11376
	s_waitcnt vmcnt(8)
	v_cvt_f32_f16_e32 v132, v50
	s_waitcnt vmcnt(7)
	v_pk_mul_f32 v[140:141], v[132:133], v[14:15] op_sel_hi:[0,1]
	v_exp_f32_e32 v140, v140
	v_exp_f32_e32 v141, v141
	v_pk_mul_f32 v[142:143], v[132:133], v[16:17] op_sel_hi:[0,1]
	v_exp_f32_e32 v142, v142
	v_exp_f32_e32 v143, v143
	v_fma_mix_f32 v138, v132, v42, 0 op_sel_hi:[0,1,0]
	v_pk_mul_f32 v[140:141], v[140:141], v[148:149]
	v_pk_fma_f32 v[140:141], v[138:139], s[36:37], v[140:141] op_sel_hi:[0, 1, 1]
	v_pk_fma_f32 v[70:71], s[72:73], v[140:141], 0 op_sel_hi:[1, 1, 0]
	v_pk_mul_f32 v[86:87], v[142:143], v[134:135]
	s_nop 0
	v_pk_fma_f32 v[134:135], v[138:139], s[38:39], v[86:87] op_sel_hi:[0, 1, 1]
	v_pk_mul_f32 v[72:73], v[132:133], v[10:11] op_sel_hi:[0,1]
	v_exp_f32_e32 v72, v72
	v_exp_f32_e32 v73, v73
	v_pk_mul_f32 v[86:87], v[132:133], v[12:13] op_sel_hi:[0,1]
	v_exp_f32_e32 v86, v86
	v_exp_f32_e32 v87, v87
	v_pk_mul_f32 v[72:73], v[72:73], v[136:137]
	v_pk_fma_f32 v[70:71], s[74:75], v[134:135], v[70:71]
	v_pk_fma_f32 v[136:137], v[138:139], s[40:41], v[72:73] op_sel_hi:[0, 1, 1]
	v_pk_mul_f32 v[72:73], v[86:87], v[122:123]
	v_pk_mul_f32 v[74:75], v[132:133], v[8:9] op_sel_hi:[0,1]
	v_pk_fma_f32 v[122:123], v[138:139], s[42:43], v[72:73] op_sel_hi:[0, 1, 1]
	v_pk_mul_f32 v[72:73], v[132:133], v[6:7] op_sel_hi:[0,1]
	v_exp_f32_e32 v72, v72
	v_exp_f32_e32 v73, v73
	v_exp_f32_e32 v74, v74
	v_exp_f32_e32 v75, v75
	v_pk_fma_f32 v[70:71], s[76:77], v[136:137], v[70:71]
	v_pk_mul_f32 v[72:73], v[72:73], v[124:125]
	v_pk_fma_f32 v[70:71], s[78:79], v[122:123], v[70:71]
	v_pk_fma_f32 v[124:125], v[138:139], s[44:45], v[72:73] op_sel_hi:[0, 1, 1]
	v_pk_mul_f32 v[72:73], v[74:75], v[126:127]
	v_pk_mul_f32 v[74:75], v[132:133], v[4:5] op_sel_hi:[0,1]
	v_pk_fma_f32 v[126:127], v[138:139], s[46:47], v[72:73] op_sel_hi:[0, 1, 1]
	v_pk_mul_f32 v[72:73], v[132:133], v[2:3] op_sel_hi:[0,1]
	v_exp_f32_e32 v72, v72
	v_exp_f32_e32 v73, v73
	v_exp_f32_e32 v74, v74
	v_exp_f32_e32 v75, v75
	v_pk_fma_f32 v[70:71], s[80:81], v[124:125], v[70:71]
	v_pk_mul_f32 v[72:73], v[72:73], v[128:129]
	v_pk_fma_f32 v[70:71], s[82:83], v[126:127], v[70:71]
	v_pk_fma_f32 v[128:129], v[138:139], s[48:49], v[72:73] op_sel_hi:[0, 1, 1]
	v_pk_mul_f32 v[72:73], v[74:75], v[130:131]
	v_pk_fma_f32 v[70:71], s[84:85], v[128:129], v[70:71]
	v_pk_fma_f32 v[130:131], v[138:139], s[50:51], v[72:73] op_sel_hi:[0, 1, 1]
	v_pk_fma_f32 v[70:71], s[86:87], v[130:131], v[70:71]
	s_waitcnt lgkmcnt(0)
	s_load_dwordx16 s[36:51], s[54:55], 0x500
	s_load_dwordx16 s[72:87], s[54:55], 0x540
	s_nop 0
	v_add_f32_e32 v69, v70, v71
	v_fma_mix_f32 v69, v1, v42, v69 op_sel_hi:[0,1,0]
	s_waitcnt vmcnt(6)
	v_fma_mixlo_f16 v69, v69, v46, 0 op_sel_hi:[0,1,0]
	ds_write_b16 v68, v69 offset:12416
	v_cvt_f32_f16_sdwa v50, v50 dst_sel:DWORD dst_unused:UNUSED_PAD src0_sel:WORD_1
	v_pk_mul_f32 v[138:139], v[50:51], v[14:15] op_sel_hi:[0,1]
	v_exp_f32_e32 v138, v138
	v_exp_f32_e32 v139, v139
	v_pk_mul_f32 v[142:143], v[50:51], v[16:17] op_sel_hi:[0,1]
	v_exp_f32_e32 v142, v142
	v_exp_f32_e32 v143, v143
	v_fma_mix_f32 v132, v50, v42, 0 op_sel:[0,1,0] op_sel_hi:[0,1,0]
	v_pk_mul_f32 v[138:139], v[138:139], v[140:141]
	v_pk_fma_f32 v[138:139], v[132:133], s[56:57], v[138:139] op_sel_hi:[0, 1, 1]
	v_pk_fma_f32 v[54:55], s[88:89], v[138:139], 0 op_sel_hi:[1, 1, 0]
	v_pk_mul_f32 v[106:107], v[142:143], v[134:135]
	s_nop 0
	v_pk_fma_f32 v[134:135], v[132:133], s[58:59], v[106:107] op_sel_hi:[0, 1, 1]
	v_pk_mul_f32 v[56:57], v[50:51], v[10:11] op_sel_hi:[0,1]
	v_exp_f32_e32 v56, v56
	v_exp_f32_e32 v57, v57
	v_pk_mul_f32 v[106:107], v[50:51], v[12:13] op_sel_hi:[0,1]
	v_exp_f32_e32 v106, v106
	v_exp_f32_e32 v107, v107
	v_pk_mul_f32 v[56:57], v[56:57], v[136:137]
	v_pk_fma_f32 v[54:55], s[90:91], v[134:135], v[54:55]
	v_pk_fma_f32 v[136:137], v[132:133], s[60:61], v[56:57] op_sel_hi:[0, 1, 1]
	v_pk_mul_f32 v[56:57], v[106:107], v[122:123]
	v_pk_mul_f32 v[58:59], v[50:51], v[8:9] op_sel_hi:[0,1]
	v_pk_fma_f32 v[122:123], v[132:133], s[62:63], v[56:57] op_sel_hi:[0, 1, 1]
	v_pk_mul_f32 v[56:57], v[50:51], v[6:7] op_sel_hi:[0,1]
	v_exp_f32_e32 v56, v56
	v_exp_f32_e32 v57, v57
	v_exp_f32_e32 v58, v58
	v_exp_f32_e32 v59, v59
	v_pk_fma_f32 v[54:55], s[92:93], v[136:137], v[54:55]
	v_pk_mul_f32 v[56:57], v[56:57], v[124:125]
	v_pk_fma_f32 v[54:55], s[94:95], v[122:123], v[54:55]
	v_pk_fma_f32 v[124:125], v[132:133], s[64:65], v[56:57] op_sel_hi:[0, 1, 1]
	v_pk_mul_f32 v[56:57], v[58:59], v[126:127]
	v_pk_mul_f32 v[58:59], v[50:51], v[4:5] op_sel_hi:[0,1]
	v_pk_fma_f32 v[126:127], v[132:133], s[66:67], v[56:57] op_sel_hi:[0, 1, 1]
	v_pk_mul_f32 v[56:57], v[50:51], v[2:3] op_sel_hi:[0,1]
	v_exp_f32_e32 v56, v56
	v_exp_f32_e32 v57, v57
	v_exp_f32_e32 v58, v58
	v_exp_f32_e32 v59, v59
	v_pk_fma_f32 v[54:55], s[96:97], v[124:125], v[54:55]
	v_pk_mul_f32 v[56:57], v[56:57], v[128:129]
	v_pk_fma_f32 v[54:55], s[98:99], v[126:127], v[54:55]
	v_pk_fma_f32 v[128:129], v[132:133], s[68:69], v[56:57] op_sel_hi:[0, 1, 1]
	v_pk_mul_f32 v[56:57], v[58:59], v[130:131]
	v_pk_fma_f32 v[54:55], s[20:21], v[128:129], v[54:55]
	v_pk_fma_f32 v[130:131], v[132:133], s[70:71], v[56:57] op_sel_hi:[0, 1, 1]
	v_pk_fma_f32 v[54:55], s[22:23], v[130:131], v[54:55]
	s_waitcnt lgkmcnt(0)
	s_load_dwordx16 s[56:71], s[54:55], 0x580
	s_load_dwordx8 s[88:95], s[54:55], 0x5c0
	s_load_dwordx4 s[96:99], s[54:55], 0x5e0
	s_load_dwordx4 s[20:23], s[54:55], 0x5f0
	s_nop 0
	v_add_f32_e32 v50, v54, v55
	v_fma_mix_f32 v42, v1, v42, v50 op_sel:[0,1,0] op_sel_hi:[0,1,0]
	v_fma_mixlo_f16 v42, v42, v46, 0 op_sel:[0,1,0] op_sel_hi:[0,1,0]
	ds_write_b16 v68, v42 offset:13456
	v_cvt_f32_f16_e32 v42, v51
	v_pk_mul_f32 v[132:133], v[42:43], v[14:15] op_sel_hi:[0,1]
	v_exp_f32_e32 v132, v132
	v_exp_f32_e32 v133, v133
	v_pk_mul_f32 v[140:141], v[42:43], v[16:17] op_sel_hi:[0,1]
	v_exp_f32_e32 v140, v140
	v_exp_f32_e32 v141, v141
	v_fma_mix_f32 v46, v42, v43, 0 op_sel_hi:[0,1,0]
	v_pk_mul_f32 v[132:133], v[132:133], v[138:139]
	v_pk_fma_f32 v[132:133], v[46:47], s[36:37], v[132:133] op_sel_hi:[0, 1, 1]
	v_pk_fma_f32 v[70:71], s[72:73], v[132:133], 0 op_sel_hi:[1, 1, 0]
	v_pk_mul_f32 v[86:87], v[140:141], v[134:135]
	s_nop 0
	v_pk_fma_f32 v[134:135], v[46:47], s[38:39], v[86:87] op_sel_hi:[0, 1, 1]
	v_pk_mul_f32 v[72:73], v[42:43], v[10:11] op_sel_hi:[0,1]
	v_exp_f32_e32 v72, v72
	v_exp_f32_e32 v73, v73
	v_pk_mul_f32 v[86:87], v[42:43], v[12:13] op_sel_hi:[0,1]
	v_exp_f32_e32 v86, v86
	v_exp_f32_e32 v87, v87
	v_pk_mul_f32 v[72:73], v[72:73], v[136:137]
	v_pk_fma_f32 v[70:71], s[74:75], v[134:135], v[70:71]
	v_pk_fma_f32 v[136:137], v[46:47], s[40:41], v[72:73] op_sel_hi:[0, 1, 1]
	v_pk_mul_f32 v[72:73], v[86:87], v[122:123]
	v_pk_mul_f32 v[74:75], v[42:43], v[8:9] op_sel_hi:[0,1]
	v_pk_fma_f32 v[122:123], v[46:47], s[42:43], v[72:73] op_sel_hi:[0, 1, 1]
	v_pk_mul_f32 v[72:73], v[42:43], v[6:7] op_sel_hi:[0,1]
	v_exp_f32_e32 v72, v72
	v_exp_f32_e32 v73, v73
	v_exp_f32_e32 v74, v74
	v_exp_f32_e32 v75, v75
	v_pk_fma_f32 v[70:71], s[76:77], v[136:137], v[70:71]
	v_pk_mul_f32 v[72:73], v[72:73], v[124:125]
	v_pk_fma_f32 v[70:71], s[78:79], v[122:123], v[70:71]
	v_pk_fma_f32 v[124:125], v[46:47], s[44:45], v[72:73] op_sel_hi:[0, 1, 1]
	v_pk_mul_f32 v[72:73], v[74:75], v[126:127]
	v_pk_mul_f32 v[74:75], v[42:43], v[4:5] op_sel_hi:[0,1]
	v_pk_fma_f32 v[126:127], v[46:47], s[46:47], v[72:73] op_sel_hi:[0, 1, 1]
	v_pk_mul_f32 v[72:73], v[42:43], v[2:3] op_sel_hi:[0,1]
	v_exp_f32_e32 v72, v72
	v_exp_f32_e32 v73, v73
	v_exp_f32_e32 v74, v74
	v_exp_f32_e32 v75, v75
	v_pk_fma_f32 v[70:71], s[80:81], v[124:125], v[70:71]
	v_pk_mul_f32 v[72:73], v[72:73], v[128:129]
	v_pk_fma_f32 v[70:71], s[82:83], v[126:127], v[70:71]
	v_pk_fma_f32 v[128:129], v[46:47], s[48:49], v[72:73] op_sel_hi:[0, 1, 1]
	v_pk_mul_f32 v[72:73], v[74:75], v[130:131]
	v_pk_fma_f32 v[70:71], s[84:85], v[128:129], v[70:71]
	v_pk_fma_f32 v[130:131], v[46:47], s[50:51], v[72:73] op_sel_hi:[0, 1, 1]
	v_pk_fma_f32 v[70:71], s[86:87], v[130:131], v[70:71]
	s_waitcnt lgkmcnt(0)
	s_load_dwordx16 s[36:51], s[54:55], 0x600
	s_load_dwordx16 s[72:87], s[54:55], 0x640
	s_nop 0
	v_add_f32_e32 v42, v70, v71
	v_fma_mix_f32 v42, v1, v43, v42 op_sel_hi:[0,1,0]
	v_fma_mixlo_f16 v42, v42, v47, 0 op_sel_hi:[0,1,0]
	ds_write_b16 v68, v42 offset:14496
	v_cvt_f32_f16_sdwa v42, v51 dst_sel:DWORD dst_unused:UNUSED_PAD src0_sel:WORD_1
	v_pk_mul_f32 v[50:51], v[42:43], v[14:15] op_sel_hi:[0,1]
	v_exp_f32_e32 v50, v50
	v_exp_f32_e32 v51, v51
	v_pk_mul_f32 v[138:139], v[42:43], v[16:17] op_sel_hi:[0,1]
	v_exp_f32_e32 v138, v138
	v_exp_f32_e32 v139, v139
	v_fma_mix_f32 v46, v42, v43, 0 op_sel:[0,1,0] op_sel_hi:[0,1,0]
	v_pk_mul_f32 v[50:51], v[50:51], v[132:133]
	v_pk_fma_f32 v[50:51], v[46:47], s[56:57], v[50:51] op_sel_hi:[0, 1, 1]
	v_pk_fma_f32 v[54:55], s[88:89], v[50:51], 0 op_sel_hi:[1, 1, 0]
	v_pk_mul_f32 v[106:107], v[138:139], v[134:135]
	s_nop 0
	v_pk_fma_f32 v[132:133], v[46:47], s[58:59], v[106:107] op_sel_hi:[0, 1, 1]
	v_pk_mul_f32 v[56:57], v[42:43], v[10:11] op_sel_hi:[0,1]
	v_exp_f32_e32 v56, v56
	v_exp_f32_e32 v57, v57
	v_pk_mul_f32 v[106:107], v[42:43], v[12:13] op_sel_hi:[0,1]
	v_exp_f32_e32 v106, v106
	v_exp_f32_e32 v107, v107
	v_pk_mul_f32 v[56:57], v[56:57], v[136:137]
	v_pk_fma_f32 v[54:55], s[90:91], v[132:133], v[54:55]
	v_pk_fma_f32 v[134:135], v[46:47], s[60:61], v[56:57] op_sel_hi:[0, 1, 1]
	v_pk_mul_f32 v[56:57], v[106:107], v[122:123]
	v_pk_mul_f32 v[58:59], v[42:43], v[8:9] op_sel_hi:[0,1]
	v_pk_fma_f32 v[122:123], v[46:47], s[62:63], v[56:57] op_sel_hi:[0, 1, 1]
	v_pk_mul_f32 v[56:57], v[42:43], v[6:7] op_sel_hi:[0,1]
	v_exp_f32_e32 v56, v56
	v_exp_f32_e32 v57, v57
	v_exp_f32_e32 v58, v58
	v_exp_f32_e32 v59, v59
	v_pk_fma_f32 v[54:55], s[92:93], v[134:135], v[54:55]
	v_pk_mul_f32 v[56:57], v[56:57], v[124:125]
	v_pk_fma_f32 v[54:55], s[94:95], v[122:123], v[54:55]
	v_pk_fma_f32 v[124:125], v[46:47], s[64:65], v[56:57] op_sel_hi:[0, 1, 1]
	v_pk_mul_f32 v[56:57], v[58:59], v[126:127]
	v_pk_mul_f32 v[58:59], v[42:43], v[4:5] op_sel_hi:[0,1]
	v_pk_fma_f32 v[126:127], v[46:47], s[66:67], v[56:57] op_sel_hi:[0, 1, 1]
	v_pk_mul_f32 v[56:57], v[42:43], v[2:3] op_sel_hi:[0,1]
	v_exp_f32_e32 v56, v56
	v_exp_f32_e32 v57, v57
	v_exp_f32_e32 v58, v58
	v_exp_f32_e32 v59, v59
	v_pk_fma_f32 v[54:55], s[96:97], v[124:125], v[54:55]
	v_pk_mul_f32 v[56:57], v[56:57], v[128:129]
	v_pk_fma_f32 v[54:55], s[98:99], v[126:127], v[54:55]
	v_pk_fma_f32 v[128:129], v[46:47], s[68:69], v[56:57] op_sel_hi:[0, 1, 1]
	v_pk_mul_f32 v[56:57], v[58:59], v[130:131]
	v_pk_fma_f32 v[54:55], s[20:21], v[128:129], v[54:55]
	v_pk_fma_f32 v[130:131], v[46:47], s[70:71], v[56:57] op_sel_hi:[0, 1, 1]
	v_pk_fma_f32 v[54:55], s[22:23], v[130:131], v[54:55]
	s_waitcnt lgkmcnt(0)
	s_load_dwordx16 s[56:71], s[54:55], 0x680
	s_load_dwordx8 s[88:95], s[54:55], 0x6c0
	s_load_dwordx4 s[96:99], s[54:55], 0x6e0
	s_load_dwordx4 s[20:23], s[54:55], 0x6f0
	s_nop 0
	v_add_f32_e32 v42, v54, v55
	v_fma_mix_f32 v42, v1, v43, v42 op_sel:[0,1,0] op_sel_hi:[0,1,0]
	v_fma_mixlo_f16 v42, v42, v47, 0 op_sel:[0,1,0] op_sel_hi:[0,1,0]
	ds_write_b16 v68, v42 offset:15536
	v_cvt_f32_f16_e32 v42, v52
	v_pk_mul_f32 v[136:137], v[42:43], v[14:15] op_sel_hi:[0,1]
	v_exp_f32_e32 v136, v136
	v_exp_f32_e32 v137, v137
	v_pk_mul_f32 v[138:139], v[42:43], v[16:17] op_sel_hi:[0,1]
	v_exp_f32_e32 v138, v138
	v_exp_f32_e32 v139, v139
	v_fma_mix_f32 v46, v42, v44, 0 op_sel_hi:[0,1,0]
	v_pk_mul_f32 v[50:51], v[136:137], v[50:51]
	v_pk_fma_f32 v[50:51], v[46:47], s[36:37], v[50:51] op_sel_hi:[0, 1, 1]
	v_pk_fma_f32 v[70:71], s[72:73], v[50:51], 0 op_sel_hi:[1, 1, 0]
	v_pk_mul_f32 v[86:87], v[138:139], v[132:133]
	s_nop 0
	v_pk_fma_f32 v[132:133], v[46:47], s[38:39], v[86:87] op_sel_hi:[0, 1, 1]
	v_pk_mul_f32 v[72:73], v[42:43], v[10:11] op_sel_hi:[0,1]
	v_exp_f32_e32 v72, v72
	v_exp_f32_e32 v73, v73
	v_pk_mul_f32 v[86:87], v[42:43], v[12:13] op_sel_hi:[0,1]
	v_exp_f32_e32 v86, v86
	v_exp_f32_e32 v87, v87
	v_pk_mul_f32 v[72:73], v[72:73], v[134:135]
	v_pk_fma_f32 v[70:71], s[74:75], v[132:133], v[70:71]
	v_pk_fma_f32 v[134:135], v[46:47], s[40:41], v[72:73] op_sel_hi:[0, 1, 1]
	v_pk_mul_f32 v[72:73], v[86:87], v[122:123]
	v_pk_mul_f32 v[74:75], v[42:43], v[8:9] op_sel_hi:[0,1]
	v_pk_fma_f32 v[122:123], v[46:47], s[42:43], v[72:73] op_sel_hi:[0, 1, 1]
	v_pk_mul_f32 v[72:73], v[42:43], v[6:7] op_sel_hi:[0,1]
	v_exp_f32_e32 v72, v72
	v_exp_f32_e32 v73, v73
	v_exp_f32_e32 v74, v74
	v_exp_f32_e32 v75, v75
	v_pk_fma_f32 v[70:71], s[76:77], v[134:135], v[70:71]
	v_pk_mul_f32 v[72:73], v[72:73], v[124:125]
	v_pk_fma_f32 v[70:71], s[78:79], v[122:123], v[70:71]
	v_pk_fma_f32 v[124:125], v[46:47], s[44:45], v[72:73] op_sel_hi:[0, 1, 1]
	v_pk_mul_f32 v[72:73], v[74:75], v[126:127]
	v_pk_fma_f32 v[70:71], s[80:81], v[124:125], v[70:71]
	v_pk_fma_f32 v[126:127], v[46:47], s[46:47], v[72:73] op_sel_hi:[0, 1, 1]
	v_pk_mul_f32 v[72:73], v[42:43], v[2:3] op_sel_hi:[0,1]
	v_exp_f32_e32 v72, v72
	v_exp_f32_e32 v73, v73
	v_pk_mul_f32 v[42:43], v[42:43], v[4:5] op_sel_hi:[0,1]
	v_exp_f32_e32 v42, v42
	v_exp_f32_e32 v43, v43
	v_pk_mul_f32 v[72:73], v[72:73], v[128:129]
	v_pk_fma_f32 v[70:71], s[82:83], v[126:127], v[70:71]
	v_pk_fma_f32 v[128:129], v[46:47], s[48:49], v[72:73] op_sel_hi:[0, 1, 1]
	v_pk_mul_f32 v[42:43], v[42:43], v[130:131]
	v_pk_fma_f32 v[70:71], s[84:85], v[128:129], v[70:71]
	v_pk_fma_f32 v[42:43], v[46:47], s[50:51], v[42:43] op_sel_hi:[0, 1, 1]
	v_pk_fma_f32 v[46:47], s[86:87], v[42:43], v[70:71]
	s_waitcnt lgkmcnt(0)
	s_load_dwordx16 s[36:51], s[54:55], 0x700
	s_load_dwordx16 s[72:87], s[54:55], 0x740
	s_nop 0
	v_add_f32_e32 v46, v46, v47
	v_fma_mix_f32 v46, v1, v44, v46 op_sel_hi:[0,1,0]
	v_fma_mixlo_f16 v46, v46, v48, 0 op_sel_hi:[0,1,0]
	ds_write_b16 v68, v46 offset:16576
	v_cvt_f32_f16_sdwa v46, v52 dst_sel:DWORD dst_unused:UNUSED_PAD src0_sel:WORD_1
	v_pk_mul_f32 v[130:131], v[46:47], v[14:15] op_sel_hi:[0,1]
	v_exp_f32_e32 v130, v130
	v_exp_f32_e32 v131, v131
	v_pk_mul_f32 v[136:137], v[46:47], v[16:17] op_sel_hi:[0,1]
	v_exp_f32_e32 v136, v136
	v_exp_f32_e32 v137, v137
	v_fma_mix_f32 v52, v46, v44, 0 op_sel:[0,1,0] op_sel_hi:[0,1,0]
	v_pk_mul_f32 v[50:51], v[130:131], v[50:51]
	v_pk_fma_f32 v[50:51], v[52:53], s[56:57], v[50:51] op_sel_hi:[0, 1, 1]
	v_pk_fma_f32 v[54:55], s[88:89], v[50:51], 0 op_sel_hi:[1, 1, 0]
	v_pk_mul_f32 v[106:107], v[136:137], v[132:133]
	s_nop 0
	v_pk_fma_f32 v[130:131], v[52:53], s[58:59], v[106:107] op_sel_hi:[0, 1, 1]
	v_pk_mul_f32 v[56:57], v[46:47], v[10:11] op_sel_hi:[0,1]
	v_exp_f32_e32 v56, v56
	v_exp_f32_e32 v57, v57
	v_pk_mul_f32 v[106:107], v[46:47], v[12:13] op_sel_hi:[0,1]
	v_exp_f32_e32 v106, v106
	v_exp_f32_e32 v107, v107
	v_pk_mul_f32 v[56:57], v[56:57], v[134:135]
	v_pk_fma_f32 v[54:55], s[90:91], v[130:131], v[54:55]
	v_pk_fma_f32 v[132:133], v[52:53], s[60:61], v[56:57] op_sel_hi:[0, 1, 1]
	v_pk_mul_f32 v[56:57], v[106:107], v[122:123]
	v_pk_mul_f32 v[58:59], v[46:47], v[8:9] op_sel_hi:[0,1]
	v_pk_fma_f32 v[122:123], v[52:53], s[62:63], v[56:57] op_sel_hi:[0, 1, 1]
	v_pk_mul_f32 v[56:57], v[46:47], v[6:7] op_sel_hi:[0,1]
	v_exp_f32_e32 v56, v56
	v_exp_f32_e32 v57, v57
	v_exp_f32_e32 v58, v58
	v_exp_f32_e32 v59, v59
	v_pk_fma_f32 v[54:55], s[92:93], v[132:133], v[54:55]
	v_pk_mul_f32 v[56:57], v[56:57], v[124:125]
	v_pk_fma_f32 v[54:55], s[94:95], v[122:123], v[54:55]
	v_pk_fma_f32 v[124:125], v[52:53], s[64:65], v[56:57] op_sel_hi:[0, 1, 1]
	v_pk_mul_f32 v[56:57], v[58:59], v[126:127]
	v_pk_fma_f32 v[54:55], s[96:97], v[124:125], v[54:55]
	v_pk_fma_f32 v[126:127], v[52:53], s[66:67], v[56:57] op_sel_hi:[0, 1, 1]
	v_pk_mul_f32 v[56:57], v[46:47], v[2:3] op_sel_hi:[0,1]
	v_exp_f32_e32 v56, v56
	v_exp_f32_e32 v57, v57
	v_pk_mul_f32 v[46:47], v[46:47], v[4:5] op_sel_hi:[0,1]
	v_exp_f32_e32 v46, v46
	v_exp_f32_e32 v47, v47
	v_pk_mul_f32 v[56:57], v[56:57], v[128:129]
	v_pk_fma_f32 v[54:55], s[98:99], v[126:127], v[54:55]
	v_pk_fma_f32 v[128:129], v[52:53], s[68:69], v[56:57] op_sel_hi:[0, 1, 1]
	v_pk_mul_f32 v[42:43], v[46:47], v[42:43]
	v_pk_fma_f32 v[54:55], s[20:21], v[128:129], v[54:55]
	v_pk_fma_f32 v[42:43], v[52:53], s[70:71], v[42:43] op_sel_hi:[0, 1, 1]
	v_pk_fma_f32 v[46:47], s[22:23], v[42:43], v[54:55]
	s_waitcnt lgkmcnt(0)
	s_load_dwordx16 s[56:71], s[54:55], 0x780
	s_load_dwordx8 s[88:95], s[54:55], 0x7c0
	s_load_dwordx4 s[96:99], s[54:55], 0x7e0
	s_load_dwordx4 s[20:23], s[54:55], 0x7f0
	s_nop 0
	v_add_f32_e32 v46, v46, v47
	v_fma_mix_f32 v44, v1, v44, v46 op_sel:[0,1,0] op_sel_hi:[0,1,0]
	v_fma_mixlo_f16 v44, v44, v48, 0 op_sel:[0,1,0] op_sel_hi:[0,1,0]
	ds_write_b16 v68, v44 offset:17616
	v_cvt_f32_f16_e32 v44, v53
	v_pk_mul_f32 v[134:135], v[44:45], v[14:15] op_sel_hi:[0,1]
	v_exp_f32_e32 v134, v134
	v_exp_f32_e32 v135, v135
	v_pk_mul_f32 v[136:137], v[44:45], v[16:17] op_sel_hi:[0,1]
	v_exp_f32_e32 v136, v136
	v_exp_f32_e32 v137, v137
	v_fma_mix_f32 v46, v44, v45, 0 op_sel_hi:[0,1,0]
	v_pk_mul_f32 v[50:51], v[134:135], v[50:51]
	v_pk_fma_f32 v[50:51], v[46:47], s[36:37], v[50:51] op_sel_hi:[0, 1, 1]
	v_pk_fma_f32 v[70:71], s[72:73], v[50:51], 0 op_sel_hi:[1, 1, 0]
	v_pk_mul_f32 v[86:87], v[136:137], v[130:131]
	s_nop 0
	v_pk_fma_f32 v[130:131], v[46:47], s[38:39], v[86:87] op_sel_hi:[0, 1, 1]
	v_pk_mul_f32 v[72:73], v[44:45], v[10:11] op_sel_hi:[0,1]
	v_exp_f32_e32 v72, v72
	v_exp_f32_e32 v73, v73
	v_pk_mul_f32 v[86:87], v[44:45], v[12:13] op_sel_hi:[0,1]
	v_exp_f32_e32 v86, v86
	v_exp_f32_e32 v87, v87
	v_pk_mul_f32 v[72:73], v[72:73], v[132:133]
	v_pk_fma_f32 v[70:71], s[74:75], v[130:131], v[70:71]
	v_pk_fma_f32 v[132:133], v[46:47], s[40:41], v[72:73] op_sel_hi:[0, 1, 1]
	v_pk_mul_f32 v[72:73], v[86:87], v[122:123]
	v_pk_mul_f32 v[74:75], v[44:45], v[8:9] op_sel_hi:[0,1]
	v_pk_fma_f32 v[122:123], v[46:47], s[42:43], v[72:73] op_sel_hi:[0, 1, 1]
	v_pk_mul_f32 v[72:73], v[44:45], v[6:7] op_sel_hi:[0,1]
	v_exp_f32_e32 v72, v72
	v_exp_f32_e32 v73, v73
	v_exp_f32_e32 v74, v74
	v_exp_f32_e32 v75, v75
	v_pk_fma_f32 v[70:71], s[76:77], v[132:133], v[70:71]
	v_pk_mul_f32 v[72:73], v[72:73], v[124:125]
	v_pk_fma_f32 v[70:71], s[78:79], v[122:123], v[70:71]
	v_pk_fma_f32 v[124:125], v[46:47], s[44:45], v[72:73] op_sel_hi:[0, 1, 1]
	v_pk_mul_f32 v[72:73], v[74:75], v[126:127]
	v_pk_mul_f32 v[74:75], v[44:45], v[4:5] op_sel_hi:[0,1]
	v_pk_fma_f32 v[126:127], v[46:47], s[46:47], v[72:73] op_sel_hi:[0, 1, 1]
	v_pk_mul_f32 v[72:73], v[44:45], v[2:3] op_sel_hi:[0,1]
	v_exp_f32_e32 v72, v72
	v_exp_f32_e32 v73, v73
	v_exp_f32_e32 v74, v74
	v_exp_f32_e32 v75, v75
	v_pk_fma_f32 v[70:71], s[80:81], v[124:125], v[70:71]
	v_pk_mul_f32 v[72:73], v[72:73], v[128:129]
	v_pk_fma_f32 v[70:71], s[82:83], v[126:127], v[70:71]
	v_pk_fma_f32 v[128:129], v[46:47], s[48:49], v[72:73] op_sel_hi:[0, 1, 1]
	v_pk_mul_f32 v[42:43], v[74:75], v[42:43]
	v_pk_fma_f32 v[70:71], s[84:85], v[128:129], v[70:71]
	v_pk_fma_f32 v[42:43], v[46:47], s[50:51], v[42:43] op_sel_hi:[0, 1, 1]
	v_pk_fma_f32 v[46:47], s[86:87], v[42:43], v[70:71]
	s_waitcnt lgkmcnt(0)
	s_load_dwordx16 s[36:51], s[54:55], 0x800
	s_load_dwordx16 s[72:87], s[54:55], 0x840
	s_nop 0
	v_add_f32_e32 v44, v46, v47
	v_fma_mix_f32 v44, v1, v45, v44 op_sel_hi:[0,1,0]
	v_fma_mixlo_f16 v44, v44, v49, 0 op_sel_hi:[0,1,0]
	ds_write_b16 v68, v44 offset:18656
	v_cvt_f32_f16_sdwa v44, v53 dst_sel:DWORD dst_unused:UNUSED_PAD src0_sel:WORD_1
	v_pk_mul_f32 v[52:53], v[44:45], v[14:15] op_sel_hi:[0,1]
	v_pk_mul_f32 v[134:135], v[44:45], v[16:17] op_sel_hi:[0,1]
	v_exp_f32_e32 v52, v52
	v_exp_f32_e32 v53, v53
	v_exp_f32_e32 v134, v134
	v_exp_f32_e32 v135, v135
	v_fma_mix_f32 v46, v44, v45, 0 op_sel:[0,1,0] op_sel_hi:[0,1,0]
	v_pk_mul_f32 v[50:51], v[52:53], v[50:51]
	v_pk_mul_f32 v[52:53], v[134:135], v[130:131]
	v_pk_fma_f32 v[130:131], v[46:47], s[58:59], v[52:53] op_sel_hi:[0, 1, 1]
	v_pk_mul_f32 v[52:53], v[44:45], v[10:11] op_sel_hi:[0,1]
	v_pk_fma_f32 v[136:137], v[46:47], s[56:57], v[50:51] op_sel_hi:[0, 1, 1]
	v_exp_f32_e32 v52, v52
	v_exp_f32_e32 v53, v53
	v_pk_mul_f32 v[54:55], v[44:45], v[12:13] op_sel_hi:[0,1]
	v_exp_f32_e32 v54, v54
	v_exp_f32_e32 v55, v55
	v_pk_fma_f32 v[50:51], s[88:89], v[136:137], 0 op_sel_hi:[1, 1, 0]
	v_pk_mul_f32 v[52:53], v[52:53], v[132:133]
	v_pk_fma_f32 v[50:51], s[90:91], v[130:131], v[50:51]
	v_pk_fma_f32 v[132:133], v[46:47], s[60:61], v[52:53] op_sel_hi:[0, 1, 1]
	v_pk_mul_f32 v[52:53], v[54:55], v[122:123]
	v_pk_fma_f32 v[50:51], s[92:93], v[132:133], v[50:51]
	v_pk_fma_f32 v[110:111], v[46:47], s[62:63], v[52:53] op_sel_hi:[0, 1, 1]
	v_pk_mul_f32 v[52:53], v[44:45], v[6:7] op_sel_hi:[0,1]
	v_exp_f32_e32 v52, v52
	v_exp_f32_e32 v53, v53
	v_pk_mul_f32 v[54:55], v[44:45], v[8:9] op_sel_hi:[0,1]
	v_exp_f32_e32 v54, v54
	v_exp_f32_e32 v55, v55
	v_pk_mul_f32 v[52:53], v[52:53], v[124:125]
	v_pk_fma_f32 v[50:51], s[94:95], v[110:111], v[50:51]
	v_pk_fma_f32 v[112:113], v[46:47], s[64:65], v[52:53] op_sel_hi:[0, 1, 1]
	v_pk_mul_f32 v[52:53], v[54:55], v[126:127]
	v_pk_fma_f32 v[50:51], s[96:97], v[112:113], v[50:51]
	v_pk_fma_f32 v[114:115], v[46:47], s[66:67], v[52:53] op_sel_hi:[0, 1, 1]
	v_pk_mul_f32 v[52:53], v[44:45], v[2:3] op_sel_hi:[0,1]
	v_exp_f32_e32 v52, v52
	v_exp_f32_e32 v53, v53
	v_pk_mul_f32 v[54:55], v[44:45], v[4:5] op_sel_hi:[0,1]
	v_exp_f32_e32 v54, v54
	v_exp_f32_e32 v55, v55
	v_pk_mul_f32 v[52:53], v[52:53], v[128:129]
	v_pk_fma_f32 v[50:51], s[98:99], v[114:115], v[50:51]
	v_pk_fma_f32 v[116:117], v[46:47], s[68:69], v[52:53] op_sel_hi:[0, 1, 1]
	v_pk_mul_f32 v[42:43], v[54:55], v[42:43]
	v_pk_fma_f32 v[50:51], s[20:21], v[116:117], v[50:51]
	v_pk_fma_f32 v[118:119], v[46:47], s[70:71], v[42:43] op_sel_hi:[0, 1, 1]
	v_pk_fma_f32 v[42:43], s[22:23], v[118:119], v[50:51]
	s_waitcnt lgkmcnt(0)
	s_load_dwordx16 s[56:71], s[54:55], 0x880
	s_load_dwordx8 s[88:95], s[54:55], 0x8c0
	s_load_dwordx4 s[96:99], s[54:55], 0x8e0
	s_load_dwordx4 s[20:23], s[54:55], 0x8f0
	s_nop 0
	v_add_f32_e32 v42, v42, v43
	v_fma_mix_f32 v42, v1, v45, v42 op_sel:[0,1,0] op_sel_hi:[0,1,0]
	v_fma_mixlo_f16 v42, v42, v49, 0 op_sel:[0,1,0] op_sel_hi:[0,1,0]
	ds_write_b16 v68, v42 offset:19696
	s_waitcnt vmcnt(5)
	v_cvt_f32_f16_e32 v120, v38
	s_waitcnt vmcnt(4)
	v_pk_mul_f32 v[124:125], v[120:121], v[14:15] op_sel_hi:[0,1]
	v_exp_f32_e32 v124, v124
	v_exp_f32_e32 v125, v125
	v_pk_mul_f32 v[126:127], v[120:121], v[16:17] op_sel_hi:[0,1]
	v_exp_f32_e32 v126, v126
	v_exp_f32_e32 v127, v127
	v_fma_mix_f32 v122, v120, v30, 0 op_sel_hi:[0,1,0]
	v_pk_mul_f32 v[124:125], v[124:125], v[136:137]
	v_pk_fma_f32 v[124:125], v[122:123], s[36:37], v[124:125] op_sel_hi:[0, 1, 1]
	v_pk_fma_f32 v[70:71], s[72:73], v[124:125], 0 op_sel_hi:[1, 1, 0]
	v_pk_mul_f32 v[86:87], v[126:127], v[130:131]
	s_nop 0
	v_pk_fma_f32 v[126:127], v[122:123], s[38:39], v[86:87] op_sel_hi:[0, 1, 1]
	v_pk_mul_f32 v[72:73], v[120:121], v[10:11] op_sel_hi:[0,1]
	v_exp_f32_e32 v72, v72
	v_exp_f32_e32 v73, v73
	v_pk_mul_f32 v[86:87], v[120:121], v[12:13] op_sel_hi:[0,1]
	v_exp_f32_e32 v86, v86
	v_exp_f32_e32 v87, v87
	v_pk_mul_f32 v[72:73], v[72:73], v[132:133]
	v_pk_fma_f32 v[70:71], s[74:75], v[126:127], v[70:71]
	v_pk_fma_f32 v[128:129], v[122:123], s[40:41], v[72:73] op_sel_hi:[0, 1, 1]
	v_pk_mul_f32 v[72:73], v[86:87], v[110:111]
	v_pk_mul_f32 v[74:75], v[120:121], v[8:9] op_sel_hi:[0,1]
	v_pk_fma_f32 v[110:111], v[122:123], s[42:43], v[72:73] op_sel_hi:[0, 1, 1]
	v_pk_mul_f32 v[72:73], v[120:121], v[6:7] op_sel_hi:[0,1]
	v_exp_f32_e32 v72, v72
	v_exp_f32_e32 v73, v73
	v_exp_f32_e32 v74, v74
	v_exp_f32_e32 v75, v75
	v_pk_fma_f32 v[70:71], s[76:77], v[128:129], v[70:71]
	v_pk_mul_f32 v[72:73], v[72:73], v[112:113]
	v_pk_fma_f32 v[70:71], s[78:79], v[110:111], v[70:71]
	v_pk_fma_f32 v[112:113], v[122:123], s[44:45], v[72:73] op_sel_hi:[0, 1, 1]
	v_pk_mul_f32 v[72:73], v[74:75], v[114:115]
	v_pk_mul_f32 v[74:75], v[120:121], v[4:5] op_sel_hi:[0,1]
	v_pk_fma_f32 v[114:115], v[122:123], s[46:47], v[72:73] op_sel_hi:[0, 1, 1]
	v_pk_mul_f32 v[72:73], v[120:121], v[2:3] op_sel_hi:[0,1]
	v_exp_f32_e32 v72, v72
	v_exp_f32_e32 v73, v73
	v_exp_f32_e32 v74, v74
	v_exp_f32_e32 v75, v75
	v_pk_fma_f32 v[70:71], s[80:81], v[112:113], v[70:71]
	v_pk_mul_f32 v[72:73], v[72:73], v[116:117]
	v_pk_fma_f32 v[70:71], s[82:83], v[114:115], v[70:71]
	v_pk_fma_f32 v[116:117], v[122:123], s[48:49], v[72:73] op_sel_hi:[0, 1, 1]
	v_pk_mul_f32 v[72:73], v[74:75], v[118:119]
	v_pk_fma_f32 v[70:71], s[84:85], v[116:117], v[70:71]
	v_pk_fma_f32 v[118:119], v[122:123], s[50:51], v[72:73] op_sel_hi:[0, 1, 1]
	v_pk_fma_f32 v[70:71], s[86:87], v[118:119], v[70:71]
	s_waitcnt lgkmcnt(0)
	s_load_dwordx16 s[36:51], s[54:55], 0x900
	s_load_dwordx16 s[72:87], s[54:55], 0x940
	s_nop 0
	v_add_f32_e32 v69, v70, v71
	v_fma_mix_f32 v69, v1, v30, v69 op_sel_hi:[0,1,0]
	s_waitcnt vmcnt(3)
	v_fma_mixlo_f16 v69, v69, v34, 0 op_sel_hi:[0,1,0]
	ds_write_b16 v68, v69 offset:20736
	v_cvt_f32_f16_sdwa v38, v38 dst_sel:DWORD dst_unused:UNUSED_PAD src0_sel:WORD_1
	v_pk_mul_f32 v[122:123], v[38:39], v[14:15] op_sel_hi:[0,1]
	v_exp_f32_e32 v122, v122
	v_exp_f32_e32 v123, v123
	v_pk_mul_f32 v[130:131], v[38:39], v[16:17] op_sel_hi:[0,1]
	v_exp_f32_e32 v130, v130
	v_exp_f32_e32 v131, v131
	v_fma_mix_f32 v120, v38, v30, 0 op_sel:[0,1,0] op_sel_hi:[0,1,0]
	v_pk_mul_f32 v[122:123], v[122:123], v[124:125]
	v_pk_fma_f32 v[122:123], v[120:121], s[56:57], v[122:123] op_sel_hi:[0, 1, 1]
	v_pk_fma_f32 v[42:43], s[88:89], v[122:123], 0 op_sel_hi:[1, 1, 0]
	v_pk_mul_f32 v[58:59], v[130:131], v[126:127]
	s_nop 0
	v_pk_fma_f32 v[124:125], v[120:121], s[58:59], v[58:59] op_sel_hi:[0, 1, 1]
	v_pk_mul_f32 v[44:45], v[38:39], v[10:11] op_sel_hi:[0,1]
	v_exp_f32_e32 v44, v44
	v_exp_f32_e32 v45, v45
	v_pk_mul_f32 v[58:59], v[38:39], v[12:13] op_sel_hi:[0,1]
	v_exp_f32_e32 v58, v58
	v_exp_f32_e32 v59, v59
	v_pk_mul_f32 v[44:45], v[44:45], v[128:129]
	v_pk_fma_f32 v[42:43], s[90:91], v[124:125], v[42:43]
	v_pk_fma_f32 v[126:127], v[120:121], s[60:61], v[44:45] op_sel_hi:[0, 1, 1]
	v_pk_mul_f32 v[44:45], v[58:59], v[110:111]
	v_pk_mul_f32 v[46:47], v[38:39], v[8:9] op_sel_hi:[0,1]
	v_pk_fma_f32 v[110:111], v[120:121], s[62:63], v[44:45] op_sel_hi:[0, 1, 1]
	v_pk_mul_f32 v[44:45], v[38:39], v[6:7] op_sel_hi:[0,1]
	v_exp_f32_e32 v44, v44
	v_exp_f32_e32 v45, v45
	v_exp_f32_e32 v46, v46
	v_exp_f32_e32 v47, v47
	v_pk_fma_f32 v[42:43], s[92:93], v[126:127], v[42:43]
	v_pk_mul_f32 v[44:45], v[44:45], v[112:113]
	v_pk_fma_f32 v[42:43], s[94:95], v[110:111], v[42:43]
	v_pk_fma_f32 v[112:113], v[120:121], s[64:65], v[44:45] op_sel_hi:[0, 1, 1]
	v_pk_mul_f32 v[44:45], v[46:47], v[114:115]
	v_pk_mul_f32 v[46:47], v[38:39], v[4:5] op_sel_hi:[0,1]
	v_pk_fma_f32 v[114:115], v[120:121], s[66:67], v[44:45] op_sel_hi:[0, 1, 1]
	v_pk_mul_f32 v[44:45], v[38:39], v[2:3] op_sel_hi:[0,1]
	v_exp_f32_e32 v44, v44
	v_exp_f32_e32 v45, v45
	v_exp_f32_e32 v46, v46
	v_exp_f32_e32 v47, v47
	v_pk_fma_f32 v[42:43], s[96:97], v[112:113], v[42:43]
	v_pk_mul_f32 v[44:45], v[44:45], v[116:117]
	v_pk_fma_f32 v[42:43], s[98:99], v[114:115], v[42:43]
	v_pk_fma_f32 v[116:117], v[120:121], s[68:69], v[44:45] op_sel_hi:[0, 1, 1]
	v_pk_mul_f32 v[44:45], v[46:47], v[118:119]
	v_pk_fma_f32 v[42:43], s[20:21], v[116:117], v[42:43]
	v_pk_fma_f32 v[118:119], v[120:121], s[70:71], v[44:45] op_sel_hi:[0, 1, 1]
	v_pk_fma_f32 v[42:43], s[22:23], v[118:119], v[42:43]
	s_waitcnt lgkmcnt(0)
	s_load_dwordx16 s[56:71], s[54:55], 0x980
	s_load_dwordx8 s[88:95], s[54:55], 0x9c0
	s_load_dwordx4 s[96:99], s[54:55], 0x9e0
	s_load_dwordx4 s[20:23], s[54:55], 0x9f0
	s_nop 0
	v_add_f32_e32 v38, v42, v43
	v_fma_mix_f32 v30, v1, v30, v38 op_sel:[0,1,0] op_sel_hi:[0,1,0]
	v_fma_mixlo_f16 v30, v30, v34, 0 op_sel:[0,1,0] op_sel_hi:[0,1,0]
	ds_write_b16 v68, v30 offset:21776
	v_cvt_f32_f16_e32 v30, v39
	v_pk_mul_f32 v[120:121], v[30:31], v[14:15] op_sel_hi:[0,1]
	v_exp_f32_e32 v120, v120
	v_exp_f32_e32 v121, v121
	v_pk_mul_f32 v[128:129], v[30:31], v[16:17] op_sel_hi:[0,1]
	v_exp_f32_e32 v128, v128
	v_exp_f32_e32 v129, v129
	v_fma_mix_f32 v34, v30, v31, 0 op_sel_hi:[0,1,0]
	v_pk_mul_f32 v[120:121], v[120:121], v[122:123]
	v_pk_fma_f32 v[120:121], v[34:35], s[36:37], v[120:121] op_sel_hi:[0, 1, 1]
	v_pk_fma_f32 v[70:71], s[72:73], v[120:121], 0 op_sel_hi:[1, 1, 0]
	v_pk_mul_f32 v[86:87], v[128:129], v[124:125]
	s_nop 0
	v_pk_fma_f32 v[122:123], v[34:35], s[38:39], v[86:87] op_sel_hi:[0, 1, 1]
	v_pk_mul_f32 v[72:73], v[30:31], v[10:11] op_sel_hi:[0,1]
	v_exp_f32_e32 v72, v72
	v_exp_f32_e32 v73, v73
	v_pk_mul_f32 v[86:87], v[30:31], v[12:13] op_sel_hi:[0,1]
	v_exp_f32_e32 v86, v86
	v_exp_f32_e32 v87, v87
	v_pk_mul_f32 v[72:73], v[72:73], v[126:127]
	v_pk_fma_f32 v[70:71], s[74:75], v[122:123], v[70:71]
	v_pk_fma_f32 v[124:125], v[34:35], s[40:41], v[72:73] op_sel_hi:[0, 1, 1]
	v_pk_mul_f32 v[72:73], v[86:87], v[110:111]
	v_pk_mul_f32 v[74:75], v[30:31], v[8:9] op_sel_hi:[0,1]
	v_pk_fma_f32 v[110:111], v[34:35], s[42:43], v[72:73] op_sel_hi:[0, 1, 1]
	v_pk_mul_f32 v[72:73], v[30:31], v[6:7] op_sel_hi:[0,1]
	v_exp_f32_e32 v72, v72
	v_exp_f32_e32 v73, v73
	v_exp_f32_e32 v74, v74
	v_exp_f32_e32 v75, v75
	v_pk_fma_f32 v[70:71], s[76:77], v[124:125], v[70:71]
	v_pk_mul_f32 v[72:73], v[72:73], v[112:113]
	v_pk_fma_f32 v[70:71], s[78:79], v[110:111], v[70:71]
	v_pk_fma_f32 v[112:113], v[34:35], s[44:45], v[72:73] op_sel_hi:[0, 1, 1]
	v_pk_mul_f32 v[72:73], v[74:75], v[114:115]
	v_pk_mul_f32 v[74:75], v[30:31], v[4:5] op_sel_hi:[0,1]
	v_pk_fma_f32 v[114:115], v[34:35], s[46:47], v[72:73] op_sel_hi:[0, 1, 1]
	v_pk_mul_f32 v[72:73], v[30:31], v[2:3] op_sel_hi:[0,1]
	v_exp_f32_e32 v72, v72
	v_exp_f32_e32 v73, v73
	v_exp_f32_e32 v74, v74
	v_exp_f32_e32 v75, v75
	v_pk_fma_f32 v[70:71], s[80:81], v[112:113], v[70:71]
	v_pk_mul_f32 v[72:73], v[72:73], v[116:117]
	v_pk_fma_f32 v[70:71], s[82:83], v[114:115], v[70:71]
	v_pk_fma_f32 v[116:117], v[34:35], s[48:49], v[72:73] op_sel_hi:[0, 1, 1]
	v_pk_mul_f32 v[72:73], v[74:75], v[118:119]
	v_pk_fma_f32 v[70:71], s[84:85], v[116:117], v[70:71]
	v_pk_fma_f32 v[118:119], v[34:35], s[50:51], v[72:73] op_sel_hi:[0, 1, 1]
	v_pk_fma_f32 v[70:71], s[86:87], v[118:119], v[70:71]
	s_waitcnt lgkmcnt(0)
	s_load_dwordx16 s[36:51], s[54:55], 0xa00
	s_load_dwordx16 s[72:87], s[54:55], 0xa40
	s_nop 0
	v_add_f32_e32 v30, v70, v71
	v_fma_mix_f32 v30, v1, v31, v30 op_sel_hi:[0,1,0]
	v_fma_mixlo_f16 v30, v30, v35, 0 op_sel_hi:[0,1,0]
	ds_write_b16 v68, v30 offset:22816
	v_cvt_f32_f16_sdwa v30, v39 dst_sel:DWORD dst_unused:UNUSED_PAD src0_sel:WORD_1
	v_pk_mul_f32 v[38:39], v[30:31], v[14:15] op_sel_hi:[0,1]
	v_exp_f32_e32 v38, v38
	v_exp_f32_e32 v39, v39
	v_pk_mul_f32 v[126:127], v[30:31], v[16:17] op_sel_hi:[0,1]
	v_exp_f32_e32 v126, v126
	v_exp_f32_e32 v127, v127
	v_fma_mix_f32 v34, v30, v31, 0 op_sel:[0,1,0] op_sel_hi:[0,1,0]
	v_pk_mul_f32 v[38:39], v[38:39], v[120:121]
	v_pk_fma_f32 v[38:39], v[34:35], s[56:57], v[38:39] op_sel_hi:[0, 1, 1]
	v_pk_fma_f32 v[42:43], s[88:89], v[38:39], 0 op_sel_hi:[1, 1, 0]
	v_pk_mul_f32 v[58:59], v[126:127], v[122:123]
	s_nop 0
	v_pk_fma_f32 v[120:121], v[34:35], s[58:59], v[58:59] op_sel_hi:[0, 1, 1]
	v_pk_mul_f32 v[44:45], v[30:31], v[10:11] op_sel_hi:[0,1]
	v_exp_f32_e32 v44, v44
	v_exp_f32_e32 v45, v45
	v_pk_mul_f32 v[58:59], v[30:31], v[12:13] op_sel_hi:[0,1]
	v_exp_f32_e32 v58, v58
	v_exp_f32_e32 v59, v59
	v_pk_mul_f32 v[44:45], v[44:45], v[124:125]
	v_pk_fma_f32 v[42:43], s[90:91], v[120:121], v[42:43]
	v_pk_fma_f32 v[122:123], v[34:35], s[60:61], v[44:45] op_sel_hi:[0, 1, 1]
	v_pk_mul_f32 v[44:45], v[58:59], v[110:111]
	v_pk_mul_f32 v[46:47], v[30:31], v[8:9] op_sel_hi:[0,1]
	v_pk_fma_f32 v[110:111], v[34:35], s[62:63], v[44:45] op_sel_hi:[0, 1, 1]
	v_pk_mul_f32 v[44:45], v[30:31], v[6:7] op_sel_hi:[0,1]
	v_exp_f32_e32 v44, v44
	v_exp_f32_e32 v45, v45
	v_exp_f32_e32 v46, v46
	v_exp_f32_e32 v47, v47
	v_pk_fma_f32 v[42:43], s[92:93], v[122:123], v[42:43]
	v_pk_mul_f32 v[44:45], v[44:45], v[112:113]
	v_pk_fma_f32 v[42:43], s[94:95], v[110:111], v[42:43]
	v_pk_fma_f32 v[112:113], v[34:35], s[64:65], v[44:45] op_sel_hi:[0, 1, 1]
	v_pk_mul_f32 v[44:45], v[46:47], v[114:115]
	v_pk_mul_f32 v[46:47], v[30:31], v[4:5] op_sel_hi:[0,1]
	v_pk_fma_f32 v[114:115], v[34:35], s[66:67], v[44:45] op_sel_hi:[0, 1, 1]
	v_pk_mul_f32 v[44:45], v[30:31], v[2:3] op_sel_hi:[0,1]
	v_exp_f32_e32 v44, v44
	v_exp_f32_e32 v45, v45
	v_exp_f32_e32 v46, v46
	v_exp_f32_e32 v47, v47
	v_pk_fma_f32 v[42:43], s[96:97], v[112:113], v[42:43]
	v_pk_mul_f32 v[44:45], v[44:45], v[116:117]
	v_pk_fma_f32 v[42:43], s[98:99], v[114:115], v[42:43]
	v_pk_fma_f32 v[116:117], v[34:35], s[68:69], v[44:45] op_sel_hi:[0, 1, 1]
	v_pk_mul_f32 v[44:45], v[46:47], v[118:119]
	v_pk_fma_f32 v[42:43], s[20:21], v[116:117], v[42:43]
	v_pk_fma_f32 v[118:119], v[34:35], s[70:71], v[44:45] op_sel_hi:[0, 1, 1]
	v_pk_fma_f32 v[42:43], s[22:23], v[118:119], v[42:43]
	s_waitcnt lgkmcnt(0)
	s_load_dwordx16 s[56:71], s[54:55], 0xa80
	s_load_dwordx8 s[88:95], s[54:55], 0xac0
	s_load_dwordx4 s[96:99], s[54:55], 0xae0
	s_load_dwordx4 s[20:23], s[54:55], 0xaf0
	s_nop 0
	v_add_f32_e32 v30, v42, v43
	v_fma_mix_f32 v30, v1, v31, v30 op_sel:[0,1,0] op_sel_hi:[0,1,0]
	v_fma_mixlo_f16 v30, v30, v35, 0 op_sel:[0,1,0] op_sel_hi:[0,1,0]
	ds_write_b16 v68, v30 offset:23856
	v_cvt_f32_f16_e32 v30, v40
	v_pk_mul_f32 v[124:125], v[30:31], v[14:15] op_sel_hi:[0,1]
	v_exp_f32_e32 v124, v124
	v_exp_f32_e32 v125, v125
	v_pk_mul_f32 v[126:127], v[30:31], v[16:17] op_sel_hi:[0,1]
	v_exp_f32_e32 v126, v126
	v_exp_f32_e32 v127, v127
	v_fma_mix_f32 v34, v30, v32, 0 op_sel_hi:[0,1,0]
	v_pk_mul_f32 v[38:39], v[124:125], v[38:39]
	v_pk_fma_f32 v[38:39], v[34:35], s[36:37], v[38:39] op_sel_hi:[0, 1, 1]
	v_pk_fma_f32 v[70:71], s[72:73], v[38:39], 0 op_sel_hi:[1, 1, 0]
	v_pk_mul_f32 v[86:87], v[126:127], v[120:121]
	s_nop 0
	v_pk_fma_f32 v[120:121], v[34:35], s[38:39], v[86:87] op_sel_hi:[0, 1, 1]
	v_pk_mul_f32 v[72:73], v[30:31], v[10:11] op_sel_hi:[0,1]
	v_exp_f32_e32 v72, v72
	v_exp_f32_e32 v73, v73
	v_pk_mul_f32 v[86:87], v[30:31], v[12:13] op_sel_hi:[0,1]
	v_exp_f32_e32 v86, v86
	v_exp_f32_e32 v87, v87
	v_pk_mul_f32 v[72:73], v[72:73], v[122:123]
	v_pk_fma_f32 v[70:71], s[74:75], v[120:121], v[70:71]
	v_pk_fma_f32 v[122:123], v[34:35], s[40:41], v[72:73] op_sel_hi:[0, 1, 1]
	v_pk_mul_f32 v[72:73], v[86:87], v[110:111]
	v_pk_mul_f32 v[74:75], v[30:31], v[8:9] op_sel_hi:[0,1]
	v_pk_fma_f32 v[110:111], v[34:35], s[42:43], v[72:73] op_sel_hi:[0, 1, 1]
	v_pk_mul_f32 v[72:73], v[30:31], v[6:7] op_sel_hi:[0,1]
	v_exp_f32_e32 v72, v72
	v_exp_f32_e32 v73, v73
	v_exp_f32_e32 v74, v74
	v_exp_f32_e32 v75, v75
	v_pk_fma_f32 v[70:71], s[76:77], v[122:123], v[70:71]
	v_pk_mul_f32 v[72:73], v[72:73], v[112:113]
	v_pk_fma_f32 v[70:71], s[78:79], v[110:111], v[70:71]
	v_pk_fma_f32 v[112:113], v[34:35], s[44:45], v[72:73] op_sel_hi:[0, 1, 1]
	v_pk_mul_f32 v[72:73], v[74:75], v[114:115]
	v_pk_fma_f32 v[70:71], s[80:81], v[112:113], v[70:71]
	v_pk_fma_f32 v[114:115], v[34:35], s[46:47], v[72:73] op_sel_hi:[0, 1, 1]
	v_pk_mul_f32 v[72:73], v[30:31], v[2:3] op_sel_hi:[0,1]
	v_exp_f32_e32 v72, v72
	v_exp_f32_e32 v73, v73
	v_pk_mul_f32 v[30:31], v[30:31], v[4:5] op_sel_hi:[0,1]
	v_exp_f32_e32 v30, v30
	v_exp_f32_e32 v31, v31
	v_pk_mul_f32 v[72:73], v[72:73], v[116:117]
	v_pk_fma_f32 v[70:71], s[82:83], v[114:115], v[70:71]
	v_pk_fma_f32 v[116:117], v[34:35], s[48:49], v[72:73] op_sel_hi:[0, 1, 1]
	v_pk_mul_f32 v[30:31], v[30:31], v[118:119]
	v_pk_fma_f32 v[70:71], s[84:85], v[116:117], v[70:71]
	v_pk_fma_f32 v[30:31], v[34:35], s[50:51], v[30:31] op_sel_hi:[0, 1, 1]
	v_pk_fma_f32 v[34:35], s[86:87], v[30:31], v[70:71]
	s_waitcnt lgkmcnt(0)
	s_load_dwordx16 s[36:51], s[54:55], 0xb00
	s_load_dwordx16 s[72:87], s[54:55], 0xb40
	s_nop 0
	v_add_f32_e32 v34, v34, v35
	v_fma_mix_f32 v34, v1, v32, v34 op_sel_hi:[0,1,0]
	v_fma_mixlo_f16 v34, v34, v36, 0 op_sel_hi:[0,1,0]
	ds_write_b16 v68, v34 offset:24896
	v_cvt_f32_f16_sdwa v34, v40 dst_sel:DWORD dst_unused:UNUSED_PAD src0_sel:WORD_1
	v_pk_mul_f32 v[118:119], v[34:35], v[14:15] op_sel_hi:[0,1]
	v_exp_f32_e32 v118, v118
	v_exp_f32_e32 v119, v119
	v_pk_mul_f32 v[124:125], v[34:35], v[16:17] op_sel_hi:[0,1]
	v_exp_f32_e32 v124, v124
	v_exp_f32_e32 v125, v125
	v_fma_mix_f32 v40, v34, v32, 0 op_sel:[0,1,0] op_sel_hi:[0,1,0]
	v_pk_mul_f32 v[38:39], v[118:119], v[38:39]
	v_pk_fma_f32 v[38:39], v[40:41], s[56:57], v[38:39] op_sel_hi:[0, 1, 1]
	v_pk_fma_f32 v[42:43], s[88:89], v[38:39], 0 op_sel_hi:[1, 1, 0]
	v_pk_mul_f32 v[58:59], v[124:125], v[120:121]
	s_nop 0
	v_pk_fma_f32 v[118:119], v[40:41], s[58:59], v[58:59] op_sel_hi:[0, 1, 1]
	v_pk_mul_f32 v[44:45], v[34:35], v[10:11] op_sel_hi:[0,1]
	v_exp_f32_e32 v44, v44
	v_exp_f32_e32 v45, v45
	v_pk_mul_f32 v[58:59], v[34:35], v[12:13] op_sel_hi:[0,1]
	v_exp_f32_e32 v58, v58
	v_exp_f32_e32 v59, v59
	v_pk_mul_f32 v[44:45], v[44:45], v[122:123]
	v_pk_fma_f32 v[42:43], s[90:91], v[118:119], v[42:43]
	v_pk_fma_f32 v[120:121], v[40:41], s[60:61], v[44:45] op_sel_hi:[0, 1, 1]
	v_pk_mul_f32 v[44:45], v[58:59], v[110:111]
	v_pk_mul_f32 v[46:47], v[34:35], v[8:9] op_sel_hi:[0,1]
	v_pk_fma_f32 v[110:111], v[40:41], s[62:63], v[44:45] op_sel_hi:[0, 1, 1]
	v_pk_mul_f32 v[44:45], v[34:35], v[6:7] op_sel_hi:[0,1]
	v_exp_f32_e32 v44, v44
	v_exp_f32_e32 v45, v45
	v_exp_f32_e32 v46, v46
	v_exp_f32_e32 v47, v47
	v_pk_fma_f32 v[42:43], s[92:93], v[120:121], v[42:43]
	v_pk_mul_f32 v[44:45], v[44:45], v[112:113]
	v_pk_fma_f32 v[42:43], s[94:95], v[110:111], v[42:43]
	v_pk_fma_f32 v[112:113], v[40:41], s[64:65], v[44:45] op_sel_hi:[0, 1, 1]
	v_pk_mul_f32 v[44:45], v[46:47], v[114:115]
	v_pk_fma_f32 v[42:43], s[96:97], v[112:113], v[42:43]
	v_pk_fma_f32 v[114:115], v[40:41], s[66:67], v[44:45] op_sel_hi:[0, 1, 1]
	v_pk_mul_f32 v[44:45], v[34:35], v[2:3] op_sel_hi:[0,1]
	v_exp_f32_e32 v44, v44
	v_exp_f32_e32 v45, v45
	v_pk_mul_f32 v[34:35], v[34:35], v[4:5] op_sel_hi:[0,1]
	v_exp_f32_e32 v34, v34
	v_exp_f32_e32 v35, v35
	v_pk_mul_f32 v[44:45], v[44:45], v[116:117]
	v_pk_fma_f32 v[42:43], s[98:99], v[114:115], v[42:43]
	v_pk_fma_f32 v[116:117], v[40:41], s[68:69], v[44:45] op_sel_hi:[0, 1, 1]
	v_pk_mul_f32 v[30:31], v[34:35], v[30:31]
	v_pk_fma_f32 v[42:43], s[20:21], v[116:117], v[42:43]
	v_pk_fma_f32 v[30:31], v[40:41], s[70:71], v[30:31] op_sel_hi:[0, 1, 1]
	v_pk_fma_f32 v[34:35], s[22:23], v[30:31], v[42:43]
	s_waitcnt lgkmcnt(0)
	s_load_dwordx16 s[56:71], s[54:55], 0xb80
	s_load_dwordx8 s[88:95], s[54:55], 0xbc0
	s_load_dwordx4 s[96:99], s[54:55], 0xbe0
	s_load_dwordx4 s[20:23], s[54:55], 0xbf0
	s_nop 0
	v_add_f32_e32 v34, v34, v35
	v_fma_mix_f32 v32, v1, v32, v34 op_sel:[0,1,0] op_sel_hi:[0,1,0]
	v_fma_mixlo_f16 v32, v32, v36, 0 op_sel:[0,1,0] op_sel_hi:[0,1,0]
	ds_write_b16 v68, v32 offset:25936
	v_cvt_f32_f16_e32 v32, v41
	v_pk_mul_f32 v[122:123], v[32:33], v[14:15] op_sel_hi:[0,1]
	v_exp_f32_e32 v122, v122
	v_exp_f32_e32 v123, v123
	v_pk_mul_f32 v[124:125], v[32:33], v[16:17] op_sel_hi:[0,1]
	v_exp_f32_e32 v124, v124
	v_exp_f32_e32 v125, v125
	v_fma_mix_f32 v34, v32, v33, 0 op_sel_hi:[0,1,0]
	v_pk_mul_f32 v[38:39], v[122:123], v[38:39]
	v_pk_fma_f32 v[38:39], v[34:35], s[36:37], v[38:39] op_sel_hi:[0, 1, 1]
	v_pk_fma_f32 v[70:71], s[72:73], v[38:39], 0 op_sel_hi:[1, 1, 0]
	v_pk_mul_f32 v[86:87], v[124:125], v[118:119]
	s_nop 0
	v_pk_fma_f32 v[118:119], v[34:35], s[38:39], v[86:87] op_sel_hi:[0, 1, 1]
	v_pk_mul_f32 v[72:73], v[32:33], v[10:11] op_sel_hi:[0,1]
	v_exp_f32_e32 v72, v72
	v_exp_f32_e32 v73, v73
	v_pk_mul_f32 v[86:87], v[32:33], v[12:13] op_sel_hi:[0,1]
	v_exp_f32_e32 v86, v86
	v_exp_f32_e32 v87, v87
	v_pk_mul_f32 v[72:73], v[72:73], v[120:121]
	v_pk_fma_f32 v[70:71], s[74:75], v[118:119], v[70:71]
	v_pk_fma_f32 v[120:121], v[34:35], s[40:41], v[72:73] op_sel_hi:[0, 1, 1]
	v_pk_mul_f32 v[72:73], v[86:87], v[110:111]
	v_pk_mul_f32 v[74:75], v[32:33], v[8:9] op_sel_hi:[0,1]
	v_pk_fma_f32 v[110:111], v[34:35], s[42:43], v[72:73] op_sel_hi:[0, 1, 1]
	v_pk_mul_f32 v[72:73], v[32:33], v[6:7] op_sel_hi:[0,1]
	v_exp_f32_e32 v72, v72
	v_exp_f32_e32 v73, v73
	v_exp_f32_e32 v74, v74
	v_exp_f32_e32 v75, v75
	v_pk_fma_f32 v[70:71], s[76:77], v[120:121], v[70:71]
	v_pk_mul_f32 v[72:73], v[72:73], v[112:113]
	v_pk_fma_f32 v[70:71], s[78:79], v[110:111], v[70:71]
	v_pk_fma_f32 v[112:113], v[34:35], s[44:45], v[72:73] op_sel_hi:[0, 1, 1]
	v_pk_mul_f32 v[72:73], v[74:75], v[114:115]
	v_pk_mul_f32 v[74:75], v[32:33], v[4:5] op_sel_hi:[0,1]
	v_pk_fma_f32 v[114:115], v[34:35], s[46:47], v[72:73] op_sel_hi:[0, 1, 1]
	v_pk_mul_f32 v[72:73], v[32:33], v[2:3] op_sel_hi:[0,1]
	v_exp_f32_e32 v72, v72
	v_exp_f32_e32 v73, v73
	v_exp_f32_e32 v74, v74
	v_exp_f32_e32 v75, v75
	v_pk_fma_f32 v[70:71], s[80:81], v[112:113], v[70:71]
	v_pk_mul_f32 v[72:73], v[72:73], v[116:117]
	v_pk_fma_f32 v[70:71], s[82:83], v[114:115], v[70:71]
	v_pk_fma_f32 v[116:117], v[34:35], s[48:49], v[72:73] op_sel_hi:[0, 1, 1]
	v_pk_mul_f32 v[30:31], v[74:75], v[30:31]
	v_pk_fma_f32 v[70:71], s[84:85], v[116:117], v[70:71]
	v_pk_fma_f32 v[30:31], v[34:35], s[50:51], v[30:31] op_sel_hi:[0, 1, 1]
	v_pk_fma_f32 v[34:35], s[86:87], v[30:31], v[70:71]
	s_waitcnt lgkmcnt(0)
	s_load_dwordx16 s[36:51], s[54:55], 0xc00
	s_load_dwordx16 s[72:87], s[54:55], 0xc40
	s_nop 0
	v_add_f32_e32 v32, v34, v35
	v_fma_mix_f32 v32, v1, v33, v32 op_sel_hi:[0,1,0]
	v_fma_mixlo_f16 v32, v32, v37, 0 op_sel_hi:[0,1,0]
	ds_write_b16 v68, v32 offset:26976
	v_cvt_f32_f16_sdwa v32, v41 dst_sel:DWORD dst_unused:UNUSED_PAD src0_sel:WORD_1
	v_pk_mul_f32 v[40:41], v[32:33], v[14:15] op_sel_hi:[0,1]
	v_pk_mul_f32 v[122:123], v[32:33], v[16:17] op_sel_hi:[0,1]
	v_exp_f32_e32 v40, v40
	v_exp_f32_e32 v41, v41
	v_exp_f32_e32 v122, v122
	v_exp_f32_e32 v123, v123
	v_fma_mix_f32 v34, v32, v33, 0 op_sel:[0,1,0] op_sel_hi:[0,1,0]
	v_pk_mul_f32 v[38:39], v[40:41], v[38:39]
	v_pk_mul_f32 v[40:41], v[122:123], v[118:119]
	v_pk_fma_f32 v[118:119], v[34:35], s[58:59], v[40:41] op_sel_hi:[0, 1, 1]
	v_pk_mul_f32 v[40:41], v[32:33], v[10:11] op_sel_hi:[0,1]
	v_pk_fma_f32 v[124:125], v[34:35], s[56:57], v[38:39] op_sel_hi:[0, 1, 1]
	v_exp_f32_e32 v40, v40
	v_exp_f32_e32 v41, v41
	v_pk_mul_f32 v[42:43], v[32:33], v[12:13] op_sel_hi:[0,1]
	v_exp_f32_e32 v42, v42
	v_exp_f32_e32 v43, v43
	v_pk_fma_f32 v[38:39], s[88:89], v[124:125], 0 op_sel_hi:[1, 1, 0]
	v_pk_mul_f32 v[40:41], v[40:41], v[120:121]
	v_pk_fma_f32 v[38:39], s[90:91], v[118:119], v[38:39]
	v_pk_fma_f32 v[120:121], v[34:35], s[60:61], v[40:41] op_sel_hi:[0, 1, 1]
	v_pk_mul_f32 v[40:41], v[42:43], v[110:111]
	v_pk_fma_f32 v[38:39], s[92:93], v[120:121], v[38:39]
	v_pk_fma_f32 v[62:63], v[34:35], s[62:63], v[40:41] op_sel_hi:[0, 1, 1]
	v_pk_mul_f32 v[40:41], v[32:33], v[6:7] op_sel_hi:[0,1]
	v_exp_f32_e32 v40, v40
	v_exp_f32_e32 v41, v41
	v_pk_mul_f32 v[42:43], v[32:33], v[8:9] op_sel_hi:[0,1]
	v_exp_f32_e32 v42, v42
	v_exp_f32_e32 v43, v43
	v_pk_mul_f32 v[40:41], v[40:41], v[112:113]
	v_pk_fma_f32 v[38:39], s[94:95], v[62:63], v[38:39]
	v_pk_fma_f32 v[64:65], v[34:35], s[64:65], v[40:41] op_sel_hi:[0, 1, 1]
	v_pk_mul_f32 v[40:41], v[42:43], v[114:115]
	v_pk_fma_f32 v[38:39], s[96:97], v[64:65], v[38:39]
	v_pk_fma_f32 v[102:103], v[34:35], s[66:67], v[40:41] op_sel_hi:[0, 1, 1]
	v_pk_mul_f32 v[40:41], v[32:33], v[2:3] op_sel_hi:[0,1]
	v_exp_f32_e32 v40, v40
	v_exp_f32_e32 v41, v41
	v_pk_mul_f32 v[42:43], v[32:33], v[4:5] op_sel_hi:[0,1]
	v_exp_f32_e32 v42, v42
	v_exp_f32_e32 v43, v43
	v_pk_mul_f32 v[40:41], v[40:41], v[116:117]
	v_pk_fma_f32 v[38:39], s[98:99], v[102:103], v[38:39]
	v_pk_fma_f32 v[104:105], v[34:35], s[68:69], v[40:41] op_sel_hi:[0, 1, 1]
	v_pk_mul_f32 v[30:31], v[42:43], v[30:31]
	v_pk_fma_f32 v[38:39], s[20:21], v[104:105], v[38:39]
	v_pk_fma_f32 v[106:107], v[34:35], s[70:71], v[30:31] op_sel_hi:[0, 1, 1]
	v_pk_fma_f32 v[30:31], s[22:23], v[106:107], v[38:39]
	s_waitcnt lgkmcnt(0)
	s_load_dwordx16 s[56:71], s[54:55], 0xc80
	s_load_dwordx8 s[88:95], s[54:55], 0xcc0
	s_load_dwordx4 s[96:99], s[54:55], 0xce0
	s_load_dwordx4 s[20:23], s[54:55], 0xcf0
	s_nop 0
	v_add_f32_e32 v30, v30, v31
	v_fma_mix_f32 v30, v1, v33, v30 op_sel:[0,1,0] op_sel_hi:[0,1,0]
	v_fma_mixlo_f16 v30, v30, v37, 0 op_sel:[0,1,0] op_sel_hi:[0,1,0]
	ds_write_b16 v68, v30 offset:28016
	s_waitcnt vmcnt(2)
	v_cvt_f32_f16_e32 v108, v26
	s_waitcnt vmcnt(1)
	v_pk_mul_f32 v[112:113], v[108:109], v[14:15] op_sel_hi:[0,1]
	v_exp_f32_e32 v112, v112
	v_exp_f32_e32 v113, v113
	v_pk_mul_f32 v[114:115], v[108:109], v[16:17] op_sel_hi:[0,1]
	v_exp_f32_e32 v114, v114
	v_exp_f32_e32 v115, v115
	v_fma_mix_f32 v110, v108, v18, 0 op_sel_hi:[0,1,0]
	v_pk_mul_f32 v[112:113], v[112:113], v[124:125]
	v_pk_fma_f32 v[112:113], v[110:111], s[36:37], v[112:113] op_sel_hi:[0, 1, 1]
	v_pk_fma_f32 v[70:71], s[72:73], v[112:113], 0 op_sel_hi:[1, 1, 0]
	v_pk_mul_f32 v[86:87], v[114:115], v[118:119]
	s_nop 0
	v_pk_fma_f32 v[114:115], v[110:111], s[38:39], v[86:87] op_sel_hi:[0, 1, 1]
	v_pk_mul_f32 v[72:73], v[108:109], v[10:11] op_sel_hi:[0,1]
	v_exp_f32_e32 v72, v72
	v_exp_f32_e32 v73, v73
	v_pk_mul_f32 v[86:87], v[108:109], v[12:13] op_sel_hi:[0,1]
	v_exp_f32_e32 v86, v86
	v_exp_f32_e32 v87, v87
	v_pk_mul_f32 v[72:73], v[72:73], v[120:121]
	v_pk_fma_f32 v[70:71], s[74:75], v[114:115], v[70:71]
	v_pk_fma_f32 v[116:117], v[110:111], s[40:41], v[72:73] op_sel_hi:[0, 1, 1]
	v_pk_mul_f32 v[62:63], v[86:87], v[62:63]
	v_pk_fma_f32 v[70:71], s[76:77], v[116:117], v[70:71]
	v_pk_fma_f32 v[118:119], v[110:111], s[42:43], v[62:63] op_sel_hi:[0, 1, 1]
	v_pk_fma_f32 v[62:63], s[78:79], v[118:119], v[70:71]
	v_pk_mul_f32 v[70:71], v[108:109], v[6:7] op_sel_hi:[0,1]
	v_exp_f32_e32 v70, v70
	v_exp_f32_e32 v71, v71
	v_pk_mul_f32 v[72:73], v[108:109], v[8:9] op_sel_hi:[0,1]
	v_exp_f32_e32 v72, v72
	v_exp_f32_e32 v73, v73
	v_pk_mul_f32 v[64:65], v[70:71], v[64:65]
	v_pk_mul_f32 v[70:71], v[108:109], v[4:5] op_sel_hi:[0,1]
	v_pk_fma_f32 v[120:121], v[110:111], s[44:45], v[64:65] op_sel_hi:[0, 1, 1]
	v_pk_mul_f32 v[64:65], v[72:73], v[102:103]
	v_exp_f32_e32 v70, v70
	v_pk_fma_f32 v[102:103], v[110:111], s[46:47], v[64:65] op_sel_hi:[0, 1, 1]
	v_pk_mul_f32 v[64:65], v[108:109], v[2:3] op_sel_hi:[0,1]
	v_exp_f32_e32 v64, v64
	v_exp_f32_e32 v65, v65
	v_exp_f32_e32 v71, v71
	v_pk_fma_f32 v[62:63], s[80:81], v[120:121], v[62:63]
	v_pk_mul_f32 v[64:65], v[64:65], v[104:105]
	v_pk_fma_f32 v[62:63], s[82:83], v[102:103], v[62:63]
	v_pk_fma_f32 v[104:105], v[110:111], s[48:49], v[64:65] op_sel_hi:[0, 1, 1]
	v_pk_mul_f32 v[64:65], v[70:71], v[106:107]
	v_pk_fma_f32 v[62:63], s[84:85], v[104:105], v[62:63]
	v_pk_fma_f32 v[98:99], v[110:111], s[50:51], v[64:65] op_sel_hi:[0, 1, 1]
	v_pk_fma_f32 v[62:63], s[86:87], v[98:99], v[62:63]
	s_nop 0
	v_add_f32_e32 v62, v62, v63
	v_fma_mix_f32 v62, v1, v18, v62 op_sel_hi:[0,1,0]
	s_waitcnt vmcnt(0)
	v_fma_mixlo_f16 v62, v62, v22, 0 op_sel_hi:[0,1,0]
	ds_write_b16 v68, v62 offset:29056
	v_lshrrev_b32_e32 v196, 6, v0
	v_and_b32_e32 v197, 48, v0
	v_lshl_or_b32 v196, v196, 7, v197
	v_and_b32_e32 v197, 15, v0
	v_or_b32_e32 v197, s28, v197
	v_lshl_or_b32 v196, v197, 10, v196
	v_add_u32_e32 v197, 0x4000, v196
	global_load_dwordx4 v[180:183], v196, s[4:5]
	global_load_dwordx4 v[184:187], v196, s[4:5] offset:64
	global_load_dwordx4 v[188:191], v197, s[4:5]
	global_load_dwordx4 v[192:195], v197, s[4:5] offset:64
	v_and_b32_e32 v196, 63, v0
	v_lshlrev_b32_e32 v196, 4, v196
	global_load_dwordx4 v[204:207], v196, s[6:7]
	global_load_dwordx4 v[208:211], v196, s[8:9]
	s_waitcnt lgkmcnt(0)
	s_load_dwordx16 s[36:51], s[54:55], 0xd00
	s_load_dwordx16 s[72:87], s[54:55], 0xd40
	v_cvt_f32_f16_sdwa v26, v26 dst_sel:DWORD dst_unused:UNUSED_PAD src0_sel:WORD_1
	v_pk_mul_f32 v[106:107], v[26:27], v[14:15] op_sel_hi:[0,1]
	v_exp_f32_e32 v106, v106
	v_exp_f32_e32 v107, v107
	v_pk_mul_f32 v[108:109], v[26:27], v[16:17] op_sel_hi:[0,1]
	v_exp_f32_e32 v108, v108
	v_exp_f32_e32 v109, v109
	v_fma_mix_f32 v100, v26, v18, 0 op_sel:[0,1,0] op_sel_hi:[0,1,0]
	v_pk_mul_f32 v[106:107], v[106:107], v[112:113]
	v_pk_fma_f32 v[106:107], v[100:101], s[56:57], v[106:107] op_sel_hi:[0, 1, 1]
	v_pk_fma_f32 v[30:31], s[88:89], v[106:107], 0 op_sel_hi:[1, 1, 0]
	v_pk_mul_f32 v[46:47], v[108:109], v[114:115]
	s_nop 0
	v_pk_fma_f32 v[108:109], v[100:101], s[58:59], v[46:47] op_sel_hi:[0, 1, 1]
	v_pk_mul_f32 v[32:33], v[26:27], v[10:11] op_sel_hi:[0,1]
	v_exp_f32_e32 v32, v32
	v_exp_f32_e32 v33, v33
	v_pk_mul_f32 v[46:47], v[26:27], v[12:13] op_sel_hi:[0,1]
	v_exp_f32_e32 v46, v46
	v_exp_f32_e32 v47, v47
	v_pk_mul_f32 v[32:33], v[32:33], v[116:117]
	v_pk_fma_f32 v[30:31], s[90:91], v[108:109], v[30:31]
	v_pk_fma_f32 v[110:111], v[100:101], s[60:61], v[32:33] op_sel_hi:[0, 1, 1]
	v_pk_mul_f32 v[32:33], v[46:47], v[118:119]
	v_pk_mul_f32 v[34:35], v[26:27], v[8:9] op_sel_hi:[0,1]
	v_pk_fma_f32 v[112:113], v[100:101], s[62:63], v[32:33] op_sel_hi:[0, 1, 1]
	v_pk_mul_f32 v[32:33], v[26:27], v[6:7] op_sel_hi:[0,1]
	v_exp_f32_e32 v32, v32
	v_exp_f32_e32 v33, v33
	v_exp_f32_e32 v34, v34
	v_exp_f32_e32 v35, v35
	v_pk_fma_f32 v[30:31], s[92:93], v[110:111], v[30:31]
	v_pk_mul_f32 v[32:33], v[32:33], v[120:121]
	v_pk_fma_f32 v[30:31], s[94:95], v[112:113], v[30:31]
	v_pk_fma_f32 v[114:115], v[100:101], s[64:65], v[32:33] op_sel_hi:[0, 1, 1]
	v_pk_mul_f32 v[32:33], v[34:35], v[102:103]
	v_pk_mul_f32 v[34:35], v[26:27], v[4:5] op_sel_hi:[0,1]
	v_pk_fma_f32 v[102:103], v[100:101], s[66:67], v[32:33] op_sel_hi:[0, 1, 1]
	v_pk_mul_f32 v[32:33], v[26:27], v[2:3] op_sel_hi:[0,1]
	v_exp_f32_e32 v32, v32
	v_exp_f32_e32 v33, v33
	v_exp_f32_e32 v34, v34
	v_exp_f32_e32 v35, v35
	v_pk_fma_f32 v[30:31], s[96:97], v[114:115], v[30:31]
	v_pk_mul_f32 v[32:33], v[32:33], v[104:105]
	v_pk_fma_f32 v[30:31], s[98:99], v[102:103], v[30:31]
	v_pk_fma_f32 v[104:105], v[100:101], s[68:69], v[32:33] op_sel_hi:[0, 1, 1]
	v_pk_mul_f32 v[32:33], v[34:35], v[98:99]
	v_pk_fma_f32 v[30:31], s[20:21], v[104:105], v[30:31]
	v_pk_fma_f32 v[98:99], v[100:101], s[70:71], v[32:33] op_sel_hi:[0, 1, 1]
	v_pk_fma_f32 v[30:31], s[22:23], v[98:99], v[30:31]
	s_waitcnt lgkmcnt(0)
	s_load_dwordx16 s[56:71], s[54:55], 0xd80
	s_load_dwordx8 s[88:95], s[54:55], 0xdc0
	s_load_dwordx4 s[96:99], s[54:55], 0xde0
	s_load_dwordx4 s[20:23], s[54:55], 0xdf0
	s_nop 0
	v_add_f32_e32 v26, v30, v31
	v_fma_mix_f32 v18, v1, v18, v26 op_sel:[0,1,0] op_sel_hi:[0,1,0]
	v_fma_mixlo_f16 v18, v18, v22, 0 op_sel:[0,1,0] op_sel_hi:[0,1,0]
	ds_write_b16 v68, v18 offset:30096
	v_cvt_f32_f16_e32 v18, v27
	v_pk_mul_f32 v[100:101], v[18:19], v[14:15] op_sel_hi:[0,1]
	v_exp_f32_e32 v100, v100
	v_exp_f32_e32 v101, v101
	v_pk_mul_f32 v[116:117], v[18:19], v[16:17] op_sel_hi:[0,1]
	v_exp_f32_e32 v116, v116
	v_exp_f32_e32 v117, v117
	v_fma_mix_f32 v22, v18, v19, 0 op_sel_hi:[0,1,0]
	v_pk_mul_f32 v[100:101], v[100:101], v[106:107]
	v_pk_fma_f32 v[100:101], v[22:23], s[36:37], v[100:101] op_sel_hi:[0, 1, 1]
	v_pk_fma_f32 v[62:63], s[72:73], v[100:101], 0 op_sel_hi:[1, 1, 0]
	v_pk_mul_f32 v[82:83], v[116:117], v[108:109]
	s_nop 0
	v_pk_fma_f32 v[106:107], v[22:23], s[38:39], v[82:83] op_sel_hi:[0, 1, 1]
	v_pk_mul_f32 v[64:65], v[18:19], v[10:11] op_sel_hi:[0,1]
	v_exp_f32_e32 v64, v64
	v_exp_f32_e32 v65, v65
	v_pk_mul_f32 v[82:83], v[18:19], v[12:13] op_sel_hi:[0,1]
	v_exp_f32_e32 v82, v82
	v_exp_f32_e32 v83, v83
	v_pk_mul_f32 v[64:65], v[64:65], v[110:111]
	v_pk_fma_f32 v[62:63], s[74:75], v[106:107], v[62:63]
	v_pk_fma_f32 v[108:109], v[22:23], s[40:41], v[64:65] op_sel_hi:[0, 1, 1]
	v_pk_mul_f32 v[64:65], v[82:83], v[112:113]
	v_pk_mul_f32 v[70:71], v[18:19], v[8:9] op_sel_hi:[0,1]
	v_pk_fma_f32 v[110:111], v[22:23], s[42:43], v[64:65] op_sel_hi:[0, 1, 1]
	v_pk_mul_f32 v[64:65], v[18:19], v[6:7] op_sel_hi:[0,1]
	v_exp_f32_e32 v64, v64
	v_exp_f32_e32 v65, v65
	v_exp_f32_e32 v70, v70
	v_exp_f32_e32 v71, v71
	v_pk_fma_f32 v[62:63], s[76:77], v[108:109], v[62:63]
	v_pk_mul_f32 v[64:65], v[64:65], v[114:115]
	v_pk_fma_f32 v[62:63], s[78:79], v[110:111], v[62:63]
	v_pk_fma_f32 v[112:113], v[22:23], s[44:45], v[64:65] op_sel_hi:[0, 1, 1]
	v_pk_mul_f32 v[64:65], v[70:71], v[102:103]
	v_pk_mul_f32 v[70:71], v[18:19], v[4:5] op_sel_hi:[0,1]
	v_pk_fma_f32 v[102:103], v[22:23], s[46:47], v[64:65] op_sel_hi:[0, 1, 1]
	v_pk_mul_f32 v[64:65], v[18:19], v[2:3] op_sel_hi:[0,1]
	v_exp_f32_e32 v64, v64
	v_exp_f32_e32 v65, v65
	v_exp_f32_e32 v70, v70
	v_exp_f32_e32 v71, v71
	v_pk_fma_f32 v[62:63], s[80:81], v[112:113], v[62:63]
	v_pk_mul_f32 v[64:65], v[64:65], v[104:105]
	v_pk_fma_f32 v[62:63], s[82:83], v[102:103], v[62:63]
	v_pk_fma_f32 v[104:105], v[22:23], s[48:49], v[64:65] op_sel_hi:[0, 1, 1]
	v_pk_mul_f32 v[64:65], v[70:71], v[98:99]
	v_pk_fma_f32 v[62:63], s[84:85], v[104:105], v[62:63]
	v_pk_fma_f32 v[98:99], v[22:23], s[50:51], v[64:65] op_sel_hi:[0, 1, 1]
	v_pk_fma_f32 v[62:63], s[86:87], v[98:99], v[62:63]
	s_waitcnt lgkmcnt(0)
	s_load_dwordx16 s[36:51], s[54:55], 0xe00
	s_load_dwordx16 s[72:87], s[54:55], 0xe40
	s_nop 0
	v_add_f32_e32 v18, v62, v63
	v_fma_mix_f32 v18, v1, v19, v18 op_sel_hi:[0,1,0]
	v_fma_mixlo_f16 v18, v18, v23, 0 op_sel_hi:[0,1,0]
	ds_write_b16 v68, v18 offset:31136
	v_cvt_f32_f16_sdwa v18, v27 dst_sel:DWORD dst_unused:UNUSED_PAD src0_sel:WORD_1
	v_pk_mul_f32 v[26:27], v[18:19], v[14:15] op_sel_hi:[0,1]
	v_exp_f32_e32 v26, v26
	v_exp_f32_e32 v27, v27
	v_pk_mul_f32 v[114:115], v[18:19], v[16:17] op_sel_hi:[0,1]
	v_exp_f32_e32 v114, v114
	v_exp_f32_e32 v115, v115
	v_fma_mix_f32 v22, v18, v19, 0 op_sel:[0,1,0] op_sel_hi:[0,1,0]
	v_pk_mul_f32 v[26:27], v[26:27], v[100:101]
	v_pk_fma_f32 v[26:27], v[22:23], s[56:57], v[26:27] op_sel_hi:[0, 1, 1]
	v_pk_fma_f32 v[30:31], s[88:89], v[26:27], 0 op_sel_hi:[1, 1, 0]
	v_pk_mul_f32 v[46:47], v[114:115], v[106:107]
	s_nop 0
	v_pk_fma_f32 v[100:101], v[22:23], s[58:59], v[46:47] op_sel_hi:[0, 1, 1]
	v_pk_mul_f32 v[32:33], v[18:19], v[10:11] op_sel_hi:[0,1]
	v_exp_f32_e32 v32, v32
	v_exp_f32_e32 v33, v33
	v_pk_mul_f32 v[46:47], v[18:19], v[12:13] op_sel_hi:[0,1]
	v_exp_f32_e32 v46, v46
	v_exp_f32_e32 v47, v47
	v_pk_mul_f32 v[32:33], v[32:33], v[108:109]
	v_pk_fma_f32 v[30:31], s[90:91], v[100:101], v[30:31]
	v_pk_fma_f32 v[106:107], v[22:23], s[60:61], v[32:33] op_sel_hi:[0, 1, 1]
	v_pk_mul_f32 v[32:33], v[46:47], v[110:111]
	v_pk_mul_f32 v[34:35], v[18:19], v[8:9] op_sel_hi:[0,1]
	v_pk_fma_f32 v[108:109], v[22:23], s[62:63], v[32:33] op_sel_hi:[0, 1, 1]
	v_pk_mul_f32 v[32:33], v[18:19], v[6:7] op_sel_hi:[0,1]
	v_exp_f32_e32 v32, v32
	v_exp_f32_e32 v33, v33
	v_exp_f32_e32 v34, v34
	v_exp_f32_e32 v35, v35
	v_pk_fma_f32 v[30:31], s[92:93], v[106:107], v[30:31]
	v_pk_mul_f32 v[32:33], v[32:33], v[112:113]
	v_pk_fma_f32 v[30:31], s[94:95], v[108:109], v[30:31]
	v_pk_fma_f32 v[110:111], v[22:23], s[64:65], v[32:33] op_sel_hi:[0, 1, 1]
	v_pk_mul_f32 v[32:33], v[34:35], v[102:103]
	v_pk_mul_f32 v[34:35], v[18:19], v[4:5] op_sel_hi:[0,1]
	v_pk_fma_f32 v[102:103], v[22:23], s[66:67], v[32:33] op_sel_hi:[0, 1, 1]
	v_pk_mul_f32 v[32:33], v[18:19], v[2:3] op_sel_hi:[0,1]
	v_exp_f32_e32 v32, v32
	v_exp_f32_e32 v33, v33
	v_exp_f32_e32 v34, v34
	v_exp_f32_e32 v35, v35
	v_pk_fma_f32 v[30:31], s[96:97], v[110:111], v[30:31]
	v_pk_mul_f32 v[32:33], v[32:33], v[104:105]
	v_pk_fma_f32 v[30:31], s[98:99], v[102:103], v[30:31]
	v_pk_fma_f32 v[104:105], v[22:23], s[68:69], v[32:33] op_sel_hi:[0, 1, 1]
	v_pk_mul_f32 v[32:33], v[34:35], v[98:99]
	v_pk_fma_f32 v[30:31], s[20:21], v[104:105], v[30:31]
	v_pk_fma_f32 v[98:99], v[22:23], s[70:71], v[32:33] op_sel_hi:[0, 1, 1]
	v_pk_fma_f32 v[30:31], s[22:23], v[98:99], v[30:31]
	s_waitcnt lgkmcnt(0)
	s_load_dwordx16 s[56:71], s[54:55], 0xe80
	s_load_dwordx8 s[88:95], s[54:55], 0xec0
	s_load_dwordx4 s[96:99], s[54:55], 0xee0
	s_load_dwordx4 s[20:23], s[54:55], 0xef0
	s_nop 0
	v_add_f32_e32 v18, v30, v31
	v_fma_mix_f32 v18, v1, v19, v18 op_sel:[0,1,0] op_sel_hi:[0,1,0]
	v_fma_mixlo_f16 v18, v18, v23, 0 op_sel:[0,1,0] op_sel_hi:[0,1,0]
	ds_write_b16 v68, v18 offset:32176
	v_cvt_f32_f16_e32 v18, v28
	v_pk_mul_f32 v[112:113], v[18:19], v[14:15] op_sel_hi:[0,1]
	v_exp_f32_e32 v112, v112
	v_exp_f32_e32 v113, v113
	v_pk_mul_f32 v[114:115], v[18:19], v[16:17] op_sel_hi:[0,1]
	v_exp_f32_e32 v114, v114
	v_exp_f32_e32 v115, v115
	v_fma_mix_f32 v22, v18, v20, 0 op_sel_hi:[0,1,0]
	v_pk_mul_f32 v[26:27], v[112:113], v[26:27]
	v_pk_fma_f32 v[26:27], v[22:23], s[36:37], v[26:27] op_sel_hi:[0, 1, 1]
	v_pk_fma_f32 v[62:63], s[72:73], v[26:27], 0 op_sel_hi:[1, 1, 0]
	v_pk_mul_f32 v[82:83], v[114:115], v[100:101]
	s_nop 0
	v_pk_fma_f32 v[100:101], v[22:23], s[38:39], v[82:83] op_sel_hi:[0, 1, 1]
	v_pk_mul_f32 v[64:65], v[18:19], v[10:11] op_sel_hi:[0,1]
	v_exp_f32_e32 v64, v64
	v_exp_f32_e32 v65, v65
	v_pk_mul_f32 v[82:83], v[18:19], v[12:13] op_sel_hi:[0,1]
	v_exp_f32_e32 v82, v82
	v_exp_f32_e32 v83, v83
	v_pk_mul_f32 v[64:65], v[64:65], v[106:107]
	v_pk_fma_f32 v[62:63], s[74:75], v[100:101], v[62:63]
	v_pk_fma_f32 v[106:107], v[22:23], s[40:41], v[64:65] op_sel_hi:[0, 1, 1]
	v_pk_mul_f32 v[64:65], v[82:83], v[108:109]
	v_pk_mul_f32 v[70:71], v[18:19], v[8:9] op_sel_hi:[0,1]
	v_pk_fma_f32 v[108:109], v[22:23], s[42:43], v[64:65] op_sel_hi:[0, 1, 1]
	v_pk_mul_f32 v[64:65], v[18:19], v[6:7] op_sel_hi:[0,1]
	v_exp_f32_e32 v64, v64
	v_exp_f32_e32 v65, v65
	v_exp_f32_e32 v70, v70
	v_exp_f32_e32 v71, v71
	v_pk_fma_f32 v[62:63], s[76:77], v[106:107], v[62:63]
	v_pk_mul_f32 v[64:65], v[64:65], v[110:111]
	v_pk_fma_f32 v[62:63], s[78:79], v[108:109], v[62:63]
	v_pk_fma_f32 v[110:111], v[22:23], s[44:45], v[64:65] op_sel_hi:[0, 1, 1]
	v_pk_mul_f32 v[64:65], v[70:71], v[102:103]
	v_pk_fma_f32 v[62:63], s[80:81], v[110:111], v[62:63]
	v_pk_fma_f32 v[102:103], v[22:23], s[46:47], v[64:65] op_sel_hi:[0, 1, 1]
	v_pk_mul_f32 v[64:65], v[18:19], v[2:3] op_sel_hi:[0,1]
	v_exp_f32_e32 v64, v64
	v_exp_f32_e32 v65, v65
	v_pk_mul_f32 v[18:19], v[18:19], v[4:5] op_sel_hi:[0,1]
	v_exp_f32_e32 v18, v18
	v_exp_f32_e32 v19, v19
	v_pk_mul_f32 v[64:65], v[64:65], v[104:105]
	v_pk_fma_f32 v[62:63], s[82:83], v[102:103], v[62:63]
	v_pk_fma_f32 v[104:105], v[22:23], s[48:49], v[64:65] op_sel_hi:[0, 1, 1]
	v_pk_mul_f32 v[18:19], v[18:19], v[98:99]
	v_pk_fma_f32 v[62:63], s[84:85], v[104:105], v[62:63]
	v_pk_fma_f32 v[18:19], v[22:23], s[50:51], v[18:19] op_sel_hi:[0, 1, 1]
	v_pk_fma_f32 v[22:23], s[86:87], v[18:19], v[62:63]
	s_waitcnt lgkmcnt(0)
	s_load_dwordx16 s[36:51], s[54:55], 0xf00
	s_load_dwordx16 s[72:87], s[54:55], 0xf40
	s_nop 0
	v_add_f32_e32 v22, v22, v23
	v_fma_mix_f32 v22, v1, v20, v22 op_sel_hi:[0,1,0]
	v_fma_mixlo_f16 v22, v22, v24, 0 op_sel_hi:[0,1,0]
	ds_write_b16 v68, v22 offset:33216
	v_cvt_f32_f16_sdwa v22, v28 dst_sel:DWORD dst_unused:UNUSED_PAD src0_sel:WORD_1
	v_pk_mul_f32 v[98:99], v[22:23], v[14:15] op_sel_hi:[0,1]
	v_exp_f32_e32 v98, v98
	v_exp_f32_e32 v99, v99
	v_pk_mul_f32 v[112:113], v[22:23], v[16:17] op_sel_hi:[0,1]
	v_exp_f32_e32 v112, v112
	v_exp_f32_e32 v113, v113
	v_fma_mix_f32 v28, v22, v20, 0 op_sel:[0,1,0] op_sel_hi:[0,1,0]
	v_pk_mul_f32 v[26:27], v[98:99], v[26:27]
	v_pk_fma_f32 v[26:27], v[28:29], s[56:57], v[26:27] op_sel_hi:[0, 1, 1]
	v_pk_fma_f32 v[30:31], s[88:89], v[26:27], 0 op_sel_hi:[1, 1, 0]
	v_pk_mul_f32 v[46:47], v[112:113], v[100:101]
	s_nop 0
	v_pk_fma_f32 v[98:99], v[28:29], s[58:59], v[46:47] op_sel_hi:[0, 1, 1]
	v_pk_mul_f32 v[32:33], v[22:23], v[10:11] op_sel_hi:[0,1]
	v_exp_f32_e32 v32, v32
	v_exp_f32_e32 v33, v33
	v_pk_mul_f32 v[46:47], v[22:23], v[12:13] op_sel_hi:[0,1]
	v_exp_f32_e32 v46, v46
	v_exp_f32_e32 v47, v47
	v_pk_mul_f32 v[32:33], v[32:33], v[106:107]
	v_pk_fma_f32 v[30:31], s[90:91], v[98:99], v[30:31]
	v_pk_fma_f32 v[100:101], v[28:29], s[60:61], v[32:33] op_sel_hi:[0, 1, 1]
	v_pk_mul_f32 v[32:33], v[46:47], v[108:109]
	v_pk_mul_f32 v[34:35], v[22:23], v[8:9] op_sel_hi:[0,1]
	v_pk_fma_f32 v[106:107], v[28:29], s[62:63], v[32:33] op_sel_hi:[0, 1, 1]
	v_pk_mul_f32 v[32:33], v[22:23], v[6:7] op_sel_hi:[0,1]
	v_exp_f32_e32 v32, v32
	v_exp_f32_e32 v33, v33
	v_exp_f32_e32 v34, v34
	v_exp_f32_e32 v35, v35
	v_pk_fma_f32 v[30:31], s[92:93], v[100:101], v[30:31]
	v_pk_mul_f32 v[32:33], v[32:33], v[110:111]
	v_pk_fma_f32 v[30:31], s[94:95], v[106:107], v[30:31]
	v_pk_fma_f32 v[108:109], v[28:29], s[64:65], v[32:33] op_sel_hi:[0, 1, 1]
	v_pk_mul_f32 v[32:33], v[34:35], v[102:103]
	v_pk_fma_f32 v[30:31], s[96:97], v[108:109], v[30:31]
	v_pk_fma_f32 v[102:103], v[28:29], s[66:67], v[32:33] op_sel_hi:[0, 1, 1]
	v_pk_mul_f32 v[32:33], v[22:23], v[2:3] op_sel_hi:[0,1]
	v_exp_f32_e32 v32, v32
	v_exp_f32_e32 v33, v33
	v_pk_mul_f32 v[22:23], v[22:23], v[4:5] op_sel_hi:[0,1]
	v_exp_f32_e32 v22, v22
	v_exp_f32_e32 v23, v23
	v_pk_mul_f32 v[32:33], v[32:33], v[104:105]
	v_pk_fma_f32 v[30:31], s[98:99], v[102:103], v[30:31]
	v_pk_fma_f32 v[104:105], v[28:29], s[68:69], v[32:33] op_sel_hi:[0, 1, 1]
	v_pk_mul_f32 v[18:19], v[22:23], v[18:19]
	v_pk_fma_f32 v[30:31], s[20:21], v[104:105], v[30:31]
	v_pk_fma_f32 v[18:19], v[28:29], s[70:71], v[18:19] op_sel_hi:[0, 1, 1]
	v_pk_fma_f32 v[22:23], s[22:23], v[18:19], v[30:31]
	s_waitcnt lgkmcnt(0)
	s_load_dwordx16 s[56:71], s[54:55], 0xf80
	s_load_dwordx8 s[88:95], s[54:55], 0xfc0
	s_load_dwordx4 s[96:99], s[54:55], 0xfe0
	s_load_dwordx4 s[20:23], s[54:55], 0xff0
	s_nop 0
	v_add_f32_e32 v22, v22, v23
	v_fma_mix_f32 v20, v1, v20, v22 op_sel:[0,1,0] op_sel_hi:[0,1,0]
	v_fma_mixlo_f16 v20, v20, v24, 0 op_sel:[0,1,0] op_sel_hi:[0,1,0]
	ds_write_b16 v68, v20 offset:34256
	v_cvt_f32_f16_e32 v20, v29
	v_pk_mul_f32 v[110:111], v[20:21], v[14:15] op_sel_hi:[0,1]
	v_exp_f32_e32 v110, v110
	v_exp_f32_e32 v111, v111
	v_pk_mul_f32 v[112:113], v[20:21], v[16:17] op_sel_hi:[0,1]
	v_exp_f32_e32 v112, v112
	v_exp_f32_e32 v113, v113
	v_fma_mix_f32 v22, v20, v21, 0 op_sel_hi:[0,1,0]
	v_pk_mul_f32 v[26:27], v[110:111], v[26:27]
	v_pk_fma_f32 v[26:27], v[22:23], s[36:37], v[26:27] op_sel_hi:[0, 1, 1]
	v_pk_fma_f32 v[62:63], s[72:73], v[26:27], 0 op_sel_hi:[1, 1, 0]
	v_pk_mul_f32 v[82:83], v[112:113], v[98:99]
	s_nop 0
	v_pk_fma_f32 v[64:65], v[22:23], s[38:39], v[82:83] op_sel_hi:[0, 1, 1]
	v_pk_mul_f32 v[82:83], v[20:21], v[10:11] op_sel_hi:[0,1]
	v_pk_fma_f32 v[62:63], s[74:75], v[64:65], v[62:63]
	v_exp_f32_e32 v82, v82
	v_exp_f32_e32 v83, v83
	v_pk_mul_f32 v[84:85], v[20:21], v[12:13] op_sel_hi:[0,1]
	v_exp_f32_e32 v84, v84
	v_exp_f32_e32 v85, v85
	v_pk_mul_f32 v[82:83], v[82:83], v[100:101]
	s_nop 0
	v_pk_fma_f32 v[70:71], v[22:23], s[40:41], v[82:83] op_sel_hi:[0, 1, 1]
	v_pk_mul_f32 v[82:83], v[84:85], v[106:107]
	v_pk_mul_f32 v[84:85], v[20:21], v[8:9] op_sel_hi:[0,1]
	v_pk_fma_f32 v[72:73], v[22:23], s[42:43], v[82:83] op_sel_hi:[0, 1, 1]
	v_pk_mul_f32 v[82:83], v[20:21], v[6:7] op_sel_hi:[0,1]
	v_exp_f32_e32 v82, v82
	v_exp_f32_e32 v83, v83
	v_exp_f32_e32 v84, v84
	v_exp_f32_e32 v85, v85
	v_pk_fma_f32 v[62:63], s[76:77], v[70:71], v[62:63]
	v_pk_mul_f32 v[82:83], v[82:83], v[108:109]
	v_pk_fma_f32 v[62:63], s[78:79], v[72:73], v[62:63]
	v_pk_fma_f32 v[74:75], v[22:23], s[44:45], v[82:83] op_sel_hi:[0, 1, 1]
	v_pk_mul_f32 v[82:83], v[84:85], v[102:103]
	v_pk_mul_f32 v[84:85], v[20:21], v[4:5] op_sel_hi:[0,1]
	v_pk_fma_f32 v[76:77], v[22:23], s[46:47], v[82:83] op_sel_hi:[0, 1, 1]
	v_pk_mul_f32 v[82:83], v[20:21], v[2:3] op_sel_hi:[0,1]
	v_exp_f32_e32 v82, v82
	v_exp_f32_e32 v83, v83
	v_exp_f32_e32 v84, v84
	v_exp_f32_e32 v85, v85
	v_pk_fma_f32 v[62:63], s[80:81], v[74:75], v[62:63]
	v_pk_mul_f32 v[82:83], v[82:83], v[104:105]
	v_pk_fma_f32 v[62:63], s[82:83], v[76:77], v[62:63]
	v_pk_fma_f32 v[78:79], v[22:23], s[48:49], v[82:83] op_sel_hi:[0, 1, 1]
	v_pk_mul_f32 v[18:19], v[84:85], v[18:19]
	v_pk_fma_f32 v[62:63], s[84:85], v[78:79], v[62:63]
	v_pk_fma_f32 v[18:19], v[22:23], s[50:51], v[18:19] op_sel_hi:[0, 1, 1]
	v_pk_fma_f32 v[22:23], s[86:87], v[18:19], v[62:63]
	s_nop 0
	v_add_f32_e32 v20, v22, v23
	v_fma_mix_f32 v20, v1, v21, v20 op_sel_hi:[0,1,0]
	v_fma_mixlo_f16 v20, v20, v25, 0 op_sel_hi:[0,1,0]
	ds_write_b16 v68, v20 offset:35296
	s_waitcnt lgkmcnt(0)
	v_cvt_f32_f16_sdwa v20, v29 dst_sel:DWORD dst_unused:UNUSED_PAD src0_sel:WORD_1
	v_pk_mul_f32 v[14:15], v[20:21], v[14:15] op_sel_hi:[0,1]
	v_exp_f32_e32 v14, v14
	v_exp_f32_e32 v15, v15
	v_pk_mul_f32 v[16:17], v[20:21], v[16:17] op_sel_hi:[0,1]
	v_exp_f32_e32 v16, v16
	v_exp_f32_e32 v17, v17
	v_pk_mul_f32 v[10:11], v[20:21], v[10:11] op_sel_hi:[0,1]
	v_exp_f32_e32 v10, v10
	v_exp_f32_e32 v11, v11
	v_pk_mul_f32 v[12:13], v[20:21], v[12:13] op_sel_hi:[0,1]
	v_exp_f32_e32 v12, v12
	v_exp_f32_e32 v13, v13
	v_pk_mul_f32 v[6:7], v[20:21], v[6:7] op_sel_hi:[0,1]
	v_fma_mix_f32 v22, v20, v21, 0 op_sel:[0,1,0] op_sel_hi:[0,1,0]
	v_pk_mul_f32 v[14:15], v[14:15], v[26:27]
	v_exp_f32_e32 v6, v6
	v_exp_f32_e32 v7, v7
	v_pk_mul_f32 v[8:9], v[20:21], v[8:9] op_sel_hi:[0,1]
	v_pk_fma_f32 v[14:15], v[22:23], s[56:57], v[14:15] op_sel_hi:[0, 1, 1]
	v_pk_mul_f32 v[16:17], v[16:17], v[64:65]
	v_exp_f32_e32 v8, v8
	v_exp_f32_e32 v9, v9
	v_pk_mul_f32 v[2:3], v[20:21], v[2:3] op_sel_hi:[0,1]
	v_pk_fma_f32 v[14:15], s[88:89], v[14:15], 0 op_sel_hi:[1, 1, 0]
	v_pk_fma_f32 v[16:17], v[22:23], s[58:59], v[16:17] op_sel_hi:[0, 1, 1]
	v_pk_mul_f32 v[10:11], v[10:11], v[70:71]
	v_exp_f32_e32 v2, v2
	v_exp_f32_e32 v3, v3
	v_pk_mul_f32 v[4:5], v[20:21], v[4:5] op_sel_hi:[0,1]
	v_pk_fma_f32 v[14:15], s[90:91], v[16:17], v[14:15]
	v_pk_fma_f32 v[10:11], v[22:23], s[60:61], v[10:11] op_sel_hi:[0, 1, 1]
	v_pk_mul_f32 v[12:13], v[12:13], v[72:73]
	v_exp_f32_e32 v4, v4
	v_exp_f32_e32 v5, v5
	v_pk_fma_f32 v[10:11], s[92:93], v[10:11], v[14:15]
	v_pk_fma_f32 v[12:13], v[22:23], s[62:63], v[12:13] op_sel_hi:[0, 1, 1]
	v_pk_mul_f32 v[6:7], v[6:7], v[74:75]
	v_pk_fma_f32 v[10:11], s[94:95], v[12:13], v[10:11]
	v_pk_fma_f32 v[6:7], v[22:23], s[64:65], v[6:7] op_sel_hi:[0, 1, 1]
	v_pk_mul_f32 v[8:9], v[8:9], v[76:77]
	v_pk_fma_f32 v[6:7], s[96:97], v[6:7], v[10:11]
	v_pk_fma_f32 v[8:9], v[22:23], s[66:67], v[8:9] op_sel_hi:[0, 1, 1]
	v_pk_mul_f32 v[2:3], v[2:3], v[78:79]
	v_pk_fma_f32 v[6:7], s[98:99], v[8:9], v[6:7]
	v_pk_fma_f32 v[2:3], v[22:23], s[68:69], v[2:3] op_sel_hi:[0, 1, 1]
	v_pk_mul_f32 v[4:5], v[4:5], v[18:19]
	v_pk_fma_f32 v[2:3], s[20:21], v[2:3], v[6:7]
	v_pk_fma_f32 v[4:5], v[22:23], s[70:71], v[4:5] op_sel_hi:[0, 1, 1]
	v_pk_fma_f32 v[2:3], s[22:23], v[4:5], v[2:3]
	s_nop 0
	v_add_f32_e32 v2, v2, v3
	v_fma_mix_f32 v1, v1, v21, v2 op_sel:[0,1,0] op_sel_hi:[0,1,0]
	v_fma_mixlo_f16 v1, v1, v25, 0 op_sel:[0,1,0] op_sel_hi:[0,1,0]
	ds_write_b16 v68, v1 offset:36336
	v_lshlrev_b32_e32 v1, 9, v0
	v_and_b32_e32 v2, 0x38000, v1
	v_mov_b32_e32 v3, v67
	v_and_b32_e32 v1, 63, v0
	s_bfe_u32 s14, s2, 0x40003
	v_lshl_add_u64 v[2:3], s[18:19], 0, v[2:3]
	v_lshlrev_b32_e32 v58, 4, v1
	v_mov_b32_e32 v59, v67
	s_lshl_b32 s13, s14, 6
	v_lshl_add_u64 v[20:21], v[2:3], 0, v[58:59]
	s_lshl_b32 s26, s14, 10
	s_add_i32 s12, s13, 64
	v_lshl_add_u64 v[2:3], v[20:21], 0, s[26:27]
	s_and_b32 s15, s12, 0x3c0
	v_add_co_u32_e32 v4, vcc, s52, v2
	s_lshl_b32 s26, s15, 4
	s_lshl_b32 s12, s12, 4
	v_addc_co_u32_e32 v5, vcc, 0, v3, vcc
	global_load_dwordx4 v[28:31], v[2:3], off
	global_load_dwordx4 v[32:35], v[4:5], off
	v_lshl_add_u64 v[2:3], v[20:21], 0, s[26:27]
	s_or_b32 s26, s12, 0x4000
	s_add_i32 s12, s13, 0x80
	s_and_b32 s15, s12, 0x3c0
	v_lshl_add_u64 v[4:5], v[20:21], 0, s[26:27]
	s_lshl_b32 s26, s15, 4
	s_lshl_b32 s12, s12, 4
	global_load_dwordx4 v[36:39], v[2:3], off
	global_load_dwordx4 v[40:43], v[4:5], off
	v_lshl_add_u64 v[2:3], v[20:21], 0, s[26:27]
	s_or_b32 s26, s12, 0x4000
	s_add_i32 s12, s13, 0xc0
	s_and_b32 s15, s12, 0x3c0
	v_lshl_add_u64 v[4:5], v[20:21], 0, s[26:27]
	s_lshl_b32 s26, s15, 4
	s_lshl_b32 s12, s12, 4
	global_load_dwordx4 v[44:47], v[2:3], off
	global_load_dwordx4 v[48:51], v[4:5], off
	v_lshl_add_u64 v[2:3], v[20:21], 0, s[26:27]
	s_or_b32 s26, s12, 0x4000
	s_add_i32 s12, s13, 0x100
	s_and_b32 s15, s12, 0x3c0
	v_lshl_add_u64 v[4:5], v[20:21], 0, s[26:27]
	s_lshl_b32 s26, s15, 4
	s_lshl_b32 s12, s12, 4
	global_load_dwordx4 v[52:55], v[2:3], off
	global_load_dwordx4 v[60:63], v[4:5], off
	v_lshl_add_u64 v[2:3], v[20:21], 0, s[26:27]
	s_or_b32 s26, s12, 0x4000
	s_add_i32 s12, s13, 0x140
	s_and_b32 s15, s12, 0x3c0
	v_lshl_add_u64 v[4:5], v[20:21], 0, s[26:27]
	s_lshl_b32 s26, s15, 4
	s_lshl_b32 s12, s12, 4
	global_load_dwordx4 v[68:71], v[2:3], off
	global_load_dwordx4 v[72:75], v[4:5], off
	v_lshl_add_u64 v[2:3], v[20:21], 0, s[26:27]
	s_or_b32 s26, s12, 0x4000
	s_add_i32 s12, s13, 0x180
	s_and_b32 s15, s12, 0x3c0
	v_lshl_add_u64 v[4:5], v[20:21], 0, s[26:27]
	s_lshl_b32 s26, s15, 4
	s_lshl_b32 s12, s12, 4
	global_load_dwordx4 v[76:79], v[2:3], off
	global_load_dwordx4 v[82:85], v[4:5], off
	v_lshl_add_u64 v[2:3], v[20:21], 0, s[26:27]
	s_or_b32 s26, s12, 0x4000
	s_add_i32 s12, s13, 0x1c0
	s_and_b32 s15, s12, 0x3c0
	v_lshl_add_u64 v[4:5], v[20:21], 0, s[26:27]
	s_lshl_b32 s26, s15, 4
	s_lshl_b32 s12, s12, 4
	v_lshl_add_u64 v[18:19], v[20:21], 0, s[26:27]
	s_or_b32 s26, s12, 0x4000
	s_xor_b32 s15, s13, 0x200
	v_lshl_add_u64 v[22:23], v[20:21], 0, s[26:27]
	s_lshl_b32 s26, s15, 4
	global_load_dwordx4 v[14:17], v[2:3], off
	global_load_dwordx4 v[10:13], v[4:5], off
	global_load_dwordx4 v[6:9], v[18:19], off
	s_nop 0
	global_load_dwordx4 v[2:5], v[22:23], off
	v_lshl_add_u64 v[18:19], v[20:21], 0, s[26:27]
	v_add_co_u32_e32 v22, vcc, s52, v18
	s_waitcnt lgkmcnt(0)
	s_barrier
	v_addc_co_u32_e32 v23, vcc, 0, v19, vcc
	global_load_dwordx4 v[86:89], v[18:19], off
	global_load_dwordx4 v[90:93], v[22:23], off
	v_lshrrev_b32_e32 v118, 6, v0
	v_lshlrev_b32_e32 v22, 7, v118
	v_mov_b32_e32 v23, v67
	v_and_b32_e32 v81, 15, v0
	v_lshl_add_u64 v[24:25], s[4:5], 0, v[22:23]
	v_and_b32_e32 v18, 48, v0
	v_mov_b32_e32 v19, v67
	s_movk_i32 s12, 0x410
	v_lshl_add_u64 v[56:57], v[24:25], 0, v[18:19]
	v_mad_u32_u24 v19, v81, s12, v18
	v_add_u32_e32 v23, s13, v19
	ds_read_b128 v[94:97], v23 offset:4096
	ds_read_b128 v[98:101], v23 offset:20736
	v_or_b32_e32 v26, s28, v81
	v_mov_b32_e32 v27, v67
	v_lshlrev_b64 v[24:25], 10, v[26:27]
	v_or_b32_e32 v26, 16, v26
	v_lshlrev_b64 v[26:27], 10, v[26:27]
	v_lshrrev_b32_e32 v23, 1, v0
	v_lshl_add_u64 v[24:25], v[56:57], 0, v[24:25]
	v_lshl_add_u64 v[26:27], v[56:57], 0, v[26:27]
	v_and_b32_e32 v80, 24, v23
	s_lshl_b32 s14, s14, 5
	s_setprio 1
	s_waitcnt vmcnt(17) lgkmcnt(1)
	v_mfma_f32_16x16x32_f16 v[102:105], v[28:31], v[94:97], 0
	s_waitcnt lgkmcnt(0)
	v_mfma_f32_16x16x32_f16 v[28:31], v[28:31], v[98:101], 0
	s_waitcnt vmcnt(16)
	v_mfma_f32_16x16x32_f16 v[94:97], v[32:35], v[94:97], 0
	v_mfma_f32_16x16x32_f16 v[32:35], v[32:35], v[98:101], 0
	s_setprio 0
	s_add_i32 s16, s13, 0x240
	s_and_b32 s17, s16, 0x3c0
	s_lshl_b32 s26, s17, 4
	s_lshl_b32 s16, s16, 4
	v_lshl_add_u64 v[56:57], v[20:21], 0, s[26:27]
	s_or_b32 s26, s16, 0x4000
	v_lshl_add_u64 v[64:65], v[20:21], 0, s[26:27]
	global_load_dwordx4 v[98:101], v[56:57], off
	global_load_dwordx4 v[106:109], v[64:65], off
	s_add_i32 s16, s14, 32
	s_and_b32 s16, s16, 0x1e0
	v_lshl_add_u32 v23, s16, 1, v19
	ds_read_b128 v[110:113], v23 offset:4096
	ds_read_b128 v[114:117], v23 offset:20736
	s_setprio 1
	s_waitcnt vmcnt(17) lgkmcnt(1)
	v_mfma_f32_16x16x32_f16 v[102:105], v[36:39], v[110:113], v[102:105]
	s_waitcnt lgkmcnt(0)
	v_mfma_f32_16x16x32_f16 v[28:31], v[36:39], v[114:117], v[28:31]
	s_waitcnt vmcnt(16)
	v_mfma_f32_16x16x32_f16 v[36:39], v[40:43], v[110:113], v[94:97]
	v_mfma_f32_16x16x32_f16 v[32:35], v[40:43], v[114:117], v[32:35]
	s_setprio 0
	s_add_i32 s16, s13, 0x280
	s_and_b32 s17, s16, 0x3c0
	s_lshl_b32 s26, s17, 4
	s_lshl_b32 s16, s16, 4
	v_lshl_add_u64 v[56:57], v[20:21], 0, s[26:27]
	s_or_b32 s26, s16, 0x4000
	v_lshl_add_u64 v[64:65], v[20:21], 0, s[26:27]
	global_load_dwordx4 v[40:43], v[56:57], off
	global_load_dwordx4 v[94:97], v[64:65], off
	s_add_i32 s16, s14, 64
	s_and_b32 s16, s16, 0x1e0
	v_lshl_add_u32 v23, s16, 1, v19
	ds_read_b128 v[110:113], v23 offset:4096
	ds_read_b128 v[114:117], v23 offset:20736
	s_setprio 1
	s_waitcnt vmcnt(17) lgkmcnt(1)
	v_mfma_f32_16x16x32_f16 v[102:105], v[44:47], v[110:113], v[102:105]
	s_waitcnt lgkmcnt(0)
	v_mfma_f32_16x16x32_f16 v[28:31], v[44:47], v[114:117], v[28:31]
	s_waitcnt vmcnt(16)
	v_mfma_f32_16x16x32_f16 v[36:39], v[48:51], v[110:113], v[36:39]
	v_mfma_f32_16x16x32_f16 v[32:35], v[48:51], v[114:117], v[32:35]
	s_setprio 0
	s_add_i32 s16, s13, 0x2c0
	s_and_b32 s17, s16, 0x3c0
	s_lshl_b32 s26, s17, 4
	s_lshl_b32 s16, s16, 4
	v_lshl_add_u64 v[56:57], v[20:21], 0, s[26:27]
	s_or_b32 s26, s16, 0x4000
	v_lshl_add_u64 v[64:65], v[20:21], 0, s[26:27]
	global_load_dwordx4 v[44:47], v[56:57], off
	global_load_dwordx4 v[48:51], v[64:65], off
	s_add_i32 s16, s14, 0x60
	s_and_b32 s16, s16, 0x1e0
	v_lshl_add_u32 v23, s16, 1, v19
	ds_read_b128 v[110:113], v23 offset:4096
	ds_read_b128 v[114:117], v23 offset:20736
	s_setprio 1
	s_waitcnt vmcnt(17) lgkmcnt(1)
	v_mfma_f32_16x16x32_f16 v[102:105], v[52:55], v[110:113], v[102:105]
	s_waitcnt lgkmcnt(0)
	v_mfma_f32_16x16x32_f16 v[28:31], v[52:55], v[114:117], v[28:31]
	s_waitcnt vmcnt(16)
	v_mfma_f32_16x16x32_f16 v[36:39], v[60:63], v[110:113], v[36:39]
	v_mfma_f32_16x16x32_f16 v[32:35], v[60:63], v[114:117], v[32:35]
	s_setprio 0
	s_add_i32 s16, s13, 0x300
	s_and_b32 s17, s16, 0x3c0
	s_lshl_b32 s26, s17, 4
	s_lshl_b32 s16, s16, 4
	v_lshl_add_u64 v[56:57], v[20:21], 0, s[26:27]
	s_or_b32 s26, s16, 0x4000
	v_lshl_add_u64 v[64:65], v[20:21], 0, s[26:27]
	global_load_dwordx4 v[52:55], v[56:57], off
	global_load_dwordx4 v[60:63], v[64:65], off
	s_add_i32 s16, s14, 0x80
	s_and_b32 s16, s16, 0x1e0
	v_lshl_add_u32 v23, s16, 1, v19
	ds_read_b128 v[110:113], v23 offset:4096
	ds_read_b128 v[114:117], v23 offset:20736
	s_setprio 1
	s_waitcnt vmcnt(17) lgkmcnt(1)
	v_mfma_f32_16x16x32_f16 v[102:105], v[68:71], v[110:113], v[102:105]
	s_waitcnt lgkmcnt(0)
	v_mfma_f32_16x16x32_f16 v[28:31], v[68:71], v[114:117], v[28:31]
	s_waitcnt vmcnt(16)
	v_mfma_f32_16x16x32_f16 v[36:39], v[72:75], v[110:113], v[36:39]
	v_mfma_f32_16x16x32_f16 v[32:35], v[72:75], v[114:117], v[32:35]
	s_setprio 0
	s_add_i32 s16, s13, 0x340
	s_and_b32 s17, s16, 0x3c0
	s_lshl_b32 s26, s17, 4
	s_lshl_b32 s16, s16, 4
	v_lshl_add_u64 v[56:57], v[20:21], 0, s[26:27]
	s_or_b32 s26, s16, 0x4000
	v_lshl_add_u64 v[64:65], v[20:21], 0, s[26:27]
	global_load_dwordx4 v[68:71], v[56:57], off
	global_load_dwordx4 v[72:75], v[64:65], off
	s_add_i32 s16, s14, 0xa0
	s_and_b32 s16, s16, 0x1e0
	v_lshl_add_u32 v23, s16, 1, v19
	ds_read_b128 v[110:113], v23 offset:4096
	ds_read_b128 v[114:117], v23 offset:20736
	s_setprio 1
	s_waitcnt vmcnt(17) lgkmcnt(1)
	v_mfma_f32_16x16x32_f16 v[102:105], v[76:79], v[110:113], v[102:105]
	s_waitcnt lgkmcnt(0)
	v_mfma_f32_16x16x32_f16 v[28:31], v[76:79], v[114:117], v[28:31]
	s_waitcnt vmcnt(16)
	v_mfma_f32_16x16x32_f16 v[36:39], v[82:85], v[110:113], v[36:39]
	v_mfma_f32_16x16x32_f16 v[32:35], v[82:85], v[114:117], v[32:35]
	s_setprio 0
	s_add_i32 s16, s13, 0x380
	s_and_b32 s17, s16, 0x3c0
	s_lshl_b32 s26, s17, 4
	s_lshl_b32 s16, s16, 4
	v_lshl_add_u64 v[56:57], v[20:21], 0, s[26:27]
	s_or_b32 s26, s16, 0x4000
	v_lshl_add_u64 v[64:65], v[20:21], 0, s[26:27]
	global_load_dwordx4 v[76:79], v[56:57], off
	global_load_dwordx4 v[82:85], v[64:65], off
	s_add_i32 s16, s14, 0xc0
	s_and_b32 s16, s16, 0x1e0
	v_lshl_add_u32 v23, s16, 1, v19
	ds_read_b128 v[110:113], v23 offset:4096
	ds_read_b128 v[114:117], v23 offset:20736
	s_setprio 1
	s_waitcnt vmcnt(17) lgkmcnt(1)
	v_mfma_f32_16x16x32_f16 v[102:105], v[14:17], v[110:113], v[102:105]
	s_waitcnt lgkmcnt(0)
	v_mfma_f32_16x16x32_f16 v[14:17], v[14:17], v[114:117], v[28:31]
	s_waitcnt vmcnt(16)
	v_mfma_f32_16x16x32_f16 v[28:31], v[10:13], v[110:113], v[36:39]
	v_mfma_f32_16x16x32_f16 v[10:13], v[10:13], v[114:117], v[32:35]
	s_setprio 0
	s_addk_i32 s13, 0x3c0
	s_and_b32 s16, s13, 0x3c0
	s_lshl_b32 s26, s16, 4
	s_lshl_b32 s13, s13, 4
	v_lshl_add_u64 v[56:57], v[20:21], 0, s[26:27]
	s_or_b32 s26, s13, 0x4000
	v_lshl_add_u64 v[20:21], v[20:21], 0, s[26:27]
	global_load_dwordx4 v[32:35], v[56:57], off
	global_load_dwordx4 v[36:39], v[20:21], off
	s_add_i32 s13, s14, 0xe0
	s_and_b32 s13, s13, 0x1e0
	v_lshl_add_u32 v20, s13, 1, v19
	ds_read_b128 v[110:113], v20 offset:4096
	ds_read_b128 v[114:117], v20 offset:20736
	s_setprio 1
	s_waitcnt vmcnt(17) lgkmcnt(1)
	v_mfma_f32_16x16x32_f16 v[102:105], v[6:9], v[110:113], v[102:105]
	s_waitcnt lgkmcnt(0)
	v_mfma_f32_16x16x32_f16 v[6:9], v[6:9], v[114:117], v[14:17]
	s_waitcnt vmcnt(16)
	v_mfma_f32_16x16x32_f16 v[14:17], v[2:5], v[110:113], v[28:31]
	v_mfma_f32_16x16x32_f16 v[2:5], v[2:5], v[114:117], v[10:13]
	s_setprio 0
	v_add_u32_e32 v20, s15, v19
	s_nop 0
	ds_read_b128 v[10:13], v20 offset:4096
	ds_read_b128 v[28:31], v20 offset:20736
	s_setprio 1
	s_waitcnt vmcnt(15) lgkmcnt(1)
	v_mfma_f32_16x16x32_f16 v[102:105], v[86:89], v[10:13], v[102:105]
	s_waitcnt lgkmcnt(0)
	v_mfma_f32_16x16x32_f16 v[6:9], v[86:89], v[28:31], v[6:9]
	s_waitcnt vmcnt(14)
	v_mfma_f32_16x16x32_f16 v[10:13], v[90:93], v[10:13], v[14:17]
	v_mfma_f32_16x16x32_f16 v[2:5], v[90:93], v[28:31], v[2:5]
	s_setprio 0
	s_add_i32 s13, s14, 0x120
	s_and_b32 s13, s13, 0x1e0
	v_lshl_add_u32 v20, s13, 1, v19
	ds_read_b128 v[14:17], v20 offset:4096
	ds_read_b128 v[28:31], v20 offset:20736
	s_setprio 1
	s_waitcnt vmcnt(13) lgkmcnt(1)
	v_mfma_f32_16x16x32_f16 v[86:89], v[98:101], v[14:17], v[102:105]
	s_waitcnt lgkmcnt(0)
	v_mfma_f32_16x16x32_f16 v[6:9], v[98:101], v[28:31], v[6:9]
	s_waitcnt vmcnt(12)
	v_mfma_f32_16x16x32_f16 v[10:13], v[106:109], v[14:17], v[10:13]
	v_mfma_f32_16x16x32_f16 v[2:5], v[106:109], v[28:31], v[2:5]
	s_setprio 0
	s_add_i32 s13, s14, 0x140
	s_and_b32 s13, s13, 0x1e0
	v_lshl_add_u32 v20, s13, 1, v19
	ds_read_b128 v[14:17], v20 offset:4096
	ds_read_b128 v[28:31], v20 offset:20736
	s_setprio 1
	s_waitcnt vmcnt(11) lgkmcnt(1)
	v_mfma_f32_16x16x32_f16 v[86:89], v[40:43], v[14:17], v[86:89]
	s_waitcnt lgkmcnt(0)
	v_mfma_f32_16x16x32_f16 v[6:9], v[40:43], v[28:31], v[6:9]
	s_waitcnt vmcnt(10)
	v_mfma_f32_16x16x32_f16 v[10:13], v[94:97], v[14:17], v[10:13]
	v_mfma_f32_16x16x32_f16 v[2:5], v[94:97], v[28:31], v[2:5]
	s_setprio 0
	s_add_i32 s13, s14, 0x160
	s_and_b32 s13, s13, 0x1e0
	v_lshl_add_u32 v20, s13, 1, v19
	ds_read_b128 v[14:17], v20 offset:4096
	ds_read_b128 v[28:31], v20 offset:20736
	s_setprio 1
	s_waitcnt vmcnt(9) lgkmcnt(1)
	v_mfma_f32_16x16x32_f16 v[40:43], v[44:47], v[14:17], v[86:89]
	s_waitcnt lgkmcnt(0)
	v_mfma_f32_16x16x32_f16 v[6:9], v[44:47], v[28:31], v[6:9]
	s_waitcnt vmcnt(8)
	v_mfma_f32_16x16x32_f16 v[10:13], v[48:51], v[14:17], v[10:13]
	v_mfma_f32_16x16x32_f16 v[2:5], v[48:51], v[28:31], v[2:5]
	s_setprio 0
	s_add_i32 s13, s14, 0x180
	s_and_b32 s13, s13, 0x1e0
	v_lshl_add_u32 v20, s13, 1, v19
	ds_read_b128 v[14:17], v20 offset:4096
	ds_read_b128 v[28:31], v20 offset:20736
	s_setprio 1
	s_waitcnt vmcnt(7) lgkmcnt(1)
	v_mfma_f32_16x16x32_f16 v[40:43], v[52:55], v[14:17], v[40:43]
	s_waitcnt lgkmcnt(0)
	v_mfma_f32_16x16x32_f16 v[6:9], v[52:55], v[28:31], v[6:9]
	s_waitcnt vmcnt(6)
	v_mfma_f32_16x16x32_f16 v[10:13], v[60:63], v[14:17], v[10:13]
	v_mfma_f32_16x16x32_f16 v[2:5], v[60:63], v[28:31], v[2:5]
	s_setprio 0
	s_add_i32 s13, s14, 0x1a0
	s_and_b32 s13, s13, 0x1e0
	v_lshl_add_u32 v20, s13, 1, v19
	ds_read_b128 v[14:17], v20 offset:4096
	ds_read_b128 v[28:31], v20 offset:20736
	s_setprio 1
	s_waitcnt vmcnt(5) lgkmcnt(1)
	v_mfma_f32_16x16x32_f16 v[40:43], v[68:71], v[14:17], v[40:43]
	s_waitcnt lgkmcnt(0)
	v_mfma_f32_16x16x32_f16 v[6:9], v[68:71], v[28:31], v[6:9]
	s_waitcnt vmcnt(4)
	v_mfma_f32_16x16x32_f16 v[10:13], v[72:75], v[14:17], v[10:13]
	v_mfma_f32_16x16x32_f16 v[2:5], v[72:75], v[28:31], v[2:5]
	s_setprio 0
	s_add_i32 s13, s14, 0x1c0
	s_and_b32 s13, s13, 0x1e0
	v_lshl_add_u32 v20, s13, 1, v19
	ds_read_b128 v[14:17], v20 offset:4096
	ds_read_b128 v[28:31], v20 offset:20736
	s_setprio 1
	s_waitcnt vmcnt(3) lgkmcnt(1)
	v_mfma_f32_16x16x32_f16 v[40:43], v[76:79], v[14:17], v[40:43]
	s_waitcnt lgkmcnt(0)
	v_mfma_f32_16x16x32_f16 v[6:9], v[76:79], v[28:31], v[6:9]
	s_waitcnt vmcnt(2)
	v_mfma_f32_16x16x32_f16 v[10:13], v[82:85], v[14:17], v[10:13]
	v_mfma_f32_16x16x32_f16 v[2:5], v[82:85], v[28:31], v[2:5]
	s_setprio 0
	s_addk_i32 s14, 0x1e0
	s_and_b32 s13, s14, 0x1e0
	v_lshl_add_u32 v20, s13, 1, v19
	ds_read_b128 v[14:17], v20 offset:4096
	ds_read_b128 v[28:31], v20 offset:20736
	s_setprio 1
	s_waitcnt vmcnt(1) lgkmcnt(1)
	v_mfma_f32_16x16x32_f16 v[40:43], v[32:35], v[14:17], v[40:43]
	s_waitcnt lgkmcnt(0)
	v_mfma_f32_16x16x32_f16 v[6:9], v[32:35], v[28:31], v[6:9]
	s_waitcnt vmcnt(0)
	v_mfma_f32_16x16x32_f16 v[10:13], v[36:39], v[14:17], v[10:13]
	v_mfma_f32_16x16x32_f16 v[2:5], v[36:39], v[28:31], v[2:5]
	s_setprio 0
	v_add_u32_e32 v19, v19, v22
	v_lshlrev_b32_e32 v20, 15, v118
	v_mov_b32_e32 v21, v67
	s_bfe_u32 s22, s2, 0x30003
	v_lshl_add_u64 v[20:21], s[10:11], 0, v[20:21]
	s_lshl_b32 s26, s22, 10
	v_lshl_add_u64 v[64:65], v[20:21], 0, v[58:59]
	v_lshl_add_u64 v[52:53], v[64:65], 0, s[26:27]
	v_add_co_u32_e32 v76, vcc, s29, v52
	s_lshl_b32 s53, s22, 6
	s_nop 0
	v_addc_co_u32_e32 v77, vcc, 0, v53, vcc
	s_mov_b32 s14, 0x14000
	v_mov_b32_e32 v22, 0x14000
	v_mul_u32_u24_e32 v23, 0x210, v81
	s_add_i32 s38, s53, 64
	v_lshlrev_b32_e32 v83, 2, v118
	s_movk_i32 s16, 0x1040
	s_movk_i32 s18, 0x840
	v_lshl_or_b32 v1, v1, 3, v22
	v_add3_u32 v84, v23, v18, s14
	s_and_b32 s14, s38, 0x1c0
	s_movk_i32 s20, 0x210
	s_mov_b32 s19, s27
	v_mad_u32_u24 v56, v118, s16, v58
	v_or_b32_e32 v22, 1, v83
	v_mad_u32_u24 v98, v118, s18, v1
	s_lshl_b32 s18, s14, 4
	v_mad_u32_u24 v99, v22, s12, v58
	v_mad_u32_u24 v85, v22, s20, v1
	v_lshl_add_u64 v[54:55], v[64:65], 0, s[18:19]
	s_add_i32 s12, s53, 0xc0
	s_and_b32 s2, s3, 0x7ffffff
	s_lshl_b32 s3, s22, 5
	s_and_b32 s39, s12, 0x1c0
	s_lshl_b32 s14, s39, 4
	s_add_i32 s39, s3, 32
	s_and_b32 s39, s39, 0xe0
	v_lshl_add_u32 v82, s39, 1, v84
	s_add_i32 s11, s53, 0x80
	s_lshl_b32 s16, s38, 4
	s_mov_b32 s21, s27
	s_and_b32 s30, s11, 0x1c0
	s_lshl_b32 s11, s11, 4
	s_or_b32 s20, s16, 0x2000
	s_mov_b32 s23, s27
	s_mov_b32 s31, s27
	s_mov_b32 s35, s27
	s_or_b32 s22, s16, 0x6000
	s_lshl_b32 s30, s30, 4
	s_or_b32 s34, s11, 0x2000
	v_lshl_add_u64 v[26:27], v[64:65], 0, s[20:21]
	v_lshl_add_u64 v[28:29], v[64:65], 0, s[22:23]
	v_lshl_add_u64 v[30:31], v[64:65], 0, s[30:31]
	v_lshl_add_u64 v[32:33], v[64:65], 0, s[34:35]
	s_mov_b64 s[40:41], 0x40000
	v_lshl_add_u64 v[60:61], v[64:65], 0, s[40:41]
	s_mov_b32 s37, s27
	s_or_b32 s36, s11, 0x6000
	v_lshl_add_u64 v[74:75], v[64:65], 0, s[36:37]
	s_mov_b32 s15, s27
	s_lshl_b32 s12, s12, 4
	v_lshl_add_u64 v[70:71], v[64:65], 0, s[14:15]
	s_mov_b32 s17, s27
	s_or_b32 s16, s12, 0x2000
	s_mov_b32 s13, s27
	s_or_b32 s12, s12, 0x6000
	v_lshl_add_u64 v[72:73], v[64:65], 0, s[16:17]
	v_lshl_add_u64 v[68:69], v[64:65], 0, s[12:13]
	v_add_u32_e32 v1, s53, v84
	s_xor_b32 s10, s26, 0x1000
	s_mov_b32 s11, s27
	s_mov_b32 s49, s27
	s_mov_b32 s51, s27
	s_mov_b32 s47, s27
	v_pk_add_f32 v[14:15], v[180:181], v[40:41]
	v_pk_add_f32 v[16:17], v[182:183], v[42:43]
	v_pk_add_f32 v[10:11], v[184:185], v[10:11]
	v_pk_add_f32 v[12:13], v[186:187], v[12:13]
	v_pk_add_f32 v[6:7], v[188:189], v[6:7]
	v_pk_add_f32 v[8:9], v[190:191], v[8:9]
	v_pk_add_f32 v[2:3], v[192:193], v[2:3]
	v_pk_add_f32 v[4:5], v[194:195], v[4:5]
	ds_write_b128 v19, v[14:17] offset:37376
	ds_write_b128 v19, v[10:13] offset:37440
	ds_write_b128 v19, v[6:9] offset:54016
	ds_write_b128 v19, v[2:5] offset:54080
	v_mov_b64_e32 v[34:35], v[204:205]
	v_mov_b64_e32 v[36:37], v[206:207]
	v_mov_b64_e32 v[38:39], v[208:209]
	v_mov_b64_e32 v[40:41], v[210:211]
	v_add_co_u32_e32 v2, vcc, s52, v52
	s_waitcnt lgkmcnt(0)
	s_nop 0
	v_addc_co_u32_e32 v3, vcc, 0, v53, vcc
	v_add_co_u32_e32 v4, vcc, s33, v52
	s_barrier
	s_nop 0
	v_addc_co_u32_e32 v5, vcc, 0, v53, vcc
	global_load_dwordx4 v[14:17], v[2:3], off
	global_load_dwordx4 v[18:21], v[4:5], off
	global_load_dwordx4 v[22:25], v[52:53], off
	global_load_dwordx4 v[10:13], v[54:55], off
	ds_read_b128 v[2:5], v56 offset:37376
	ds_read_b128 v[6:9], v99 offset:37376
	v_add_co_u32_e32 v78, vcc, s52, v54
	s_mov_b32 s43, s27
	s_waitcnt lgkmcnt(1)
	v_add_f32_e32 v42, v2, v3
	v_add_f32_e32 v42, v42, v4
	v_add_f32_e32 v42, v42, v5
	v_addc_co_u32_e32 v79, vcc, 0, v55, vcc
	s_nop 0
	v_add_f32_dpp v42, v42, v42 quad_perm:[1,0,3,2] row_mask:0xf bank_mask:0xf bound_ctrl:1
	s_mov_b32 s45, s27
	s_mov_b32 s41, s27
	v_add_f32_dpp v42, v42, v42 quad_perm:[2,3,0,1] row_mask:0xf bank_mask:0xf bound_ctrl:1
	v_lshl_add_u64 v[62:63], v[64:65], 0, s[10:11]
	v_lshl_add_u64 v[58:59], s[4:5], 0, v[58:59]
	v_add_f32_dpp v42, v42, v42 row_half_mirror row_mask:0xf bank_mask:0xf bound_ctrl:1
	v_lshl_add_u64 v[152:153], v[60:61], 0, s[26:27]
	v_lshl_add_u64 v[154:155], v[60:61], 0, s[18:19]
	v_add_f32_dpp v42, v42, v42 row_mirror row_mask:0xf bank_mask:0xf bound_ctrl:1
	v_lshl_add_u64 v[156:157], v[60:61], 0, s[20:21]
	v_readlane_b32 s8, v42, 16
	v_readlane_b32 s9, v42, 48
	v_readlane_b32 s6, v42, 0
	v_readlane_b32 s7, v42, 32
	v_mov_b32_e32 v42, s8
	v_mov_b32_e32 v43, s9
	v_pk_add_f32 v[42:43], s[6:7], v[42:43]
	s_mov_b32 s6, 0x3b800000
	v_add_f32_e32 v42, v42, v43
	v_mul_f32_e32 v42, 0x3b800000, v42
	v_pk_add_f32 v[86:87], v[2:3], v[42:43] op_sel_hi:[1,0] neg_lo:[0,1] neg_hi:[0,1]
	v_pk_add_f32 v[88:89], v[4:5], v[42:43] op_sel_hi:[1,0] neg_lo:[0,1] neg_hi:[0,1]
	v_pk_mul_f32 v[42:43], v[86:87], v[86:87]
	v_pk_mul_f32 v[44:45], v[88:89], v[88:89]
	v_add_f32_e32 v42, v42, v43
	v_add_f32_e32 v42, v44, v42
	s_waitcnt lgkmcnt(0)
	v_add_f32_e32 v44, v6, v7
	v_add_f32_e32 v42, v45, v42
	v_add_f32_e32 v44, v44, v8
	v_add_f32_e32 v44, v44, v9
	v_add_f32_dpp v42, v42, v42 quad_perm:[1,0,3,2] row_mask:0xf bank_mask:0xf bound_ctrl:1
	v_lshl_add_u64 v[158:159], v[60:61], 0, s[22:23]
	v_add_f32_dpp v44, v44, v44 quad_perm:[1,0,3,2] row_mask:0xf bank_mask:0xf bound_ctrl:1
	v_add_f32_dpp v42, v42, v42 quad_perm:[2,3,0,1] row_mask:0xf bank_mask:0xf bound_ctrl:1
	v_lshl_add_u64 v[160:161], v[60:61], 0, s[30:31]
	v_add_f32_dpp v44, v44, v44 quad_perm:[2,3,0,1] row_mask:0xf bank_mask:0xf bound_ctrl:1
	v_add_f32_dpp v42, v42, v42 row_half_mirror row_mask:0xf bank_mask:0xf bound_ctrl:1
	v_lshl_add_u64 v[162:163], v[60:61], 0, s[34:35]
	v_add_f32_dpp v44, v44, v44 row_half_mirror row_mask:0xf bank_mask:0xf bound_ctrl:1
	v_add_f32_dpp v42, v42, v42 row_mirror row_mask:0xf bank_mask:0xf bound_ctrl:1
	v_lshl_add_u64 v[164:165], v[60:61], 0, s[36:37]
	v_readlane_b32 s7, v42, 16
	v_readlane_b32 s39, v42, 48
	v_add_f32_dpp v44, v44, v44 row_mirror row_mask:0xf bank_mask:0xf bound_ctrl:1
	v_readlane_b32 s8, v42, 0
	v_readlane_b32 s9, v42, 32
	v_mov_b32_e32 v42, s7
	v_mov_b32_e32 v43, s39
	v_readlane_b32 s7, v44, 16
	v_readlane_b32 s39, v44, 48
	v_pk_add_f32 v[42:43], s[8:9], v[42:43]
	v_readlane_b32 s8, v44, 0
	v_readlane_b32 s9, v44, 32
	v_mov_b32_e32 v44, s7
	v_mov_b32_e32 v45, s39
	v_pk_add_f32 v[44:45], s[8:9], v[44:45]
	s_nop 0
	v_add_f32_e32 v44, v44, v45
	v_mul_f32_e32 v44, 0x3b800000, v44
	v_pk_add_f32 v[90:91], v[6:7], v[44:45] op_sel_hi:[1,0] neg_lo:[0,1] neg_hi:[0,1]
	v_pk_add_f32 v[92:93], v[8:9], v[44:45] op_sel_hi:[1,0] neg_lo:[0,1] neg_hi:[0,1]
	v_pk_mul_f32 v[46:47], v[90:91], v[90:91]
	v_pk_mul_f32 v[44:45], v[92:93], v[92:93]
	v_add_f32_e32 v46, v46, v47
	v_add_f32_e32 v44, v44, v46
	v_add_f32_e32 v44, v45, v44
	v_mov_b32_e32 v47, v42
	s_nop 0
	v_add_f32_dpp v44, v44, v44 quad_perm:[1,0,3,2] row_mask:0xf bank_mask:0xf bound_ctrl:1
	s_nop 1
	v_add_f32_dpp v44, v44, v44 quad_perm:[2,3,0,1] row_mask:0xf bank_mask:0xf bound_ctrl:1
	s_nop 1
	v_add_f32_dpp v44, v44, v44 row_half_mirror row_mask:0xf bank_mask:0xf bound_ctrl:1
	s_nop 1
	v_add_f32_dpp v44, v44, v44 row_mirror row_mask:0xf bank_mask:0xf bound_ctrl:1
	s_nop 0
	v_readlane_b32 s7, v44, 16
	v_readlane_b32 s39, v44, 48
	v_readlane_b32 s8, v44, 0
	v_readlane_b32 s9, v44, 32
	v_mov_b32_e32 v44, s7
	v_mov_b32_e32 v45, s39
	v_pk_add_f32 v[44:45], s[8:9], v[44:45]
	s_mov_b32 s8, 0x3727c5ac
	v_mov_b32_e32 v46, v44
	v_mov_b32_e32 v42, v45
	v_pk_add_f32 v[42:43], v[46:47], v[42:43]
	v_mov_b64_e32 v[94:95], s[8:9]
	v_pk_fma_f32 v[96:97], v[42:43], s[6:7], v[94:95] op_sel_hi:[1,0,0]
	s_mov_b32 s7, 0x800000
	v_mul_f32_e32 v42, 0x4b800000, v97
	v_cmp_gt_f32_e32 vcc, s7, v97
	s_nop 1
	v_cndmask_b32_e32 v42, v97, v42, vcc
	v_rsq_f32_e32 v97, v42
	global_load_dwordx4 v[54:57], v[26:27], off
	global_load_dwordx4 v[50:53], v[28:29], off
	global_load_dwordx4 v[46:49], v[30:31], off
	global_load_dwordx4 v[42:45], v[32:33], off
	v_mul_f32_e32 v26, 0x45800000, v97
	v_cndmask_b32_e32 v26, v97, v26, vcc
	v_pk_mul_f32 v[28:29], v[86:87], v[26:27] op_sel_hi:[1,0]
	v_cmp_gt_f32_e32 vcc, s7, v96
	s_waitcnt vmcnt(8)
	v_pk_fma_f32 v[28:29], v[34:35], v[28:29], v[38:39]
	v_pk_mul_f32 v[26:27], v[88:89], v[26:27] op_sel_hi:[1,0]
	v_cvt_pk_f16_f32 v28, v28, v29
	v_mul_f32_e32 v29, 0x4b800000, v96
	v_cndmask_b32_e32 v29, v96, v29, vcc
	v_rsq_f32_e32 v32, v29
	v_pk_fma_f32 v[26:27], v[36:37], v[26:27], v[40:41]
	s_nop 0
	v_cvt_pk_f16_f32 v29, v26, v27
	v_mul_f32_e32 v26, 0x45800000, v32
	v_cndmask_b32_e32 v26, v32, v26, vcc
	ds_write_b64 v98, v[28:29]
	v_pk_mul_f32 v[28:29], v[90:91], v[26:27] op_sel_hi:[1,0]
	v_pk_mul_f32 v[26:27], v[92:93], v[26:27] op_sel_hi:[1,0]
	v_pk_fma_f32 v[28:29], v[34:35], v[28:29], v[38:39]
	v_pk_fma_f32 v[26:27], v[36:37], v[26:27], v[40:41]
	v_cvt_pk_f16_f32 v28, v28, v29
	v_cvt_pk_f16_f32 v29, v26, v27
	ds_write_b64 v85, v[28:29]
	ds_read_b128 v[26:29], v99 offset:38416
	v_add_co_u32_e32 v102, vcc, s52, v30
	s_nop 1
	v_addc_co_u32_e32 v103, vcc, 0, v31, vcc
	ds_read_b128 v[30:33], v99 offset:39456
	s_waitcnt lgkmcnt(1)
	v_add_f32_e32 v86, v26, v27
	v_add_f32_e32 v86, v86, v28
	v_add_f32_e32 v86, v86, v29
	s_nop 1
	v_add_f32_dpp v86, v86, v86 quad_perm:[1,0,3,2] row_mask:0xf bank_mask:0xf bound_ctrl:1
	s_nop 1
	v_add_f32_dpp v86, v86, v86 quad_perm:[2,3,0,1] row_mask:0xf bank_mask:0xf bound_ctrl:1
	s_nop 1
	v_add_f32_dpp v86, v86, v86 row_half_mirror row_mask:0xf bank_mask:0xf bound_ctrl:1
	s_nop 1
	v_add_f32_dpp v86, v86, v86 row_mirror row_mask:0xf bank_mask:0xf bound_ctrl:1
	s_nop 0
	v_readlane_b32 s39, v86, 16
	v_readlane_b32 s40, v86, 48
	v_readlane_b32 s8, v86, 0
	v_readlane_b32 s9, v86, 32
	v_mov_b32_e32 v86, s39
	v_mov_b32_e32 v87, s40
	v_pk_add_f32 v[86:87], s[8:9], v[86:87]
	s_nop 0
	v_add_f32_e32 v86, v86, v87
	v_mul_f32_e32 v86, 0x3b800000, v86
	v_pk_add_f32 v[104:105], v[26:27], v[86:87] op_sel_hi:[1,0] neg_lo:[0,1] neg_hi:[0,1]
	v_pk_add_f32 v[106:107], v[28:29], v[86:87] op_sel_hi:[1,0] neg_lo:[0,1] neg_hi:[0,1]
	v_pk_mul_f32 v[88:89], v[104:105], v[104:105]
	v_pk_mul_f32 v[86:87], v[106:107], v[106:107]
	v_add_f32_e32 v88, v88, v89
	v_add_f32_e32 v86, v86, v88
	s_waitcnt lgkmcnt(0)
	v_add_f32_e32 v88, v30, v31
	v_add_f32_e32 v86, v87, v86
	v_add_f32_e32 v88, v88, v32
	v_add_f32_e32 v88, v88, v33
	v_add_f32_dpp v86, v86, v86 quad_perm:[1,0,3,2] row_mask:0xf bank_mask:0xf bound_ctrl:1
	s_nop 0
	v_add_f32_dpp v88, v88, v88 quad_perm:[1,0,3,2] row_mask:0xf bank_mask:0xf bound_ctrl:1
	v_add_f32_dpp v86, v86, v86 quad_perm:[2,3,0,1] row_mask:0xf bank_mask:0xf bound_ctrl:1
	s_nop 0
	v_add_f32_dpp v88, v88, v88 quad_perm:[2,3,0,1] row_mask:0xf bank_mask:0xf bound_ctrl:1
	v_add_f32_dpp v86, v86, v86 row_half_mirror row_mask:0xf bank_mask:0xf bound_ctrl:1
	s_nop 0
	v_add_f32_dpp v88, v88, v88 row_half_mirror row_mask:0xf bank_mask:0xf bound_ctrl:1
	v_add_f32_dpp v86, v86, v86 row_mirror row_mask:0xf bank_mask:0xf bound_ctrl:1
	s_nop 0
	v_readlane_b32 s39, v86, 16
	v_readlane_b32 s40, v86, 48
	v_add_f32_dpp v88, v88, v88 row_mirror row_mask:0xf bank_mask:0xf bound_ctrl:1
	v_readlane_b32 s8, v86, 0
	v_readlane_b32 s9, v86, 32
	v_mov_b32_e32 v86, s39
	v_mov_b32_e32 v87, s40
	v_readlane_b32 s39, v88, 16
	v_readlane_b32 s40, v88, 48
	v_pk_add_f32 v[86:87], s[8:9], v[86:87]
	v_readlane_b32 s8, v88, 0
	v_readlane_b32 s9, v88, 32
	v_mov_b32_e32 v88, s39
	v_mov_b32_e32 v89, s40
	v_pk_add_f32 v[88:89], s[8:9], v[88:89]
	s_nop 0
	v_add_f32_e32 v88, v88, v89
	v_mul_f32_e32 v88, 0x3b800000, v88
	v_pk_add_f32 v[108:109], v[30:31], v[88:89] op_sel_hi:[1,0] neg_lo:[0,1] neg_hi:[0,1]
	v_pk_add_f32 v[110:111], v[32:33], v[88:89] op_sel_hi:[1,0] neg_lo:[0,1] neg_hi:[0,1]
	v_pk_mul_f32 v[90:91], v[108:109], v[108:109]
	v_pk_mul_f32 v[88:89], v[110:111], v[110:111]
	v_add_f32_e32 v90, v90, v91
	v_add_f32_e32 v88, v88, v90
	v_add_f32_e32 v88, v89, v88
	v_mov_b32_e32 v91, v86
	s_nop 0
	v_add_f32_dpp v88, v88, v88 quad_perm:[1,0,3,2] row_mask:0xf bank_mask:0xf bound_ctrl:1
	s_nop 1
	v_add_f32_dpp v88, v88, v88 quad_perm:[2,3,0,1] row_mask:0xf bank_mask:0xf bound_ctrl:1
	s_nop 1
	v_add_f32_dpp v88, v88, v88 row_half_mirror row_mask:0xf bank_mask:0xf bound_ctrl:1
	s_nop 1
	v_add_f32_dpp v88, v88, v88 row_mirror row_mask:0xf bank_mask:0xf bound_ctrl:1
	s_nop 0
	v_readlane_b32 s39, v88, 16
	v_readlane_b32 s40, v88, 48
	v_readlane_b32 s8, v88, 0
	v_readlane_b32 s9, v88, 32
	v_mov_b32_e32 v88, s39
	v_mov_b32_e32 v89, s40
	v_pk_add_f32 v[88:89], s[8:9], v[88:89]
	s_mov_b32 s9, s27
	v_mov_b32_e32 v90, v88
	v_mov_b32_e32 v86, v89
	v_pk_add_f32 v[86:87], v[90:91], v[86:87]
	s_mov_b32 s39, s27
	v_pk_fma_f32 v[112:113], v[86:87], s[6:7], v[94:95] op_sel_hi:[1,0,0]
	s_add_i32 s6, s53, 0x140
	v_mul_f32_e32 v86, 0x4b800000, v113
	v_cmp_gt_f32_e32 vcc, s7, v113
	s_nop 1
	v_cndmask_b32_e32 v86, v113, v86, vcc
	v_rsq_f32_e32 v113, v86
	global_load_dwordx4 v[86:89], v[78:79], off
	global_load_dwordx4 v[90:93], v[102:103], off
	global_load_dwordx4 v[94:97], v[76:77], off
	global_load_dwordx4 v[98:101], v[74:75], off
	v_mul_f32_e32 v74, 0x45800000, v113
	v_cndmask_b32_e32 v74, v113, v74, vcc
	v_pk_mul_f32 v[76:77], v[104:105], v[74:75] op_sel_hi:[1,0]
	v_mul_f32_e32 v75, 0x4b800000, v112
	v_cmp_gt_f32_e32 vcc, s7, v112
	v_pk_fma_f32 v[76:77], v[34:35], v[76:77], v[38:39]
	s_and_b32 s7, s6, 0x1c0
	v_cndmask_b32_e32 v75, v112, v75, vcc
	v_rsq_f32_e32 v78, v75
	v_pk_mul_f32 v[74:75], v[106:107], v[74:75] op_sel_hi:[1,0]
	v_cvt_pk_f16_f32 v76, v76, v77
	v_pk_fma_f32 v[74:75], v[36:37], v[74:75], v[40:41]
	s_lshl_b32 s6, s6, 4
	v_cvt_pk_f16_f32 v77, v74, v75
	v_mul_f32_e32 v74, 0x45800000, v78
	v_cndmask_b32_e32 v74, v78, v74, vcc
	v_pk_mul_f32 v[78:79], v[108:109], v[74:75] op_sel_hi:[1,0]
	s_or_b32 s50, s6, 0x2000
	v_pk_fma_f32 v[34:35], v[34:35], v[78:79], v[38:39]
	v_pk_mul_f32 v[38:39], v[110:111], v[74:75] op_sel_hi:[1,0]
	v_add_co_u32_e32 v78, vcc, s52, v70
	v_pk_fma_f32 v[36:37], v[36:37], v[38:39], v[40:41]
	v_cvt_pk_f16_f32 v34, v34, v35
	v_cvt_pk_f16_f32 v35, v36, v37
	v_addc_co_u32_e32 v79, vcc, 0, v71, vcc
	ds_write2_b64 v85, v[76:77], v[34:35] offset0:66 offset1:132
	s_waitcnt lgkmcnt(0)
	s_barrier
	global_load_dwordx4 v[34:37], v[70:71], off
	global_load_dwordx4 v[38:41], v[72:73], off
	s_nop 0
	global_load_dwordx4 v[70:73], v[78:79], off
	global_load_dwordx4 v[74:77], v[68:69], off
	s_or_b32 s46, s6, 0x6000
	s_sub_i32 s6, s38, s3
	s_and_b32 s6, s6, 0xe0
	v_lshl_add_u32 v172, s6, 1, v84
	s_add_i32 s6, s53, 0x180
	s_lshl_b32 s48, s7, 4
	s_and_b32 s7, s6, 0x1c0
	s_lshl_b32 s6, s6, 4
	s_or_b32 s44, s6, 0x2000
	s_or_b32 s40, s6, 0x6000
	s_add_i32 s6, s3, 0x60
	s_and_b32 s6, s6, 0xe0
	v_lshl_add_u32 v173, s6, 1, v84
	s_add_i32 s6, s53, 0x1c0
	s_xor_b32 s53, s53, 0x100
	v_add_u32_e32 v174, s53, v84
	s_add_i32 s53, s3, 0xa0
	s_lshl_b32 s42, s7, 4
	s_and_b32 s7, s6, 0x1c0
	s_lshl_b32 s6, s6, 4
	s_and_b32 s53, s53, 0xe0
	s_lshl_b32 s8, s7, 4
	s_or_b32 s38, s6, 0x2000
	s_or_b32 s6, s6, 0x6000
	s_mov_b32 s7, s27
	v_lshl_add_u32 v175, s53, 1, v84
	s_add_i32 s53, s3, 0xc0
	s_addk_i32 s3, 0xe0
	v_lshl_add_u64 v[68:69], v[64:65], 0, s[48:49]
	v_lshl_add_u64 v[78:79], v[64:65], 0, s[50:51]
	v_lshl_add_u64 v[138:139], v[64:65], 0, s[46:47]
	v_lshl_add_u64 v[140:141], v[64:65], 0, s[42:43]
	v_lshl_add_u64 v[142:143], v[64:65], 0, s[44:45]
	v_lshl_add_u64 v[144:145], v[64:65], 0, s[40:41]
	v_lshl_add_u64 v[146:147], v[64:65], 0, s[8:9]
	v_lshl_add_u64 v[148:149], v[64:65], 0, s[38:39]
	v_lshl_add_u64 v[150:151], v[64:65], 0, s[6:7]
	s_and_b32 s53, s53, 0xe0
	s_and_b32 s3, s3, 0xe0
	v_add_u32_e32 v64, s28, v83
	v_mov_b32_e32 v65, v67
	v_lshl_add_u32 v176, s53, 1, v84
	v_lshl_add_u32 v177, s3, 1, v84
	v_lshlrev_b64 v[84:85], 10, v[64:65]
	ds_read_b128 v[102:105], v1
	ds_read_b128 v[106:109], v1 offset:8448
	v_lshl_add_u64 v[166:167], v[58:59], 0, v[84:85]
	v_or_b32_e32 v84, 1, v64
	v_mov_b32_e32 v85, v67
	v_lshlrev_b64 v[84:85], 10, v[84:85]
	v_lshl_add_u64 v[168:169], v[58:59], 0, v[84:85]
	v_or_b32_e32 v84, 2, v64
	v_mov_b32_e32 v85, v67
	v_or_b32_e32 v64, 3, v64
	v_lshlrev_b64 v[84:85], 10, v[84:85]
	v_lshlrev_b64 v[64:65], 10, v[64:65]
	v_lshl_add_u64 v[170:171], v[58:59], 0, v[84:85]
	v_lshl_add_u64 v[58:59], v[58:59], 0, v[64:65]
	s_setprio 1
	s_waitcnt vmcnt(13) lgkmcnt(1)
	v_mfma_f32_16x16x32_f16 v[110:113], v[102:105], v[22:25], 0
	s_waitcnt lgkmcnt(0)
	v_mfma_f32_16x16x32_f16 v[22:25], v[106:109], v[22:25], 0
	s_waitcnt vmcnt(5)
	v_mfma_f32_16x16x32_f16 v[114:117], v[102:105], v[94:97], 0
	v_mfma_f32_16x16x32_f16 v[94:97], v[106:109], v[94:97], 0
	v_mfma_f32_16x16x32_f16 v[118:121], v[102:105], v[14:17], 0
	v_mfma_f32_16x16x32_f16 v[14:17], v[106:109], v[14:17], 0
	v_mfma_f32_16x16x32_f16 v[102:105], v[102:105], v[18:21], 0
	v_mfma_f32_16x16x32_f16 v[18:21], v[106:109], v[18:21], 0
	s_setprio 0
	v_add_co_u32_e32 v64, vcc, s29, v62
	global_load_dwordx4 v[106:109], v[62:63], off
	s_nop 0
	v_addc_co_u32_e32 v65, vcc, 0, v63, vcc
	v_add_co_u32_e32 v84, vcc, s52, v62
	s_nop 1
	v_addc_co_u32_e32 v85, vcc, 0, v63, vcc
	v_add_co_u32_e32 v62, vcc, s33, v62
	global_load_dwordx4 v[122:125], v[64:65], off
	global_load_dwordx4 v[126:129], v[84:85], off
	v_addc_co_u32_e32 v63, vcc, 0, v63, vcc
	global_load_dwordx4 v[62:65], v[62:63], off
	ds_read_b128 v[130:133], v82
	ds_read_b128 v[134:137], v82 offset:8448
	s_setprio 1
	s_waitcnt lgkmcnt(1)
	v_mfma_f32_16x16x32_f16 v[110:113], v[130:133], v[10:13], v[110:113]
	s_waitcnt lgkmcnt(0)
	v_mfma_f32_16x16x32_f16 v[10:13], v[134:137], v[10:13], v[22:25]
	v_mfma_f32_16x16x32_f16 v[22:25], v[130:133], v[54:57], v[114:117]
	v_mfma_f32_16x16x32_f16 v[54:57], v[134:137], v[54:57], v[94:97]
	v_mfma_f32_16x16x32_f16 v[94:97], v[130:133], v[86:89], v[118:121]
	v_mfma_f32_16x16x32_f16 v[14:17], v[134:137], v[86:89], v[14:17]
	v_mfma_f32_16x16x32_f16 v[84:87], v[130:133], v[50:53], v[102:105]
	v_mfma_f32_16x16x32_f16 v[18:21], v[134:137], v[50:53], v[18:21]
	s_setprio 0
	global_load_dwordx4 v[50:53], v[68:69], off
	global_load_dwordx4 v[102:105], v[78:79], off
	v_add_co_u32_e32 v68, vcc, s52, v68
	s_nop 1
	v_addc_co_u32_e32 v69, vcc, 0, v69, vcc
	global_load_dwordx4 v[114:117], v[68:69], off
	global_load_dwordx4 v[118:121], v[138:139], off
	ds_read_b128 v[130:133], v172
	ds_read_b128 v[134:137], v172 offset:8448
	s_setprio 1
	s_waitcnt lgkmcnt(1)
	v_mfma_f32_16x16x32_f16 v[110:113], v[130:133], v[46:49], v[110:113]
	s_waitcnt lgkmcnt(0)
	v_mfma_f32_16x16x32_f16 v[10:13], v[134:137], v[46:49], v[10:13]
	v_mfma_f32_16x16x32_f16 v[22:25], v[130:133], v[42:45], v[22:25]
	v_mfma_f32_16x16x32_f16 v[42:45], v[134:137], v[42:45], v[54:57]
	v_mfma_f32_16x16x32_f16 v[46:49], v[130:133], v[90:93], v[94:97]
	v_mfma_f32_16x16x32_f16 v[14:17], v[134:137], v[90:93], v[14:17]
	s_waitcnt vmcnt(12)
	v_mfma_f32_16x16x32_f16 v[54:57], v[130:133], v[98:101], v[84:87]
	v_mfma_f32_16x16x32_f16 v[18:21], v[134:137], v[98:101], v[18:21]
	s_setprio 0
	v_add_co_u32_e32 v68, vcc, s52, v140
	global_load_dwordx4 v[84:87], v[140:141], off
	global_load_dwordx4 v[88:91], v[142:143], off
	v_addc_co_u32_e32 v69, vcc, 0, v141, vcc
	global_load_dwordx4 v[92:95], v[68:69], off
	global_load_dwordx4 v[96:99], v[144:145], off
	ds_read_b128 v[130:133], v173
	ds_read_b128 v[134:137], v173 offset:8448
	s_setprio 1
	s_waitcnt vmcnt(15) lgkmcnt(1)
	v_mfma_f32_16x16x32_f16 v[110:113], v[130:133], v[34:37], v[110:113]
	s_waitcnt lgkmcnt(0)
	v_mfma_f32_16x16x32_f16 v[10:13], v[134:137], v[34:37], v[10:13]
	s_waitcnt vmcnt(14)
	v_mfma_f32_16x16x32_f16 v[22:25], v[130:133], v[38:41], v[22:25]
	v_mfma_f32_16x16x32_f16 v[34:37], v[134:137], v[38:41], v[42:45]
	s_waitcnt vmcnt(13)
	v_mfma_f32_16x16x32_f16 v[38:41], v[130:133], v[70:73], v[46:49]
	v_mfma_f32_16x16x32_f16 v[14:17], v[134:137], v[70:73], v[14:17]
	s_waitcnt vmcnt(12)
	v_mfma_f32_16x16x32_f16 v[42:45], v[130:133], v[74:77], v[54:57]
	v_mfma_f32_16x16x32_f16 v[18:21], v[134:137], v[74:77], v[18:21]
	s_setprio 0
	v_add_co_u32_e32 v68, vcc, s52, v146
	global_load_dwordx4 v[46:49], v[146:147], off
	global_load_dwordx4 v[54:57], v[148:149], off
	v_addc_co_u32_e32 v69, vcc, 0, v147, vcc
	global_load_dwordx4 v[68:71], v[68:69], off
	s_nop 0
	global_load_dwordx4 v[72:75], v[150:151], off
	ds_read_b128 v[76:79], v174
	ds_read_b128 v[130:133], v174 offset:8448
	s_setprio 1
	s_waitcnt vmcnt(15) lgkmcnt(1)
	v_mfma_f32_16x16x32_f16 v[110:113], v[76:79], v[106:109], v[110:113]
	s_waitcnt lgkmcnt(0)
	v_mfma_f32_16x16x32_f16 v[10:13], v[130:133], v[106:109], v[10:13]
	s_waitcnt vmcnt(14)
	v_mfma_f32_16x16x32_f16 v[22:25], v[76:79], v[122:125], v[22:25]
	v_mfma_f32_16x16x32_f16 v[34:37], v[130:133], v[122:125], v[34:37]
	s_waitcnt vmcnt(13)
	v_mfma_f32_16x16x32_f16 v[38:41], v[76:79], v[126:129], v[38:41]
	v_mfma_f32_16x16x32_f16 v[14:17], v[130:133], v[126:129], v[14:17]
	s_waitcnt vmcnt(12)
	v_mfma_f32_16x16x32_f16 v[42:45], v[76:79], v[62:65], v[42:45]
	v_mfma_f32_16x16x32_f16 v[18:21], v[130:133], v[62:65], v[18:21]
	s_setprio 0
	ds_read_b128 v[62:65], v175
	ds_read_b128 v[76:79], v175 offset:8448
	s_setprio 1
	s_waitcnt vmcnt(11) lgkmcnt(1)
	v_mfma_f32_16x16x32_f16 v[106:109], v[62:65], v[50:53], v[110:113]
	s_waitcnt lgkmcnt(0)
	v_mfma_f32_16x16x32_f16 v[10:13], v[76:79], v[50:53], v[10:13]
	s_waitcnt vmcnt(10)
	v_mfma_f32_16x16x32_f16 v[22:25], v[62:65], v[102:105], v[22:25]
	v_mfma_f32_16x16x32_f16 v[34:37], v[76:79], v[102:105], v[34:37]
	s_waitcnt vmcnt(9)
	v_mfma_f32_16x16x32_f16 v[38:41], v[62:65], v[114:117], v[38:41]
	v_mfma_f32_16x16x32_f16 v[14:17], v[76:79], v[114:117], v[14:17]
	s_waitcnt vmcnt(8)
	v_mfma_f32_16x16x32_f16 v[42:45], v[62:65], v[118:121], v[42:45]
	v_mfma_f32_16x16x32_f16 v[18:21], v[76:79], v[118:121], v[18:21]
	s_setprio 0
	ds_read_b128 v[50:53], v176
	ds_read_b128 v[62:65], v176 offset:8448
	s_setprio 1
	s_waitcnt vmcnt(7) lgkmcnt(1)
	v_mfma_f32_16x16x32_f16 v[76:79], v[50:53], v[84:87], v[106:109]
	s_waitcnt lgkmcnt(0)
	v_mfma_f32_16x16x32_f16 v[10:13], v[62:65], v[84:87], v[10:13]
	s_waitcnt vmcnt(6)
	v_mfma_f32_16x16x32_f16 v[22:25], v[50:53], v[88:91], v[22:25]
	v_mfma_f32_16x16x32_f16 v[34:37], v[62:65], v[88:91], v[34:37]
	s_waitcnt vmcnt(5)
	v_mfma_f32_16x16x32_f16 v[38:41], v[50:53], v[92:95], v[38:41]
	v_mfma_f32_16x16x32_f16 v[14:17], v[62:65], v[92:95], v[14:17]
	s_waitcnt vmcnt(4)
	v_mfma_f32_16x16x32_f16 v[42:45], v[50:53], v[96:99], v[42:45]
	v_mfma_f32_16x16x32_f16 v[18:21], v[62:65], v[96:99], v[18:21]
	s_setprio 0
	ds_read_b128 v[50:53], v177
	ds_read_b128 v[62:65], v177 offset:8448
	s_setprio 1
	s_waitcnt vmcnt(3) lgkmcnt(1)
	v_mfma_f32_16x16x32_f16 v[76:79], v[50:53], v[46:49], v[76:79]
	s_waitcnt lgkmcnt(0)
	v_mfma_f32_16x16x32_f16 v[10:13], v[62:65], v[46:49], v[10:13]
	s_waitcnt vmcnt(2)
	v_mfma_f32_16x16x32_f16 v[22:25], v[50:53], v[54:57], v[22:25]
	v_mfma_f32_16x16x32_f16 v[34:37], v[62:65], v[54:57], v[34:37]
	s_waitcnt vmcnt(1)
	v_mfma_f32_16x16x32_f16 v[38:41], v[50:53], v[68:71], v[38:41]
	v_mfma_f32_16x16x32_f16 v[14:17], v[62:65], v[68:71], v[14:17]
	s_waitcnt vmcnt(0)
	v_mfma_f32_16x16x32_f16 v[42:45], v[50:53], v[72:75], v[42:45]
	v_mfma_f32_16x16x32_f16 v[18:21], v[62:65], v[72:75], v[18:21]
	s_setprio 0
	v_add_co_u32_e32 v108, vcc, s29, v152
	v_and_b32_e32 v67, 0x1c0, v0
	s_nop 0
	v_addc_co_u32_e32 v109, vcc, 0, v153, vcc
	v_add_co_u32_e32 v46, vcc, s52, v152
	s_movk_i32 s4, 0x50
	s_nop 0
	v_addc_co_u32_e32 v47, vcc, 0, v153, vcc
	v_add_co_u32_e32 v68, vcc, s33, v152
	v_or_b32_e32 v116, 16, v67
	s_nop 0
	v_addc_co_u32_e32 v69, vcc, 0, v153, vcc
	v_add_co_u32_e32 v110, vcc, s52, v154
	global_load_dwordx4 v[46:49], v[46:47], off
	s_nop 0
	global_load_dwordx4 v[50:53], v[68:69], off
	global_load_dwordx4 v[54:57], v[152:153], off
	global_load_dwordx4 v[62:65], v[154:155], off
	v_addc_co_u32_e32 v111, vcc, 0, v155, vcc
	v_add_co_u32_e32 v112, vcc, s52, v160
	global_load_dwordx4 v[68:71], v[156:157], off
	global_load_dwordx4 v[72:75], v[158:159], off
	global_load_dwordx4 v[84:87], v[160:161], off
	global_load_dwordx4 v[88:91], v[162:163], off
	v_addc_co_u32_e32 v113, vcc, 0, v161, vcc
	global_load_dwordx4 v[92:95], v[110:111], off
	global_load_dwordx4 v[96:99], v[112:113], off
	global_load_dwordx4 v[100:103], v[108:109], off
	global_load_dwordx4 v[104:107], v[164:165], off
	s_nop 0
	global_store_dwordx4 v[166:167], v[2:5], off sc0 sc1
	global_store_dwordx4 v[168:169], v[6:9], off sc0 sc1
	global_store_dwordx4 v[170:171], v[26:29], off sc0 sc1
	global_store_dwordx4 v[58:59], v[30:33], off sc0 sc1
	v_and_b32_e32 v4, 0x1cf, v0
	v_cvt_pk_f16_f32 v3, v78, v79
	v_cvt_pk_f16_f32 v2, v76, v77
	v_mad_u32_u24 v4, v4, s4, v80
	v_or_b32_e32 v5, v116, v81
	v_or_b32_e32 v117, 32, v67
	ds_write_b64 v4, v[2:3]
	v_cvt_pk_f16_f32 v3, v24, v25
	v_cvt_pk_f16_f32 v2, v22, v23
	v_mad_u32_u24 v5, v5, s4, v80
	v_or_b32_e32 v6, v117, v81
	v_or_b32_e32 v118, 48, v67
	ds_write_b64 v5, v[2:3]
	v_cvt_pk_f16_f32 v3, v40, v41
	v_cvt_pk_f16_f32 v2, v38, v39
	v_mad_u32_u24 v6, v6, s4, v80
	v_or_b32_e32 v7, v118, v81
	ds_write_b64 v6, v[2:3]
	v_cvt_pk_f16_f32 v3, v44, v45
	v_cvt_pk_f16_f32 v2, v42, v43
	v_mad_u32_u24 v7, v7, s4, v80
	ds_write_b64 v7, v[2:3]
	v_cvt_pk_f16_f32 v3, v12, v13
	v_cvt_pk_f16_f32 v2, v10, v11
	ds_write_b64 v4, v[2:3] offset:32
	v_cvt_pk_f16_f32 v3, v36, v37
	v_cvt_pk_f16_f32 v2, v34, v35
	ds_write_b64 v5, v[2:3] offset:32
	v_cvt_pk_f16_f32 v3, v16, v17
	v_cvt_pk_f16_f32 v2, v14, v15
	v_lshl_add_u64 v[10:11], v[60:61], 0, s[14:15]
	ds_write_b64 v6, v[2:3] offset:32
	v_cvt_pk_f16_f32 v2, v18, v19
	v_add_co_u32_e32 v18, vcc, s52, v10
	v_cvt_pk_f16_f32 v3, v20, v21
	v_lshl_add_u64 v[12:13], v[60:61], 0, s[16:17]
	v_addc_co_u32_e32 v19, vcc, 0, v11, vcc
	ds_write_b64 v7, v[2:3] offset:32
	s_waitcnt lgkmcnt(0)
	s_barrier
	global_load_dwordx4 v[2:5], v[10:11], off
	global_load_dwordx4 v[6:9], v[12:13], off
	v_lshl_add_u64 v[20:21], v[60:61], 0, s[12:13]
	global_load_dwordx4 v[10:13], v[18:19], off
	global_load_dwordx4 v[14:17], v[20:21], off
	ds_read_b128 v[18:21], v1
	ds_read_b128 v[22:25], v1 offset:8448
	s_mov_b32 s3, s27
	s_setprio 1
	s_waitcnt vmcnt(17) lgkmcnt(1)
	v_mfma_f32_16x16x32_f16 v[26:29], v[18:21], v[54:57], 0
	s_waitcnt lgkmcnt(0)
	v_mfma_f32_16x16x32_f16 v[30:33], v[22:25], v[54:57], 0
	s_waitcnt vmcnt(9)
	v_mfma_f32_16x16x32_f16 v[34:37], v[18:21], v[100:103], 0
	v_mfma_f32_16x16x32_f16 v[38:41], v[22:25], v[100:103], 0
	v_mfma_f32_16x16x32_f16 v[42:45], v[18:21], v[46:49], 0
	v_mfma_f32_16x16x32_f16 v[46:49], v[22:25], v[46:49], 0
	v_mfma_f32_16x16x32_f16 v[18:21], v[18:21], v[50:53], 0
	v_mfma_f32_16x16x32_f16 v[22:25], v[22:25], v[50:53], 0
	s_setprio 0
	v_lshl_add_u64 v[58:59], v[60:61], 0, s[10:11]
	v_add_co_u32_e32 v76, vcc, s29, v58
	s_nop 1
	v_addc_co_u32_e32 v77, vcc, 0, v59, vcc
	v_add_co_u32_e32 v108, vcc, s52, v58
	global_load_dwordx4 v[50:53], v[58:59], off
	global_load_dwordx4 v[54:57], v[76:77], off
	v_addc_co_u32_e32 v109, vcc, 0, v59, vcc
	v_add_co_u32_e32 v58, vcc, s33, v58
	s_nop 1
	v_addc_co_u32_e32 v59, vcc, 0, v59, vcc
	global_load_dwordx4 v[76:79], v[108:109], off
	global_load_dwordx4 v[100:103], v[58:59], off
	ds_read_b128 v[108:111], v82
	ds_read_b128 v[112:115], v82 offset:8448
	s_setprio 1
	s_waitcnt lgkmcnt(1)
	v_mfma_f32_16x16x32_f16 v[26:29], v[108:111], v[62:65], v[26:29]
	s_waitcnt lgkmcnt(0)
	v_mfma_f32_16x16x32_f16 v[30:33], v[112:115], v[62:65], v[30:33]
	v_mfma_f32_16x16x32_f16 v[34:37], v[108:111], v[68:71], v[34:37]
	v_mfma_f32_16x16x32_f16 v[38:41], v[112:115], v[68:71], v[38:41]
	v_mfma_f32_16x16x32_f16 v[42:45], v[108:111], v[92:95], v[42:45]
	v_mfma_f32_16x16x32_f16 v[46:49], v[112:115], v[92:95], v[46:49]
	v_mfma_f32_16x16x32_f16 v[18:21], v[108:111], v[72:75], v[18:21]
	v_mfma_f32_16x16x32_f16 v[22:25], v[112:115], v[72:75], v[22:25]
	s_setprio 0
	v_lshl_add_u64 v[58:59], v[60:61], 0, s[48:49]
	v_lshl_add_u64 v[72:73], v[60:61], 0, s[50:51]
	global_load_dwordx4 v[62:65], v[58:59], off
	global_load_dwordx4 v[68:71], v[72:73], off
	v_add_co_u32_e32 v58, vcc, s52, v58
	v_lshl_add_u64 v[82:83], v[60:61], 0, s[46:47]
	s_nop 0
	v_addc_co_u32_e32 v59, vcc, 0, v59, vcc
	global_load_dwordx4 v[72:75], v[58:59], off
	global_load_dwordx4 v[92:95], v[82:83], off
	ds_read_b128 v[108:111], v172
	ds_read_b128 v[112:115], v172 offset:8448
	s_setprio 1
	s_waitcnt lgkmcnt(1)
	v_mfma_f32_16x16x32_f16 v[26:29], v[108:111], v[84:87], v[26:29]
	s_waitcnt lgkmcnt(0)
	v_mfma_f32_16x16x32_f16 v[30:33], v[112:115], v[84:87], v[30:33]
	v_mfma_f32_16x16x32_f16 v[34:37], v[108:111], v[88:91], v[34:37]
	v_mfma_f32_16x16x32_f16 v[38:41], v[112:115], v[88:91], v[38:41]
	v_mfma_f32_16x16x32_f16 v[42:45], v[108:111], v[96:99], v[42:45]
	v_mfma_f32_16x16x32_f16 v[46:49], v[112:115], v[96:99], v[46:49]
	s_waitcnt vmcnt(16)
	v_mfma_f32_16x16x32_f16 v[18:21], v[108:111], v[104:107], v[18:21]
	v_mfma_f32_16x16x32_f16 v[22:25], v[112:115], v[104:107], v[22:25]
	s_setprio 0
	v_lshl_add_u64 v[58:59], v[60:61], 0, s[42:43]
	v_lshl_add_u64 v[90:91], v[60:61], 0, s[44:45]
	global_load_dwordx4 v[82:85], v[58:59], off
	global_load_dwordx4 v[86:89], v[90:91], off
	v_add_co_u32_e32 v58, vcc, s52, v58
	v_lshl_add_u64 v[90:91], v[60:61], 0, s[40:41]
	s_nop 0
	v_addc_co_u32_e32 v59, vcc, 0, v59, vcc
	global_load_dwordx4 v[96:99], v[58:59], off
	global_load_dwordx4 v[104:107], v[90:91], off
	ds_read_b128 v[108:111], v173
	ds_read_b128 v[112:115], v173 offset:8448
	s_setprio 1
	s_waitcnt vmcnt(15) lgkmcnt(1)
	v_mfma_f32_16x16x32_f16 v[26:29], v[108:111], v[2:5], v[26:29]
	s_waitcnt lgkmcnt(0)
	v_mfma_f32_16x16x32_f16 v[2:5], v[112:115], v[2:5], v[30:33]
	s_waitcnt vmcnt(14)
	v_mfma_f32_16x16x32_f16 v[30:33], v[108:111], v[6:9], v[34:37]
	v_mfma_f32_16x16x32_f16 v[6:9], v[112:115], v[6:9], v[38:41]
	s_waitcnt vmcnt(13)
	v_mfma_f32_16x16x32_f16 v[34:37], v[108:111], v[10:13], v[42:45]
	v_mfma_f32_16x16x32_f16 v[10:13], v[112:115], v[10:13], v[46:49]
	s_waitcnt vmcnt(12)
	v_mfma_f32_16x16x32_f16 v[18:21], v[108:111], v[14:17], v[18:21]
	v_mfma_f32_16x16x32_f16 v[14:17], v[112:115], v[14:17], v[22:25]
	s_setprio 0
	v_lshl_add_u64 v[42:43], v[60:61], 0, s[8:9]
	v_add_co_u32_e32 v58, vcc, s52, v42
	v_lshl_add_u64 v[44:45], v[60:61], 0, s[38:39]
	s_nop 0
	v_addc_co_u32_e32 v59, vcc, 0, v43, vcc
	global_load_dwordx4 v[22:25], v[42:43], off
	global_load_dwordx4 v[38:41], v[44:45], off
	v_lshl_add_u64 v[60:61], v[60:61], 0, s[6:7]
	global_load_dwordx4 v[42:45], v[58:59], off
	global_load_dwordx4 v[46:49], v[60:61], off
	ds_read_b128 v[58:61], v174
	ds_read_b128 v[108:111], v174 offset:8448
	s_setprio 1
	s_waitcnt vmcnt(15) lgkmcnt(1)
	v_mfma_f32_16x16x32_f16 v[26:29], v[58:61], v[50:53], v[26:29]
	s_waitcnt lgkmcnt(0)
	v_mfma_f32_16x16x32_f16 v[2:5], v[108:111], v[50:53], v[2:5]
	s_waitcnt vmcnt(14)
	v_mfma_f32_16x16x32_f16 v[30:33], v[58:61], v[54:57], v[30:33]
	v_mfma_f32_16x16x32_f16 v[6:9], v[108:111], v[54:57], v[6:9]
	s_waitcnt vmcnt(13)
	v_mfma_f32_16x16x32_f16 v[34:37], v[58:61], v[76:79], v[34:37]
	v_mfma_f32_16x16x32_f16 v[10:13], v[108:111], v[76:79], v[10:13]
	s_waitcnt vmcnt(12)
	v_mfma_f32_16x16x32_f16 v[18:21], v[58:61], v[100:103], v[18:21]
	v_mfma_f32_16x16x32_f16 v[14:17], v[108:111], v[100:103], v[14:17]
	s_setprio 0
	ds_read_b128 v[50:53], v175
	ds_read_b128 v[54:57], v175 offset:8448
	s_setprio 1
	s_waitcnt vmcnt(11) lgkmcnt(1)
	v_mfma_f32_16x16x32_f16 v[26:29], v[50:53], v[62:65], v[26:29]
	s_waitcnt lgkmcnt(0)
	v_mfma_f32_16x16x32_f16 v[2:5], v[54:57], v[62:65], v[2:5]
	s_waitcnt vmcnt(10)
	v_mfma_f32_16x16x32_f16 v[30:33], v[50:53], v[68:71], v[30:33]
	v_mfma_f32_16x16x32_f16 v[6:9], v[54:57], v[68:71], v[6:9]
	s_waitcnt vmcnt(9)
	v_mfma_f32_16x16x32_f16 v[34:37], v[50:53], v[72:75], v[34:37]
	v_mfma_f32_16x16x32_f16 v[10:13], v[54:57], v[72:75], v[10:13]
	s_waitcnt vmcnt(8)
	v_mfma_f32_16x16x32_f16 v[18:21], v[50:53], v[92:95], v[18:21]
	v_mfma_f32_16x16x32_f16 v[14:17], v[54:57], v[92:95], v[14:17]
	s_setprio 0
	ds_read_b128 v[50:53], v176
	ds_read_b128 v[54:57], v176 offset:8448
	s_setprio 1
	s_waitcnt vmcnt(7) lgkmcnt(1)
	v_mfma_f32_16x16x32_f16 v[26:29], v[50:53], v[82:85], v[26:29]
	s_waitcnt lgkmcnt(0)
	v_mfma_f32_16x16x32_f16 v[2:5], v[54:57], v[82:85], v[2:5]
	s_waitcnt vmcnt(6)
	v_mfma_f32_16x16x32_f16 v[30:33], v[50:53], v[86:89], v[30:33]
	v_mfma_f32_16x16x32_f16 v[6:9], v[54:57], v[86:89], v[6:9]
	s_waitcnt vmcnt(5)
	v_mfma_f32_16x16x32_f16 v[34:37], v[50:53], v[96:99], v[34:37]
	v_mfma_f32_16x16x32_f16 v[58:61], v[54:57], v[96:99], v[10:13]
	s_waitcnt vmcnt(4)
	v_mfma_f32_16x16x32_f16 v[18:21], v[50:53], v[104:107], v[18:21]
	v_mfma_f32_16x16x32_f16 v[50:53], v[54:57], v[104:107], v[14:17]
	s_setprio 0
	ds_read_b128 v[54:57], v177
	ds_read_b128 v[62:65], v177 offset:8448
	s_setprio 1
	s_waitcnt vmcnt(3) lgkmcnt(1)
	v_mfma_f32_16x16x32_f16 v[26:29], v[54:57], v[22:25], v[26:29]
	s_waitcnt lgkmcnt(0)
	v_mfma_f32_16x16x32_f16 v[14:17], v[62:65], v[22:25], v[2:5]
	s_waitcnt vmcnt(2)
	v_mfma_f32_16x16x32_f16 v[22:25], v[54:57], v[38:41], v[30:33]
	v_mfma_f32_16x16x32_f16 v[10:13], v[62:65], v[38:41], v[6:9]
	s_waitcnt vmcnt(1)
	v_mfma_f32_16x16x32_f16 v[30:33], v[54:57], v[42:45], v[34:37]
	v_mfma_f32_16x16x32_f16 v[6:9], v[62:65], v[42:45], v[58:61]
	s_waitcnt vmcnt(0)
	v_mfma_f32_16x16x32_f16 v[34:37], v[54:57], v[46:49], v[18:21]
	v_mfma_f32_16x16x32_f16 v[2:5], v[62:65], v[46:49], v[50:53]
	s_setprio 0
	s_nop 1
	v_mul_u32_u24_e32 v52, 0x50, v0
	ds_read_b128 v[18:21], v52
	s_lshl_b64 s[2:3], s[2:3], 15
	v_or_b32_e32 v0, s2, v66
	v_mov_b32_e32 v1, s3
	v_lshl_add_u64 v[50:51], s[24:25], 0, v[0:1]
	ds_read_b128 v[38:41], v52 offset:16
	ds_read_b128 v[42:45], v52 offset:32
	ds_read_b128 v[46:49], v52 offset:48
	s_waitcnt lgkmcnt(3)
	global_store_dwordx4 v[50:51], v[18:21], off sc0 sc1
	s_nop 1
	v_add_co_u32_e32 v18, vcc, s29, v50
	s_nop 1
	v_addc_co_u32_e32 v19, vcc, 0, v51, vcc
	s_waitcnt lgkmcnt(2)
	global_store_dwordx4 v[18:19], v[38:41], off sc0 sc1
	v_or_b32_e32 v18, 0x4000, v0
	v_mov_b32_e32 v19, s3
	v_lshl_add_u64 v[20:21], s[24:25], 0, v[18:19]
	s_waitcnt lgkmcnt(1)
	global_store_dwordx4 v[20:21], v[42:45], off sc0 sc1
	v_add_co_u32_e32 v20, vcc, s33, v50
	v_or_b32_e32 v39, 0x200, v81
	s_nop 0
	v_addc_co_u32_e32 v21, vcc, 0, v51, vcc
	s_waitcnt lgkmcnt(0)
	global_store_dwordx4 v[20:21], v[46:49], off sc0 sc1
	v_lshl_add_u64 v[0:1], s[0:1], 0, v[0:1]
	v_mov_b32_e32 v180, 0xbfb8aa3b
	v_mov_b32_e32 v181, 0xbfb8aa3b
	v_mov_b32_e32 v182, 1.0
	v_mov_b32_e32 v183, 1.0
	v_or_b32_e32 v184, v39, v67
	v_mad_u32_u24 v184, v184, s4, v80
	v_or_b32_e32 v185, v116, v39
	v_mad_u32_u24 v185, v185, s4, v80
	v_or_b32_e32 v186, v117, v39
	v_mad_u32_u24 v186, v186, s4, v80
	v_or_b32_e32 v187, v118, v39
	v_mad_u32_u24 v187, v187, s4, v80
	v_pk_mul_f32 v[188:189], v[26:27], v[180:181]
	v_pk_mul_f32 v[190:191], v[28:29], v[180:181]
	v_pk_mul_f32 v[196:197], v[22:23], v[180:181]
	v_pk_mul_f32 v[198:199], v[24:25], v[180:181]
	v_pk_mul_f32 v[204:205], v[30:31], v[180:181]
	v_pk_mul_f32 v[206:207], v[32:33], v[180:181]
	v_pk_mul_f32 v[212:213], v[34:35], v[180:181]
	v_pk_mul_f32 v[214:215], v[36:37], v[180:181]
	v_pk_mul_f32 v[220:221], v[14:15], v[180:181]
	v_pk_mul_f32 v[222:223], v[16:17], v[180:181]
	v_pk_mul_f32 v[228:229], v[10:11], v[180:181]
	v_pk_mul_f32 v[230:231], v[12:13], v[180:181]
	v_pk_mul_f32 v[236:237], v[6:7], v[180:181]
	v_pk_mul_f32 v[238:239], v[8:9], v[180:181]
	v_pk_mul_f32 v[244:245], v[2:3], v[180:181]
	v_pk_mul_f32 v[246:247], v[4:5], v[180:181]
	v_exp_f32_e32 v188, v188
	v_exp_f32_e32 v189, v189
	v_exp_f32_e32 v190, v190
	v_exp_f32_e32 v191, v191
	v_exp_f32_e32 v196, v196
	v_exp_f32_e32 v197, v197
	v_exp_f32_e32 v198, v198
	v_exp_f32_e32 v199, v199
	v_exp_f32_e32 v204, v204
	v_exp_f32_e32 v205, v205
	v_exp_f32_e32 v206, v206
	v_exp_f32_e32 v207, v207
	v_exp_f32_e32 v212, v212
	v_exp_f32_e32 v213, v213
	v_exp_f32_e32 v214, v214
	v_exp_f32_e32 v215, v215
	v_exp_f32_e32 v220, v220
	v_exp_f32_e32 v221, v221
	v_exp_f32_e32 v222, v222
	v_exp_f32_e32 v223, v223
	v_exp_f32_e32 v228, v228
	v_exp_f32_e32 v229, v229
	v_exp_f32_e32 v230, v230
	v_exp_f32_e32 v231, v231
	v_exp_f32_e32 v236, v236
	v_exp_f32_e32 v237, v237
	v_exp_f32_e32 v238, v238
	v_exp_f32_e32 v239, v239
	v_exp_f32_e32 v244, v244
	v_exp_f32_e32 v245, v245
	v_exp_f32_e32 v246, v246
	v_exp_f32_e32 v247, v247
	v_pk_add_f32 v[188:189], v[188:189], v[182:183]
	v_pk_add_f32 v[190:191], v[190:191], v[182:183]
	v_pk_add_f32 v[196:197], v[196:197], v[182:183]
	v_pk_add_f32 v[198:199], v[198:199], v[182:183]
	v_pk_add_f32 v[204:205], v[204:205], v[182:183]
	v_pk_add_f32 v[206:207], v[206:207], v[182:183]
	v_pk_add_f32 v[212:213], v[212:213], v[182:183]
	v_pk_add_f32 v[214:215], v[214:215], v[182:183]
	v_pk_add_f32 v[220:221], v[220:221], v[182:183]
	v_pk_add_f32 v[222:223], v[222:223], v[182:183]
	v_pk_add_f32 v[228:229], v[228:229], v[182:183]
	v_pk_add_f32 v[230:231], v[230:231], v[182:183]
	v_pk_add_f32 v[236:237], v[236:237], v[182:183]
	v_pk_add_f32 v[238:239], v[238:239], v[182:183]
	v_pk_add_f32 v[244:245], v[244:245], v[182:183]
	v_pk_add_f32 v[246:247], v[246:247], v[182:183]
	v_rcp_f32_e32 v188, v188
	v_rcp_f32_e32 v189, v189
	v_rcp_f32_e32 v190, v190
	v_rcp_f32_e32 v191, v191
	v_rcp_f32_e32 v196, v196
	v_rcp_f32_e32 v197, v197
	v_rcp_f32_e32 v198, v198
	v_rcp_f32_e32 v199, v199
	v_rcp_f32_e32 v204, v204
	v_rcp_f32_e32 v205, v205
	v_rcp_f32_e32 v206, v206
	v_rcp_f32_e32 v207, v207
	v_rcp_f32_e32 v212, v212
	v_rcp_f32_e32 v213, v213
	v_rcp_f32_e32 v214, v214
	v_rcp_f32_e32 v215, v215
	v_rcp_f32_e32 v220, v220
	v_rcp_f32_e32 v221, v221
	v_rcp_f32_e32 v222, v222
	v_rcp_f32_e32 v223, v223
	v_rcp_f32_e32 v228, v228
	v_rcp_f32_e32 v229, v229
	v_rcp_f32_e32 v230, v230
	v_rcp_f32_e32 v231, v231
	v_rcp_f32_e32 v236, v236
	v_rcp_f32_e32 v237, v237
	v_rcp_f32_e32 v238, v238
	v_rcp_f32_e32 v239, v239
	v_rcp_f32_e32 v244, v244
	v_rcp_f32_e32 v245, v245
	v_rcp_f32_e32 v246, v246
	v_rcp_f32_e32 v247, v247
	v_fma_mixlo_f16 v192, v26, v188, 0
	v_mul_f32_e32 v189, v27, v189
	v_mul_f32_e32 v190, v28, v190
	v_fma_mixlo_f16 v193, v29, v191, 0
	v_fma_mixlo_f16 v200, v22, v196, 0
	v_mul_f32_e32 v197, v23, v197
	v_mul_f32_e32 v198, v24, v198
	v_fma_mixlo_f16 v201, v25, v199, 0
	v_fma_mixlo_f16 v208, v30, v204, 0
	v_mul_f32_e32 v205, v31, v205
	v_mul_f32_e32 v206, v32, v206
	v_fma_mixlo_f16 v209, v33, v207, 0
	v_fma_mixlo_f16 v216, v34, v212, 0
	v_mul_f32_e32 v213, v35, v213
	v_mul_f32_e32 v214, v36, v214
	v_fma_mixlo_f16 v217, v37, v215, 0
	v_fma_mixlo_f16 v224, v14, v220, 0
	v_mul_f32_e32 v221, v15, v221
	v_mul_f32_e32 v222, v16, v222
	v_fma_mixlo_f16 v225, v17, v223, 0
	v_fma_mixlo_f16 v232, v10, v228, 0
	v_mul_f32_e32 v229, v11, v229
	v_mul_f32_e32 v230, v12, v230
	v_fma_mixlo_f16 v233, v13, v231, 0
	v_fma_mixlo_f16 v240, v6, v236, 0
	v_mul_f32_e32 v237, v7, v237
	v_mul_f32_e32 v238, v8, v238
	v_fma_mixlo_f16 v241, v9, v239, 0
	v_fma_mixlo_f16 v248, v2, v244, 0
	v_mul_f32_e32 v245, v3, v245
	v_mul_f32_e32 v246, v4, v246
	v_fma_mixlo_f16 v249, v5, v247, 0
	v_cvt_pk_f16_f32 v188, v189, v190
	v_cvt_pk_f16_f32 v196, v197, v198
	v_cvt_pk_f16_f32 v204, v205, v206
	v_cvt_pk_f16_f32 v212, v213, v214
	v_cvt_pk_f16_f32 v220, v221, v222
	v_cvt_pk_f16_f32 v228, v229, v230
	v_cvt_pk_f16_f32 v236, v237, v238
	v_cvt_pk_f16_f32 v244, v245, v246
	v_pack_b32_f16 v194, v192, v188
	v_alignbit_b32 v195, v193, v188, 16
	v_pack_b32_f16 v202, v200, v196
	v_alignbit_b32 v203, v201, v196, 16
	v_pack_b32_f16 v210, v208, v204
	v_alignbit_b32 v211, v209, v204, 16
	v_pack_b32_f16 v218, v216, v212
	v_alignbit_b32 v219, v217, v212, 16
	v_pack_b32_f16 v226, v224, v220
	v_alignbit_b32 v227, v225, v220, 16
	v_pack_b32_f16 v234, v232, v228
	v_alignbit_b32 v235, v233, v228, 16
	v_pack_b32_f16 v242, v240, v236
	v_alignbit_b32 v243, v241, v236, 16
	v_pack_b32_f16 v250, v248, v244
	v_alignbit_b32 v251, v249, v244, 16
	ds_write_b64 v184, v[194:195]
	ds_write_b64 v185, v[202:203]
	ds_write_b64 v186, v[210:211]
	ds_write_b64 v187, v[218:219]
	ds_write_b64 v184, v[226:227] offset:32
	ds_write_b64 v185, v[234:235] offset:32
	ds_write_b64 v186, v[242:243] offset:32
	ds_write_b64 v187, v[250:251] offset:32
	s_waitcnt lgkmcnt(0)
	s_barrier
	ds_read_b128 v[2:5], v52 offset:40960
	ds_read_b128 v[6:9], v52 offset:40976
	ds_read_b128 v[10:13], v52 offset:40992
	ds_read_b128 v[14:17], v52 offset:41008
	s_waitcnt lgkmcnt(3)
	global_store_dwordx4 v[0:1], v[2:5], off sc0 sc1
	s_nop 1
	v_add_co_u32_e32 v2, vcc, 0x2000, v0
	s_nop 1
	v_addc_co_u32_e32 v3, vcc, 0, v1, vcc
	v_add_co_u32_e32 v0, vcc, 0x6000, v0
	s_waitcnt lgkmcnt(2)
	global_store_dwordx4 v[2:3], v[6:9], off sc0 sc1
	v_lshl_add_u64 v[2:3], s[0:1], 0, v[18:19]
	v_addc_co_u32_e32 v1, vcc, 0, v1, vcc
	s_waitcnt lgkmcnt(1)
	global_store_dwordx4 v[2:3], v[10:13], off sc0 sc1
	s_waitcnt lgkmcnt(0)
	global_store_dwordx4 v[0:1], v[14:17], off sc0 sc1
	s_endpgm
	.p2align	8
